# PEER token loop: 64-bit encodings moved onto 8-byte boundaries by promoting 128 preceding 32-bit VALU encodings to their e64 form (no instruction added or reordered)
# speedup vs baseline: 1.0138x; 1.0049x over previous
.LBB0_719:
	s_lshl_b32 s6, s33, 3
	s_add_i32 s6, s6, s88
	v_mov_b32_e32 v247, s6
	s_ashr_i32 s89, s88, 31
	s_lshl_b64 s[74:75], s[88:89], 11
	s_lshl_b64 s[8:9], s[88:89], 2
	v_lshl_add_u64 v[24:25], v[128:129], 0, s[74:75]
	s_add_u32 s8, s37, s8
	global_load_dwordx4 v[20:23], v[24:25], off offset:1024
	s_addc_u32 s9, s73, s9
	global_load_dwordx4 v[24:27], v[24:25], off
	s_nop 0
	global_load_dword v248, v3, s[8:9]
	s_waitcnt vmcnt(6)
	v_lshlrev_b32_e32 v28, 16, v4
	v_cmp_lt_i32_e32 vcc, -1, v28
	v_lshlrev_b32_e32 v30, 16, v5
	v_lshlrev_b32_e32 v32, 16, v6
	v_cndmask_b32_e32 v29, v217, v218, vcc
	v_cmp_lt_i32_e32 vcc, -1, v4
	v_xor_b32_e32 v28, v29, v28
	v_lshlrev_b32_e32 v34, 16, v7
	v_cndmask_b32_e32 v29, v217, v218, vcc
	v_cmp_lt_i32_e32 vcc, -1, v30
	s_waitcnt vmcnt(3)
	v_lshlrev_b32_e32 v36, 16, v16
	v_lshlrev_b32_e32 v38, 16, v17
	v_cndmask_b32_e32 v31, v217, v218, vcc
	v_cmp_lt_i32_e32 vcc, -1, v5
	v_xor_b32_e32 v30, v31, v30
	v_lshlrev_b32_e32 v40, 16, v18
	v_cndmask_b32_e32 v31, v217, v218, vcc
	v_cmp_lt_i32_e32 vcc, -1, v32
	v_lshlrev_b32_e32 v42, 16, v19
	v_lshlrev_b32_e32 v44, 16, v12
	v_cndmask_b32_e32 v33, v217, v218, vcc
	v_cmp_lt_i32_e32 vcc, -1, v6
	v_xor_b32_e32 v32, v33, v32
	v_lshlrev_b32_e32 v46, 16, v13
	v_cndmask_b32_e32 v33, v217, v218, vcc
	v_cmp_lt_i32_e32 vcc, -1, v34
	v_lshlrev_b32_e32 v48, 16, v14
	v_lshlrev_b32_e32 v50, 16, v15
	v_cndmask_b32_e32 v35, v217, v218, vcc
	v_cmp_lt_i32_e32 vcc, -1, v7
	v_xor_b32_e32 v34, v35, v34
	v_lshlrev_b32_e32 v52, 16, v8
	v_cndmask_b32_e32 v35, v217, v218, vcc
	v_cmp_lt_i32_e32 vcc, -1, v36
	v_lshlrev_b32_e32 v54, 16, v9
	v_lshlrev_b32_e32 v56, 16, v10
	v_cndmask_b32_e32 v37, v217, v218, vcc
	v_cmp_lt_i32_e32 vcc, -1, v16
	v_xor_b32_e32 v36, v37, v36
	v_lshlrev_b32_e32 v58, 16, v11
	v_cndmask_b32_e32 v37, v217, v218, vcc
	v_cmp_lt_i32_e32 vcc, -1, v38
	v_bitop3_b32 v29, v29, v4, s90 bitop3:0x78
	v_bitop3_b32 v31, v31, v5, s90 bitop3:0x78
	v_cndmask_b32_e32 v39, v217, v218, vcc
	v_cmp_lt_i32_e32 vcc, -1, v17
	v_xor_b32_e64 v38, v39, v38
	v_bitop3_b32 v33, v33, v6, s90 bitop3:0x78
	v_cndmask_b32_e32 v39, v217, v218, vcc
	v_cmp_lt_i32_e32 vcc, -1, v40
	v_bitop3_b32 v35, v35, v7, s90 bitop3:0x78
	v_bitop3_b32 v37, v37, v16, s90 bitop3:0x78
	v_cndmask_b32_e32 v41, v217, v218, vcc
	v_cmp_lt_i32_e32 vcc, -1, v18
	v_xor_b32_e64 v40, v41, v40
	v_bitop3_b32 v39, v39, v17, s90 bitop3:0x78
	v_cndmask_b32_e32 v41, v217, v218, vcc
	v_cmp_lt_i32_e32 vcc, -1, v42
	v_bitop3_b32 v41, v41, v18, s90 bitop3:0x78
	v_sub_u32_e32 v28, v28, v201
	v_cndmask_b32_e32 v43, v217, v218, vcc
	v_cmp_lt_i32_e32 vcc, -1, v19
	v_xor_b32_e32 v42, v43, v42
	v_sub_u32_e64 v29, v29, v201
	v_cndmask_b32_e32 v43, v217, v218, vcc
	v_cmp_lt_i32_e32 vcc, -1, v44
	v_bitop3_b32 v43, v43, v19, s90 bitop3:0x78
	v_sub_u32_e32 v30, v30, v202
	v_cndmask_b32_e32 v45, v217, v218, vcc
	v_cmp_lt_i32_e32 vcc, -1, v12
	v_xor_b32_e32 v44, v45, v44
	v_sub_u32_e64 v31, v31, v202
	v_cndmask_b32_e32 v45, v217, v218, vcc
	v_cmp_lt_i32_e32 vcc, -1, v46
	v_bitop3_b32 v45, v45, v12, s90 bitop3:0x78
	v_sub_u32_e32 v32, v32, v203
	v_cndmask_b32_e32 v47, v217, v218, vcc
	v_cmp_lt_i32_e32 vcc, -1, v13
	v_xor_b32_e32 v46, v47, v46
	v_sub_u32_e64 v33, v33, v203
	v_cndmask_b32_e32 v47, v217, v218, vcc
	v_cmp_lt_i32_e32 vcc, -1, v48
	v_bitop3_b32 v47, v47, v13, s90 bitop3:0x78
	v_sub_u32_e32 v34, v34, v204
	v_cndmask_b32_e32 v49, v217, v218, vcc
	v_cmp_lt_i32_e32 vcc, -1, v14
	v_xor_b32_e32 v48, v49, v48
	v_sub_u32_e64 v35, v35, v204
	v_cndmask_b32_e32 v49, v217, v218, vcc
	v_cmp_lt_i32_e32 vcc, -1, v50
	v_bitop3_b32 v49, v49, v14, s90 bitop3:0x78
	v_sub_u32_e32 v36, v36, v205
	v_cndmask_b32_e32 v51, v217, v218, vcc
	v_cmp_lt_i32_e32 vcc, -1, v15
	v_xor_b32_e32 v50, v51, v50
	v_sub_u32_e64 v37, v37, v205
	v_cndmask_b32_e32 v51, v217, v218, vcc
	v_cmp_lt_i32_e32 vcc, -1, v52
	v_bitop3_b32 v51, v51, v15, s90 bitop3:0x78
	v_sub_u32_e32 v38, v38, v220
	v_cndmask_b32_e32 v53, v217, v218, vcc
	v_cmp_lt_i32_e32 vcc, -1, v8
	v_xor_b32_e32 v52, v53, v52
	v_sub_u32_e64 v39, v39, v220
	v_cndmask_b32_e32 v53, v217, v218, vcc
	v_cmp_lt_i32_e32 vcc, -1, v54
	v_bitop3_b32 v53, v53, v8, s90 bitop3:0x78
	v_sub_u32_e32 v40, v40, v221
	v_cndmask_b32_e32 v55, v217, v218, vcc
	v_cmp_lt_i32_e32 vcc, -1, v9
	v_xor_b32_e32 v54, v55, v54
	v_sub_u32_e64 v41, v41, v221
	v_cndmask_b32_e32 v55, v217, v218, vcc
	v_cmp_lt_i32_e32 vcc, -1, v56
	v_bitop3_b32 v55, v55, v9, s90 bitop3:0x78
	v_sub_u32_e32 v42, v42, v222
	v_cndmask_b32_e32 v57, v217, v218, vcc
	v_cmp_lt_i32_e32 vcc, -1, v10
	v_xor_b32_e32 v56, v57, v56
	v_sub_u32_e64 v43, v43, v222
	v_cndmask_b32_e32 v57, v217, v218, vcc
	v_cmp_lt_i32_e32 vcc, -1, v58
	v_bitop3_b32 v57, v57, v10, s90 bitop3:0x78
	v_sub_u32_e32 v44, v44, v223
	v_cndmask_b32_e32 v59, v217, v218, vcc
	v_cmp_lt_i32_e32 vcc, -1, v11
	v_xor_b32_e32 v58, v59, v58
	v_sub_u32_e32 v45, v45, v223
	v_cndmask_b32_e32 v59, v217, v218, vcc
	v_bitop3_b32 v59, v59, v11, s90 bitop3:0x78
	v_sub_u32_e32 v46, v46, v224
	v_sub_u32_e32 v47, v47, v224
	v_sub_u32_e32 v48, v48, v225
	v_sub_u32_e32 v49, v49, v225
	v_sub_u32_e32 v50, v50, v226
	v_sub_u32_e32 v51, v51, v226
	v_sub_u32_e32 v52, v52, v227
	v_sub_u32_e32 v53, v53, v227
	v_sub_u32_e32 v54, v54, v228
	v_sub_u32_e32 v55, v55, v228
	v_sub_u32_e32 v56, v56, v229
	v_sub_u32_e32 v57, v57, v229
	v_sub_u32_e32 v58, v58, v230
	v_sub_u32_e32 v59, v59, v230
	v_add_u32_e32 v28, 0x7f, v28
	v_add_u32_e32 v29, 0x7e, v29
	v_add_u32_e32 v30, 0x7f, v30
	v_add_u32_e32 v31, 0x7e, v31
	v_add_u32_e32 v32, 0x7f, v32
	v_add_u32_e32 v33, 0x7e, v33
	v_add_u32_e32 v34, 0x7f, v34
	v_add_u32_e32 v35, 0x7e, v35
	v_add_u32_e32 v36, 0x7f, v36
	v_add_u32_e32 v37, 0x7e, v37
	v_add_u32_e32 v38, 0x7f, v38
	v_add_u32_e32 v39, 0x7e, v39
	v_add_u32_e32 v40, 0x7f, v40
	v_add_u32_e32 v41, 0x7e, v41
	v_add_u32_e32 v42, 0x7f, v42
	v_add_u32_e32 v43, 0x7e, v43
	v_add_u32_e32 v44, 0x7f, v44
	v_add_u32_e32 v45, 0x7e, v45
	v_add_u32_e32 v46, 0x7f, v46
	v_add_u32_e32 v47, 0x7e, v47
	v_add_u32_e32 v48, 0x7f, v48
	v_add_u32_e32 v49, 0x7e, v49
	v_add_u32_e32 v50, 0x7f, v50
	v_add_u32_e32 v51, 0x7e, v51
	v_add_u32_e32 v52, 0x7f, v52
	v_add_u32_e32 v53, 0x7e, v53
	v_add_u32_e32 v54, 0x7f, v54
	v_add_u32_e32 v55, 0x7e, v55
	v_add_u32_e32 v56, 0x7f, v56
	v_add_u32_e32 v57, 0x7e, v57
	v_add_u32_e32 v58, 0x7f, v58
	v_add_u32_e32 v59, 0x7e, v59
	v_max_u32_e32 v60, v28, v29
	v_min_u32_e32 v28, v28, v29
	v_max_u32_e32 v29, v30, v31
	v_min_u32_e32 v30, v30, v31
	v_max_u32_e32 v31, v32, v33
	v_min_u32_e32 v32, v32, v33
	v_max_u32_e32 v33, v34, v35
	v_min_u32_e32 v34, v34, v35
	v_max_u32_e32 v35, v36, v37
	v_min_u32_e32 v36, v36, v37
	v_max_u32_e32 v37, v38, v39
	v_min_u32_e32 v38, v38, v39
	v_max_u32_e32 v39, v40, v41
	v_min_u32_e32 v40, v40, v41
	v_max_u32_e32 v41, v42, v43
	v_min_u32_e32 v42, v42, v43
	v_max_u32_e32 v43, v44, v45
	v_min_u32_e32 v44, v44, v45
	v_max_u32_e32 v45, v46, v47
	v_min_u32_e32 v46, v46, v47
	v_max_u32_e32 v47, v48, v49
	v_min_u32_e32 v48, v48, v49
	v_max_u32_e32 v49, v50, v51
	v_min_u32_e32 v50, v50, v51
	v_max_u32_e32 v51, v52, v53
	v_min_u32_e32 v52, v52, v53
	v_max_u32_e32 v53, v54, v55
	v_min_u32_e32 v54, v54, v55
	v_max_u32_e32 v55, v56, v57
	v_min_u32_e32 v56, v56, v57
	v_max_u32_e32 v57, v58, v59
	v_min_u32_e32 v58, v58, v59
	v_max_u32_e32 v59, v60, v30
	v_min_u32_e32 v30, v60, v30
	v_max_u32_e32 v60, v28, v29
	v_min_u32_e32 v28, v28, v29
	v_max_u32_e32 v29, v31, v34
	v_min_u32_e32 v31, v31, v34
	v_max_u32_e32 v34, v32, v33
	v_min_u32_e32 v32, v32, v33
	v_max_u32_e32 v33, v35, v38
	v_min_u32_e32 v35, v35, v38
	v_max_u32_e32 v38, v36, v37
	v_min_u32_e32 v36, v36, v37
	v_max_u32_e32 v37, v39, v42
	v_min_u32_e32 v39, v39, v42
	v_max_u32_e32 v42, v40, v41
	v_min_u32_e32 v40, v40, v41
	v_max_u32_e32 v41, v43, v46
	v_min_u32_e32 v43, v43, v46
	v_max_u32_e32 v46, v44, v45
	v_min_u32_e32 v44, v44, v45
	v_max_u32_e32 v45, v47, v50
	v_min_u32_e32 v47, v47, v50
	v_max_u32_e32 v50, v48, v49
	v_min_u32_e32 v48, v48, v49
	v_max_u32_e32 v49, v51, v54
	v_min_u32_e32 v51, v51, v54
	v_max_u32_e32 v54, v52, v53
	v_min_u32_e32 v52, v52, v53
	v_max_u32_e32 v53, v55, v58
	v_min_u32_e32 v55, v55, v58
	v_max_u32_e32 v58, v56, v57
	v_min_u32_e32 v56, v56, v57
	v_max_u32_e32 v57, v59, v60
	v_min_u32_e32 v59, v59, v60
	v_max_u32_e32 v60, v30, v28
	v_min_u32_e32 v28, v30, v28
	v_max_u32_e32 v30, v31, v32
	v_min_u32_e32 v31, v31, v32
	v_max_u32_e32 v32, v29, v34
	v_min_u32_e32 v29, v29, v34
	v_max_u32_e32 v34, v33, v38
	v_min_u32_e32 v33, v33, v38
	v_max_u32_e32 v38, v35, v36
	v_min_u32_e32 v35, v35, v36
	v_max_u32_e32 v36, v39, v40
	v_min_u32_e32 v39, v39, v40
	v_max_u32_e32 v40, v37, v42
	v_min_u32_e32 v37, v37, v42
	v_max_u32_e32 v42, v41, v46
	v_min_u32_e32 v41, v41, v46
	v_max_u32_e32 v46, v43, v44
	v_min_u32_e32 v43, v43, v44
	v_max_u32_e32 v44, v47, v48
	v_min_u32_e32 v47, v47, v48
	v_max_u32_e32 v48, v45, v50
	v_min_u32_e32 v45, v45, v50
	v_max_u32_e32 v50, v49, v54
	v_min_u32_e32 v49, v49, v54
	v_max_u32_e32 v54, v51, v52
	v_min_u32_e32 v51, v51, v52
	v_max_u32_e32 v52, v55, v56
	v_min_u32_e32 v55, v55, v56
	v_max_u32_e32 v56, v53, v58
	v_min_u32_e32 v53, v53, v58
	v_max_u32_e32 v58, v57, v31
	v_min_u32_e32 v31, v57, v31
	v_max_u32_e32 v57, v59, v30
	v_min_u32_e32 v30, v59, v30
	v_max_u32_e32 v59, v60, v29
	v_min_u32_e32 v29, v60, v29
	v_max_u32_e32 v60, v28, v32
	v_min_u32_e32 v28, v28, v32
	v_max_u32_e32 v32, v34, v39
	v_min_u32_e32 v34, v34, v39
	v_max_u32_e32 v39, v33, v36
	v_min_u32_e32 v33, v33, v36
	v_max_u32_e32 v36, v38, v37
	v_min_u32_e32 v37, v38, v37
	v_max_u32_e32 v38, v35, v40
	v_min_u32_e32 v35, v35, v40
	v_max_u32_e32 v40, v42, v47
	v_min_u32_e32 v42, v42, v47
	v_max_u32_e32 v47, v41, v44
	v_min_u32_e32 v41, v41, v44
	v_max_u32_e32 v44, v46, v45
	v_min_u32_e32 v45, v46, v45
	v_max_u32_e32 v46, v43, v48
	v_min_u32_e32 v43, v43, v48
	v_max_u32_e32 v48, v50, v55
	v_min_u32_e32 v50, v50, v55
	v_max_u32_e32 v55, v49, v52
	v_min_u32_e32 v49, v49, v52
	v_max_u32_e32 v52, v54, v53
	v_min_u32_e32 v53, v54, v53
	v_max_u32_e32 v54, v51, v56
	v_min_u32_e32 v51, v51, v56
	v_max_u32_e32 v56, v58, v59
	v_min_u32_e32 v58, v58, v59
	v_max_u32_e32 v59, v57, v60
	v_min_u32_e32 v57, v57, v60
	v_max_u32_e32 v60, v31, v29
	v_min_u32_e32 v29, v31, v29
	v_max_u32_e32 v31, v30, v28
	v_min_u32_e32 v28, v30, v28
	v_max_u32_e32 v30, v34, v37
	v_min_u32_e32 v34, v34, v37
	v_max_u32_e32 v37, v33, v35
	v_min_u32_e32 v33, v33, v35
	v_max_u32_e32 v35, v32, v36
	v_min_u32_e32 v32, v32, v36
	v_max_u32_e32 v36, v39, v38
	v_min_u32_e32 v38, v39, v38
	v_max_u32_e32 v39, v40, v44
	v_min_u32_e32 v40, v40, v44
	v_max_u32_e32 v44, v47, v46
	v_min_u32_e32 v46, v47, v46
	v_max_u32_e32 v47, v42, v45
	v_min_u32_e32 v42, v42, v45
	v_max_u32_e32 v45, v41, v43
	v_min_u32_e32 v41, v41, v43
	v_max_u32_e32 v43, v50, v53
	v_min_u32_e32 v50, v50, v53
	v_max_u32_e32 v53, v49, v51
	v_min_u32_e32 v49, v49, v51
	v_max_u32_e32 v51, v48, v52
	v_min_u32_e32 v48, v48, v52
	v_max_u32_e32 v52, v55, v54
	v_min_u32_e32 v54, v55, v54
	v_max_u32_e32 v55, v56, v59
	v_min_u32_e32 v56, v56, v59
	v_max_u32_e32 v59, v58, v57
	v_min_u32_e32 v57, v58, v57
	v_max_u32_e32 v58, v60, v31
	v_min_u32_e32 v31, v60, v31
	v_max_u32_e32 v60, v29, v28
	v_min_u32_e32 v28, v29, v28
	v_max_u32_e32 v29, v34, v33
	v_min_u32_e32 v33, v34, v33
	v_max_u32_e32 v34, v30, v37
	v_min_u32_e32 v30, v30, v37
	v_max_u32_e32 v37, v32, v38
	v_min_u32_e32 v32, v32, v38
	v_max_u32_e32 v38, v35, v36
	v_min_u32_e32 v35, v35, v36
	v_max_u32_e32 v36, v39, v44
	v_min_u32_e32 v39, v39, v44
	v_max_u32_e32 v44, v40, v46
	v_min_u32_e32 v40, v40, v46
	v_max_u32_e32 v46, v47, v45
	v_min_u32_e32 v45, v47, v45
	v_max_u32_e32 v47, v42, v41
	v_min_u32_e32 v41, v42, v41
	v_max_u32_e32 v42, v50, v49
	v_min_u32_e32 v49, v50, v49
	v_max_u32_e32 v50, v43, v53
	v_min_u32_e32 v43, v43, v53
	v_max_u32_e32 v53, v48, v54
	v_min_u32_e32 v48, v48, v54
	v_max_u32_e32 v54, v51, v52
	v_min_u32_e32 v51, v51, v52
	v_max_u32_e32 v52, v55, v33
	v_min_u32_e32 v33, v55, v33
	v_max_u32_e32 v55, v56, v29
	v_min_u32_e32 v29, v56, v29
	v_max_u32_e32 v56, v59, v30
	v_min_u32_e32 v30, v59, v30
	v_max_u32_e32 v59, v57, v34
	v_min_u32_e32 v34, v57, v34
	v_max_u32_e32 v57, v58, v32
	v_min_u32_e32 v32, v58, v32
	v_max_u32_e32 v58, v31, v37
	v_min_u32_e32 v31, v31, v37
	v_max_u32_e32 v37, v60, v35
	v_min_u32_e32 v35, v60, v35
	v_max_u32_e32 v60, v28, v38
	v_min_u32_e32 v28, v28, v38
	v_max_u32_e32 v38, v36, v49
	v_min_u32_e32 v36, v36, v49
	v_max_u32_e32 v49, v39, v42
	v_min_u32_e32 v39, v39, v42
	v_max_u32_e32 v42, v44, v43
	v_min_u32_e32 v43, v44, v43
	v_max_u32_e32 v44, v40, v50
	v_min_u32_e32 v40, v40, v50
	v_max_u32_e32 v50, v46, v48
	v_min_u32_e32 v46, v46, v48
	v_max_u32_e32 v48, v45, v53
	v_min_u32_e32 v45, v45, v53
	v_max_u32_e32 v53, v47, v51
	v_min_u32_e32 v47, v47, v51
	v_max_u32_e32 v51, v41, v54
	v_min_u32_e32 v41, v41, v54
	v_max_u32_e32 v54, v52, v57
	v_min_u32_e32 v52, v52, v57
	v_max_u32_e32 v57, v55, v58
	v_min_u32_e32 v55, v55, v58
	v_max_u32_e32 v58, v56, v37
	v_min_u32_e32 v37, v56, v37
	v_max_u32_e32 v56, v59, v60
	v_min_u32_e32 v59, v59, v60
	v_max_u32_e32 v60, v33, v32
	v_min_u32_e32 v32, v33, v32
	v_max_u32_e32 v33, v29, v31
	v_min_u32_e32 v29, v29, v31
	v_max_u32_e32 v31, v30, v35
	v_min_u32_e32 v30, v30, v35
	v_max_u32_e32 v35, v34, v28
	v_min_u32_e32 v28, v34, v28
	v_max_u32_e32 v34, v36, v46
	v_min_u32_e32 v36, v36, v46
	v_max_u32_e32 v46, v39, v45
	v_min_u32_e32 v39, v39, v45
	v_max_u32_e32 v45, v43, v47
	v_min_u32_e32 v43, v43, v47
	v_max_u32_e32 v47, v40, v41
	v_min_u32_e32 v40, v40, v41
	v_max_u32_e32 v41, v38, v50
	v_min_u32_e32 v38, v38, v50
	v_max_u32_e32 v50, v49, v48
	v_min_u32_e32 v48, v49, v48
	v_max_u32_e32 v49, v42, v53
	v_min_u32_e32 v42, v42, v53
	v_max_u32_e32 v53, v44, v51
	v_min_u32_e32 v44, v44, v51
	v_max_u32_e32 v51, v54, v58
	v_min_u32_e32 v54, v54, v58
	v_max_u32_e32 v58, v57, v56
	v_min_u32_e32 v56, v57, v56
	v_max_u32_e32 v57, v52, v37
	v_min_u32_e32 v37, v52, v37
	v_max_u32_e32 v52, v55, v59
	v_min_u32_e32 v55, v55, v59
	v_max_u32_e32 v59, v60, v31
	v_min_u32_e32 v31, v60, v31
	v_max_u32_e32 v60, v33, v35
	v_min_u32_e32 v33, v33, v35
	v_max_u32_e32 v35, v32, v30
	v_min_u32_e32 v30, v32, v30
	v_max_u32_e32 v32, v29, v28
	v_min_u32_e32 v28, v29, v28
	v_max_u32_e32 v29, v36, v43
	v_min_u32_e32 v36, v36, v43
	v_max_u32_e32 v43, v39, v40
	v_min_u32_e32 v39, v39, v40
	v_max_u32_e32 v40, v34, v45
	v_min_u32_e32 v34, v34, v45
	v_max_u32_e32 v45, v46, v47
	v_min_u32_e32 v46, v46, v47
	v_max_u32_e32 v47, v38, v42
	v_min_u32_e32 v38, v38, v42
	v_max_u32_e32 v42, v48, v44
	v_min_u32_e32 v44, v48, v44
	v_max_u32_e32 v48, v41, v49
	v_min_u32_e32 v41, v41, v49
	v_max_u32_e32 v49, v50, v53
	v_min_u32_e32 v50, v50, v53
	v_min_u32_e32 v53, v51, v58
	v_min_u32_e32 v61, v54, v56
	v_min_u32_e32 v62, v57, v52
	v_min_u32_e32 v63, v37, v55
	v_min_u32_e32 v64, v59, v60
	v_min_u32_e32 v65, v31, v33
	v_min_u32_e32 v66, v35, v32
	v_min_u32_e32 v67, v30, v28
	v_min_u32_e32 v68, v36, v39
	v_min_u32_e32 v69, v29, v43
	v_min_u32_e32 v70, v34, v46
	v_min_u32_e32 v71, v40, v45
	v_min_u32_e32 v72, v38, v44
	v_min_u32_e32 v73, v47, v42
	v_min_u32_e32 v74, v41, v50
	v_min_u32_e32 v75, v48, v49
	v_max3_u32 v51, v51, v58, v68
	v_max3_u32 v36, v53, v36, v39
	v_max3_u32 v39, v54, v56, v69
	v_max3_u32 v29, v61, v29, v43
	v_max3_u32 v43, v57, v52, v70
	v_max3_u32 v34, v62, v34, v46
	v_max3_u32 v37, v37, v55, v71
	v_max3_u32 v40, v63, v40, v45
	v_max3_u32 v45, v59, v60, v72
	v_max3_u32 v38, v64, v38, v44
	v_max3_u32 v31, v31, v33, v73
	v_max3_u32 v33, v65, v47, v42
	v_max3_u32 v32, v35, v32, v74
	v_max3_u32 v35, v66, v41, v50
	v_max3_u32 v28, v30, v28, v75
	v_max3_u32 v30, v67, v48, v49
	v_max_u32_e32 v41, v51, v45
	v_min_u32_e32 v42, v51, v45
	v_max_u32_e32 v44, v36, v38
	v_min_u32_e32 v36, v36, v38
	v_max_u32_e32 v38, v39, v31
	v_min_u32_e32 v31, v39, v31
	v_max_u32_e32 v39, v29, v33
	v_min_u32_e32 v29, v29, v33
	v_max_u32_e32 v33, v43, v32
	v_min_u32_e32 v32, v43, v32
	v_max_u32_e32 v43, v34, v35
	v_min_u32_e32 v34, v34, v35
	v_max_u32_e32 v35, v37, v28
	v_min_u32_e32 v28, v37, v28
	v_max_u32_e32 v37, v40, v30
	v_min_u32_e32 v30, v40, v30
	v_max_u32_e32 v40, v41, v33
	v_min_u32_e32 v33, v41, v33
	v_max_u32_e32 v41, v44, v43
	v_min_u32_e32 v43, v44, v43
	v_max_u32_e32 v44, v38, v35
	v_min_u32_e32 v35, v38, v35
	v_max_u32_e32 v38, v39, v37
	v_min_u32_e32 v37, v39, v37
	v_max_u32_e32 v39, v42, v32
	v_min_u32_e32 v32, v42, v32
	v_max_u32_e32 v42, v36, v34
	v_min_u32_e32 v34, v36, v34
	v_max_u32_e32 v36, v31, v28
	v_min_u32_e32 v28, v31, v28
	v_max_u32_e32 v31, v29, v30
	v_min_u32_e32 v29, v29, v30
	v_max_u32_e32 v30, v40, v44
	v_min_u32_e32 v40, v40, v44
	v_max_u32_e32 v44, v41, v38
	v_min_u32_e32 v38, v41, v38
	v_max_u32_e32 v41, v33, v35
	v_min_u32_e32 v33, v33, v35
	v_max_u32_e32 v35, v43, v37
	v_min_u32_e32 v37, v43, v37
	v_max_u32_e32 v43, v39, v36
	v_min_u32_e32 v36, v39, v36
	v_max_u32_e32 v39, v42, v31
	v_min_u32_e32 v31, v42, v31
	v_max_u32_e32 v42, v32, v28
	v_min_u32_e32 v28, v32, v28
	v_max_u32_e32 v32, v34, v29
	v_min_u32_e32 v29, v34, v29
	v_max_u32_e32 v34, v30, v44
	v_min_u32_e32 v30, v30, v44
	v_max_u32_e32 v44, v40, v38
	v_min_u32_e32 v38, v40, v38
	v_max_u32_e32 v40, v41, v35
	v_min_u32_e32 v35, v41, v35
	v_max_u32_e32 v41, v33, v37
	v_min_u32_e32 v33, v33, v37
	v_max_u32_e32 v37, v43, v39
	v_min_u32_e32 v39, v43, v39
	v_max_u32_e32 v43, v36, v31
	v_min_u32_e32 v31, v36, v31
	v_max_u32_e32 v36, v42, v32
	v_min_u32_e32 v32, v42, v32
	v_max_u32_e32 v42, v28, v29
	v_min_u32_e32 v28, v28, v29
	v_max_u32_dpp v46, v32, v44 quad_perm:[1,0,3,2] row_mask:0xf bank_mask:0xf bound_ctrl:1
	v_max_u32_dpp v45, v42, v30 quad_perm:[1,0,3,2] row_mask:0xf bank_mask:0xf bound_ctrl:1
	v_max_u32_dpp v29, v28, v34 quad_perm:[1,0,3,2] row_mask:0xf bank_mask:0xf bound_ctrl:1
	v_max_u32_dpp v47, v36, v38 quad_perm:[1,0,3,2] row_mask:0xf bank_mask:0xf bound_ctrl:1
	v_max_u32_dpp v48, v31, v40 quad_perm:[1,0,3,2] row_mask:0xf bank_mask:0xf bound_ctrl:1
	v_max_u32_dpp v49, v43, v35 quad_perm:[1,0,3,2] row_mask:0xf bank_mask:0xf bound_ctrl:1
	v_max_u32_dpp v50, v39, v41 quad_perm:[1,0,3,2] row_mask:0xf bank_mask:0xf bound_ctrl:1
	v_max_u32_dpp v51, v37, v33 quad_perm:[1,0,3,2] row_mask:0xf bank_mask:0xf bound_ctrl:1
	v_max_u32_dpp v33, v33, v37 quad_perm:[1,0,3,2] row_mask:0xf bank_mask:0xf bound_ctrl:1
	v_max_u32_dpp v37, v41, v39 quad_perm:[1,0,3,2] row_mask:0xf bank_mask:0xf bound_ctrl:1
	v_max_u32_dpp v35, v35, v43 quad_perm:[1,0,3,2] row_mask:0xf bank_mask:0xf bound_ctrl:1
	v_max_u32_dpp v31, v40, v31 quad_perm:[1,0,3,2] row_mask:0xf bank_mask:0xf bound_ctrl:1
	v_max_u32_dpp v36, v38, v36 quad_perm:[1,0,3,2] row_mask:0xf bank_mask:0xf bound_ctrl:1
	v_max_u32_dpp v32, v44, v32 quad_perm:[1,0,3,2] row_mask:0xf bank_mask:0xf bound_ctrl:1
	v_max_u32_dpp v30, v30, v42 quad_perm:[1,0,3,2] row_mask:0xf bank_mask:0xf bound_ctrl:1
	v_max_u32_dpp v28, v34, v28 quad_perm:[1,0,3,2] row_mask:0xf bank_mask:0xf bound_ctrl:1
	v_max_u32_e32 v34, v29, v33
	v_min_u32_e32 v29, v29, v33
	v_max_u32_e32 v33, v45, v37
	v_min_u32_e32 v37, v45, v37
	v_max_u32_e32 v38, v46, v35
	v_min_u32_e32 v35, v46, v35
	v_max_u32_e32 v39, v47, v31
	v_min_u32_e32 v31, v47, v31
	v_max_u32_e32 v40, v48, v36
	v_min_u32_e32 v36, v48, v36
	v_max_u32_e32 v41, v49, v32
	v_min_u32_e32 v32, v49, v32
	v_max_u32_e32 v42, v50, v30
	v_min_u32_e32 v30, v50, v30
	v_max_u32_e32 v43, v51, v28
	v_min_u32_e32 v28, v51, v28
	v_max_u32_e32 v44, v34, v40
	v_min_u32_e32 v34, v34, v40
	v_max_u32_e32 v40, v33, v41
	v_min_u32_e32 v33, v33, v41
	v_max_u32_e32 v41, v38, v42
	v_min_u32_e32 v38, v38, v42
	v_max_u32_e32 v42, v39, v43
	v_min_u32_e32 v39, v39, v43
	v_max_u32_e32 v43, v29, v36
	v_min_u32_e32 v29, v29, v36
	v_max_u32_e32 v36, v37, v32
	v_min_u32_e32 v32, v37, v32
	v_max_u32_e32 v37, v35, v30
	v_min_u32_e32 v30, v35, v30
	v_max_u32_e32 v35, v31, v28
	v_min_u32_e32 v28, v31, v28
	v_max_u32_e32 v31, v44, v41
	v_min_u32_e32 v41, v44, v41
	v_max_u32_e32 v44, v40, v42
	v_min_u32_e32 v42, v40, v42
	v_max_u32_e32 v45, v34, v38
	v_min_u32_e32 v34, v34, v38
	v_max_u32_e32 v38, v33, v39
	v_min_u32_e32 v33, v33, v39
	v_max_u32_e32 v39, v43, v37
	v_min_u32_e32 v43, v43, v37
	v_max_u32_e32 v46, v36, v35
	v_min_u32_e32 v35, v36, v35
	v_max_u32_e32 v47, v29, v30
	v_min_u32_e32 v50, v29, v30
	v_max_u32_e32 v51, v32, v28
	v_min_u32_e32 v52, v32, v28
	v_max_u32_e32 v40, v31, v44
	v_min_u32_e32 v30, v31, v44
	v_max_u32_e32 v36, v41, v42
	v_min_u32_e32 v28, v41, v42
	v_max_u32_e32 v41, v45, v38
	v_min_u32_e32 v31, v45, v38
	v_max_u32_e32 v37, v34, v33
	v_min_u32_e32 v29, v34, v33
	v_max_u32_e32 v48, v39, v46
	v_min_u32_e32 v34, v39, v46
	v_max_u32_e32 v42, v43, v35
	v_min_u32_e32 v32, v43, v35
	v_max_u32_e32 v49, v47, v51
	v_min_u32_e32 v35, v47, v51
	v_max_u32_e32 v44, v50, v52
	v_min_u32_e32 v33, v50, v52
	v_mov_b32_dpp v52, v35 quad_perm:[2,3,0,1] row_mask:0xf bank_mask:0xf bound_ctrl:1
	v_mov_b32_dpp v43, v44 quad_perm:[2,3,0,1] row_mask:0xf bank_mask:0xf bound_ctrl:1
	v_mov_b32_dpp v54, v33 quad_perm:[2,3,0,1] row_mask:0xf bank_mask:0xf bound_ctrl:1
	v_mov_b32_dpp v38, v49 quad_perm:[2,3,0,1] row_mask:0xf bank_mask:0xf bound_ctrl:1
	v_mov_b32_dpp v55, v32 quad_perm:[2,3,0,1] row_mask:0xf bank_mask:0xf bound_ctrl:1
	v_mov_b32_dpp v45, v42 quad_perm:[2,3,0,1] row_mask:0xf bank_mask:0xf bound_ctrl:1
	v_mov_b32_dpp v53, v34 quad_perm:[2,3,0,1] row_mask:0xf bank_mask:0xf bound_ctrl:1
	v_mov_b32_dpp v39, v48 quad_perm:[2,3,0,1] row_mask:0xf bank_mask:0xf bound_ctrl:1
	v_mov_b32_dpp v58, v29 quad_perm:[2,3,0,1] row_mask:0xf bank_mask:0xf bound_ctrl:1
	v_mov_b32_dpp v50, v37 quad_perm:[2,3,0,1] row_mask:0xf bank_mask:0xf bound_ctrl:1
	v_mov_b32_dpp v56, v31 quad_perm:[2,3,0,1] row_mask:0xf bank_mask:0xf bound_ctrl:1
	v_mov_b32_dpp v46, v41 quad_perm:[2,3,0,1] row_mask:0xf bank_mask:0xf bound_ctrl:1
	v_mov_b32_dpp v59, v28 quad_perm:[2,3,0,1] row_mask:0xf bank_mask:0xf bound_ctrl:1
	v_mov_b32_dpp v51, v36 quad_perm:[2,3,0,1] row_mask:0xf bank_mask:0xf bound_ctrl:1
	v_mov_b32_dpp v57, v30 quad_perm:[2,3,0,1] row_mask:0xf bank_mask:0xf bound_ctrl:1
	v_mov_b32_dpp v47, v40 quad_perm:[2,3,0,1] row_mask:0xf bank_mask:0xf bound_ctrl:1
	s_and_saveexec_b64 s[8:9], s[46:47]
	s_cbranch_execz .LBB0_725
	v_max_u32_e32 v40, v40, v54
	v_max_u32_e32 v48, v48, v58
	v_max_u32_e32 v41, v41, v55
	v_max_u32_e32 v49, v49, v59
	v_max_u32_e32 v36, v36, v52
	v_max_u32_e32 v42, v42, v56
	v_max_u32_e32 v37, v37, v53
	v_max_u32_e32 v44, v44, v57
	v_max_u32_e32 v43, v30, v43
	v_max_u32_e32 v50, v34, v50
	v_max_u32_e32 v45, v31, v45
	v_max_u32_e32 v51, v35, v51
	v_max_u32_e32 v38, v28, v38
	v_max_u32_e32 v46, v32, v46
	v_max_u32_e32 v39, v29, v39
	v_max_u32_e32 v47, v33, v47
	v_min_u32_e32 v54, v40, v48
	v_min_u32_e32 v55, v41, v49
	v_min_u32_e32 v52, v36, v42
	v_min_u32_e32 v53, v37, v44
	v_min_u32_e32 v34, v43, v50
	v_min_u32_e32 v35, v45, v51
	v_min_u32_e32 v32, v38, v46
	v_min_u32_e32 v33, v39, v47
	v_max_u32_e32 v40, v40, v48
	v_max_u32_e32 v41, v41, v49
	v_max_u32_e32 v42, v36, v42
	v_max_u32_e32 v44, v37, v44
	v_max_u32_e32 v43, v43, v50
	v_max_u32_e32 v45, v45, v51
	v_max_u32_e32 v46, v38, v46
	v_max_u32_e32 v47, v39, v47
	v_min_u32_e32 v48, v40, v41
	v_min_u32_e32 v36, v42, v44
	v_min_u32_e32 v49, v43, v45
	v_max_u32_e32 v40, v40, v41
	v_max_u32_e32 v41, v42, v44
	v_max_u32_e32 v44, v43, v45
	v_max_u32_e32 v45, v46, v47
	v_min_u32_e32 v58, v54, v55
	v_min_u32_e32 v56, v52, v53
	v_min_u32_e32 v59, v34, v35
	v_min_u32_e32 v28, v32, v33
	v_max_u32_e32 v54, v54, v55
	v_max_u32_e32 v52, v52, v53
	v_max_u32_e32 v55, v34, v35
	v_max_u32_e32 v32, v32, v33
	v_min_u32_e32 v50, v46, v47
	v_min_u32_e32 v42, v40, v41
	v_min_u32_e32 v46, v44, v45
	v_max_u32_e32 v40, v40, v41
	v_max_u32_e32 v44, v44, v45
	v_min_u32_e32 v57, v58, v56
	v_min_u32_e32 v29, v59, v28
	v_max_u32_e32 v56, v58, v56
	v_max_u32_e32 v28, v59, v28
	v_min_u32_e32 v53, v54, v52
	v_min_u32_e32 v33, v55, v32
	v_max_u32_e32 v52, v54, v52
	v_max_u32_e32 v32, v55, v32
	v_min_u32_e32 v37, v48, v36
	v_min_u32_e32 v38, v49, v50
	v_max_u32_e32 v36, v48, v36
	v_max_u32_e32 v48, v49, v50
	v_min_u32_e32 v43, v42, v46
	v_max_u32_e32 v42, v42, v46
	v_min_u32_e32 v41, v40, v44
	v_max_u32_e32 v40, v40, v44
	v_min_u32_e32 v31, v57, v29
	v_max_u32_e32 v30, v57, v29
	v_min_u32_e32 v29, v56, v28
	v_max_u32_e32 v28, v56, v28
	v_min_u32_e32 v35, v53, v33
	v_max_u32_e32 v34, v53, v33
	v_min_u32_e32 v33, v52, v32
	v_max_u32_e32 v32, v52, v32
	v_min_u32_e32 v39, v37, v38
	v_max_u32_e32 v38, v37, v38
	v_min_u32_e32 v37, v36, v48
	v_max_u32_e32 v36, v36, v48
	ds_write_b128 v246, v[40:43]
	ds_write_b128 v246, v[36:39] offset:16
	ds_write_b128 v246, v[32:35] offset:32
	ds_write_b128 v246, v[28:31] offset:48
.LBB0_725:
	s_or_b64 exec, exec, s[8:9]
	s_waitcnt lgkmcnt(0)
	ds_read_u16 v28, v232 offset:40960
	ds_read_u16 v30, v232 offset:40968
	ds_read_u16 v31, v232 offset:40976
	ds_read_u16 v32, v232 offset:40984
	ds_read_u16 v33, v232 offset:40992
	ds_read_u16 v34, v232 offset:41000
	ds_read_u16 v35, v232 offset:41008
	ds_read_u16 v36, v232 offset:41016
	s_waitcnt lgkmcnt(7)
	v_lshrrev_b32_e32 v29, 8, v28
	v_add_u32_e64 v29, v231, v29
	ds_read_b32 v29, v29 offset:64
	v_add_u32_sdwa v28, v231, v28 dst_sel:DWORD dst_unused:UNUSED_PAD src0_sel:DWORD src1_sel:BYTE_0
	s_waitcnt lgkmcnt(7)
	v_add_u32_sdwa v37, v231, v30 dst_sel:DWORD dst_unused:UNUSED_PAD src0_sel:DWORD src1_sel:BYTE_0
	ds_read_b32 v37, v37
	ds_read_b32 v28, v28
	s_waitcnt lgkmcnt(5)
	v_add_u32_sdwa v45, v231, v34 dst_sel:DWORD dst_unused:UNUSED_PAD src0_sel:DWORD src1_sel:BYTE_0
	s_waitcnt lgkmcnt(2)
	v_cmp_lt_i32_e32 vcc, -1, v29
	v_and_b32_e32 v38, 0xffffff80, v29
	ds_read_u16 v39, v232 offset:41024
	ds_read_u16 v40, v232 offset:41032
	ds_read_u16 v41, v232 offset:41040
	ds_read_u16 v42, v232 offset:41048
	ds_read_u16 v43, v232 offset:41056
	v_cndmask_b32_e64 v29, v218, -1, vcc
	s_waitcnt lgkmcnt(5)
	v_cmp_lt_i32_e32 vcc, -1, v28
	v_and_b32_e32 v44, 0xffffff80, v28
	v_xor_b32_e64 v29, v29, v38
	v_cndmask_b32_e64 v28, v218, -1, vcc
	v_xor_b32_e64 v28, v28, v44
	v_pk_add_f32 v[28:29], v[28:29], v[28:29] op_sel:[1,0] op_sel_hi:[0,1]
	v_cmp_lt_i32_e32 vcc, -1, v28
	v_add_u32_sdwa v44, v231, v33 dst_sel:DWORD dst_unused:UNUSED_PAD src0_sel:DWORD src1_sel:BYTE_0
	v_lshrrev_b32_e32 v33, 8, v33
	v_cndmask_b32_e64 v29, -1, v218, vcc
	v_bitop3_b32 v28, v29, s78, v28 bitop3:0x48
	v_sub_u32_e32 v28, v28, v182
	v_add_u32_e32 v38, 63, v28
	v_lshrrev_b32_e64 v28, 8, v30
	v_add_u32_sdwa v29, v231, v31 dst_sel:DWORD dst_unused:UNUSED_PAD src0_sel:DWORD src1_sel:BYTE_0
	v_lshrrev_b32_e64 v30, 8, v31
	v_add_u32_sdwa v31, v231, v32 dst_sel:DWORD dst_unused:UNUSED_PAD src0_sel:DWORD src1_sel:BYTE_0
	v_lshrrev_b32_e32 v32, 8, v32
	v_add_u32_e32 v28, v231, v28
	v_add_u32_e32 v30, v231, v30
	v_add_u32_e32 v32, v231, v32
	v_add_u32_e64 v33, v231, v33
	ds_read_b32 v28, v28 offset:64
	ds_read_b32 v46, v29
	ds_read_b32 v30, v30 offset:64
	ds_read_b32 v47, v31
	ds_read_b32 v32, v32 offset:64
	ds_read_b32 v44, v44
	ds_read_b32 v33, v33 offset:64
	ds_read_b32 v45, v45
	s_waitcnt lgkmcnt(7)
	v_cmp_lt_i32_e32 vcc, -1, v28
	v_and_b32_e32 v29, 0xffffff80, v28
	v_and_b32_e32 v31, 0xffffff80, v37
	v_cndmask_b32_e64 v28, v218, -1, vcc
	v_cmp_lt_i32_e32 vcc, -1, v37
	v_xor_b32_e32 v29, v28, v29
	s_waitcnt lgkmcnt(5)
	v_and_b32_e32 v28, 0xffffff80, v30
	v_cndmask_b32_e64 v37, v218, -1, vcc
	v_cmp_lt_i32_e32 vcc, -1, v30
	v_xor_b32_e64 v31, v37, v31
	v_and_b32_e32 v37, 0xffffff80, v46
	v_cndmask_b32_e64 v30, v218, -1, vcc
	v_cmp_lt_i32_e32 vcc, -1, v46
	v_xor_b32_e32 v28, v30, v28
	s_nop 0
	v_cndmask_b32_e64 v46, v218, -1, vcc
	v_xor_b32_e32 v30, v46, v37
	v_pk_add_f32 v[28:29], v[30:31], v[28:29]
	s_nop 0
	v_cmp_lt_i32_e32 vcc, -1, v29
	s_nop 1
	v_cndmask_b32_e32 v30, v219, v218, vcc
	v_bitop3_b32 v29, v30, v29, s78 bitop3:0x78
	v_sub_u32_e32 v29, v29, v233
	v_cmp_lt_i32_e32 vcc, -1, v28
	v_add_u32_e32 v37, 63, v29
	s_waitcnt lgkmcnt(4)
	v_and_b32_e32 v30, 0xffffff80, v47
	v_cndmask_b32_e64 v29, v219, v218, vcc
	s_waitcnt lgkmcnt(3)
	v_cmp_lt_i32_e32 vcc, -1, v32
	v_bitop3_b32 v28, v29, v28, s78 bitop3:0x78
	v_sub_u32_e64 v28, v28, v234
	v_cndmask_b32_e64 v29, v218, -1, vcc
	v_cmp_lt_i32_e32 vcc, -1, v47
	v_add_u32_e32 v46, 63, v28
	v_and_b32_e32 v28, 0xffffff80, v32
	v_cndmask_b32_e64 v31, v218, -1, vcc
	s_waitcnt lgkmcnt(1)
	v_cmp_lt_i32_e32 vcc, -1, v33
	v_xor_b32_e32 v29, v29, v28
	v_xor_b32_e32 v31, v31, v30
	v_cndmask_b32_e64 v32, v218, -1, vcc
	v_cmp_lt_i32_e32 vcc, -1, v44
	v_and_b32_e32 v28, 0xffffff80, v33
	v_and_b32_e32 v30, 0xffffff80, v44
	v_cndmask_b32_e64 v33, v218, -1, vcc
	v_xor_b32_e32 v28, v32, v28
	v_xor_b32_e64 v30, v33, v30
	v_pk_add_f32 v[28:29], v[30:31], v[28:29]
	v_add_u32_sdwa v31, v231, v36 dst_sel:DWORD dst_unused:UNUSED_PAD src0_sel:DWORD src1_sel:BYTE_0
	v_cmp_lt_i32_e32 vcc, -1, v29
	s_nop 1
	v_cndmask_b32_e64 v30, v219, v218, vcc
	v_bitop3_b32 v29, v30, v29, s78 bitop3:0x78
	v_sub_u32_e32 v29, v29, v235
	v_cmp_lt_i32_e32 vcc, -1, v28
	v_add_u32_e32 v32, 63, v29
	v_lshrrev_b32_e32 v30, 8, v35
	v_cndmask_b32_e64 v29, v219, v218, vcc
	v_bitop3_b32 v28, v29, v28, s78 bitop3:0x78
	v_sub_u32_e32 v28, v28, v236
	v_add_u32_e32 v33, 63, v28
	v_lshrrev_b32_e32 v28, 8, v34
	v_lshrrev_b32_e32 v34, 8, v36
	v_lshrrev_b32_e32 v36, 8, v39
	v_add_u32_e32 v28, v231, v28
	v_add_u32_sdwa v29, v231, v35 dst_sel:DWORD dst_unused:UNUSED_PAD src0_sel:DWORD src1_sel:BYTE_0
	v_add_u32_e32 v30, v231, v30
	v_add_u32_e32 v34, v231, v34
	v_add_u32_sdwa v35, v231, v39 dst_sel:DWORD dst_unused:UNUSED_PAD src0_sel:DWORD src1_sel:BYTE_0
	v_add_u32_e64 v36, v231, v36
	v_add_u32_sdwa v39, v231, v40 dst_sel:DWORD dst_unused:UNUSED_PAD src0_sel:DWORD src1_sel:BYTE_0
	ds_read_b32 v28, v28 offset:64
	ds_read_b32 v44, v29
	ds_read_b32 v30, v30 offset:64
	ds_read_b32 v47, v31
	ds_read_b32 v34, v34 offset:64
	ds_read_b32 v35, v35
	ds_read_b32 v36, v36 offset:64
	ds_read_b32 v39, v39
	s_waitcnt lgkmcnt(7)
	v_cmp_lt_i32_e32 vcc, -1, v28
	v_and_b32_e32 v29, 0xffffff80, v28
	v_and_b32_e32 v31, 0xffffff80, v45
	v_cndmask_b32_e64 v28, v218, -1, vcc
	v_cmp_lt_i32_e32 vcc, -1, v45
	v_xor_b32_e32 v29, v28, v29
	s_waitcnt lgkmcnt(5)
	v_and_b32_e32 v28, 0xffffff80, v30
	v_cndmask_b32_e64 v45, v218, -1, vcc
	v_cmp_lt_i32_e32 vcc, -1, v30
	v_xor_b32_e64 v31, v45, v31
	v_and_b32_e32 v45, 0xffffff80, v44
	v_cndmask_b32_e64 v30, v218, -1, vcc
	v_cmp_lt_i32_e32 vcc, -1, v44
	v_xor_b32_e32 v28, v30, v28
	s_nop 0
	v_cndmask_b32_e64 v44, v218, -1, vcc
	v_xor_b32_e32 v30, v44, v45
	v_pk_add_f32 v[28:29], v[30:31], v[28:29]
	s_nop 0
	v_cmp_lt_i32_e32 vcc, -1, v29
	s_nop 1
	v_cndmask_b32_e32 v30, v219, v218, vcc
	v_bitop3_b32 v29, v30, v29, s78 bitop3:0x78
	v_sub_u32_e32 v29, v29, v237
	v_cmp_lt_i32_e32 vcc, -1, v28
	v_add_u32_e32 v44, 63, v29
	s_waitcnt lgkmcnt(4)
	v_and_b32_e32 v30, 0xffffff80, v47
	v_cndmask_b32_e64 v29, v219, v218, vcc
	s_waitcnt lgkmcnt(3)
	v_cmp_lt_i32_e32 vcc, -1, v34
	v_bitop3_b32 v28, v29, v28, s78 bitop3:0x78
	v_sub_u32_e64 v28, v28, v238
	v_cndmask_b32_e64 v29, v218, -1, vcc
	v_cmp_lt_i32_e32 vcc, -1, v47
	v_add_u32_e32 v45, 63, v28
	v_and_b32_e32 v28, 0xffffff80, v34
	v_cndmask_b32_e64 v31, v218, -1, vcc
	s_waitcnt lgkmcnt(1)
	v_cmp_lt_i32_e32 vcc, -1, v36
	v_xor_b32_e32 v29, v29, v28
	v_xor_b32_e32 v31, v31, v30
	v_cndmask_b32_e64 v34, v218, -1, vcc
	v_cmp_lt_i32_e32 vcc, -1, v35
	v_and_b32_e32 v28, 0xffffff80, v36
	v_and_b32_e32 v30, 0xffffff80, v35
	v_cndmask_b32_e64 v35, v218, -1, vcc
	v_xor_b32_e32 v28, v34, v28
	v_xor_b32_e64 v30, v35, v30
	v_pk_add_f32 v[28:29], v[30:31], v[28:29]
	v_lshrrev_b32_e32 v36, 8, v42
	v_cmp_lt_i32_e32 vcc, -1, v29
	v_add_u32_e64 v36, v231, v36
	v_add_u32_sdwa v31, v231, v42 dst_sel:DWORD dst_unused:UNUSED_PAD src0_sel:DWORD src1_sel:BYTE_0
	v_cndmask_b32_e64 v30, v219, v218, vcc
	v_bitop3_b32 v29, v30, v29, s78 bitop3:0x78
	v_sub_u32_e32 v29, v29, v239
	v_cmp_lt_i32_e32 vcc, -1, v28
	v_add_u32_e32 v34, 63, v29
	v_lshrrev_b32_e32 v30, 8, v41
	v_cndmask_b32_e64 v29, v219, v218, vcc
	v_bitop3_b32 v28, v29, v28, s78 bitop3:0x78
	v_sub_u32_e32 v28, v28, v240
	v_add_u32_e32 v35, 63, v28
	v_lshrrev_b32_e64 v28, 8, v40
	v_add_u32_sdwa v29, v231, v41 dst_sel:DWORD dst_unused:UNUSED_PAD src0_sel:DWORD src1_sel:BYTE_0
	v_lshrrev_b32_e32 v41, 8, v43
	v_add_u32_e32 v28, v231, v28
	v_add_u32_e64 v30, v231, v30
	v_add_u32_sdwa v40, v231, v43 dst_sel:DWORD dst_unused:UNUSED_PAD src0_sel:DWORD src1_sel:BYTE_0
	v_add_u32_e64 v41, v231, v41
	ds_read_b32 v28, v28 offset:64
	ds_read_b32 v42, v29
	ds_read_b32 v30, v30 offset:64
	ds_read_b32 v43, v31
	ds_read_b32 v36, v36 offset:64
	ds_read_b32 v40, v40
	ds_read_b32 v41, v41 offset:64
	s_waitcnt lgkmcnt(6)
	v_cmp_lt_i32_e32 vcc, -1, v28
	v_and_b32_e32 v29, 0xffffff80, v28
	v_and_b32_e32 v31, 0xffffff80, v39
	v_cndmask_b32_e64 v28, v218, -1, vcc
	v_cmp_lt_i32_e32 vcc, -1, v39
	v_xor_b32_e32 v29, v28, v29
	s_waitcnt lgkmcnt(4)
	v_and_b32_e32 v28, 0xffffff80, v30
	v_cndmask_b32_e64 v39, v218, -1, vcc
	v_cmp_lt_i32_e32 vcc, -1, v30
	v_xor_b32_e64 v31, v39, v31
	v_and_b32_e32 v39, 0xffffff80, v42
	v_cndmask_b32_e64 v30, v218, -1, vcc
	v_cmp_lt_i32_e32 vcc, -1, v42
	v_xor_b32_e32 v28, v30, v28
	s_nop 0
	v_cndmask_b32_e64 v42, v218, -1, vcc
	v_xor_b32_e32 v30, v42, v39
	v_pk_add_f32 v[28:29], v[30:31], v[28:29]
	s_nop 0
	v_cmp_lt_i32_e32 vcc, -1, v29
	s_nop 1
	v_cndmask_b32_e32 v30, v219, v218, vcc
	v_bitop3_b32 v29, v30, v29, s78 bitop3:0x78
	v_sub_u32_e32 v29, v29, v241
	v_cmp_lt_i32_e32 vcc, -1, v28
	v_add_u32_e32 v39, 63, v29
	s_waitcnt lgkmcnt(3)
	v_and_b32_e32 v30, 0xffffff80, v43
	v_cndmask_b32_e64 v29, v219, v218, vcc
	s_waitcnt lgkmcnt(2)
	v_cmp_lt_i32_e32 vcc, -1, v36
	v_bitop3_b32 v28, v29, v28, s78 bitop3:0x78
	v_sub_u32_e64 v28, v28, v242
	v_cndmask_b32_e64 v29, v218, -1, vcc
	v_cmp_lt_i32_e32 vcc, -1, v43
	v_add_u32_e32 v42, 63, v28
	v_and_b32_e32 v28, 0xffffff80, v36
	v_cndmask_b32_e64 v31, v218, -1, vcc
	s_waitcnt lgkmcnt(0)
	v_cmp_lt_i32_e32 vcc, -1, v41
	v_xor_b32_e32 v29, v29, v28
	v_xor_b32_e32 v31, v31, v30
	v_cndmask_b32_e64 v36, v218, -1, vcc
	v_cmp_lt_i32_e32 vcc, -1, v40
	v_and_b32_e32 v28, 0xffffff80, v41
	v_and_b32_e32 v30, 0xffffff80, v40
	v_cndmask_b32_e64 v40, v218, -1, vcc
	v_xor_b32_e32 v28, v36, v28
	v_xor_b32_e64 v30, v40, v30
	v_pk_add_f32 v[28:29], v[30:31], v[28:29]
	v_min_u32_e32 v31, v38, v37
	v_cmp_lt_i32_e32 vcc, -1, v29
	v_max_u32_e32 v36, v46, v32
	v_min_u32_e32 v32, v46, v32
	v_cndmask_b32_e64 v30, v219, v218, vcc
	v_bitop3_b32 v29, v30, v29, s78 bitop3:0x78
	v_sub_u32_e32 v29, v29, v243
	v_cmp_lt_i32_e32 vcc, -1, v28
	v_add_u32_e32 v29, 63, v29
	v_max_u32_e32 v40, v35, v39
	v_cndmask_b32_e64 v30, v219, v218, vcc
	v_bitop3_b32 v28, v30, v28, s78 bitop3:0x78
	v_max_u32_e32 v30, v38, v37
	v_max_u32_e32 v37, v33, v44
	v_min_u32_e32 v33, v33, v44
	v_max_u32_e32 v38, v45, v34
	v_min_u32_e32 v34, v45, v34
	v_min_u32_e32 v35, v35, v39
	v_max_u32_e32 v39, v42, v29
	v_min_u32_e32 v29, v42, v29
	v_sub_u32_e32 v28, v28, v244
	v_max_u32_e32 v41, v30, v32
	v_min_u32_e32 v30, v30, v32
	v_max_u32_e32 v32, v31, v36
	v_min_u32_e32 v31, v31, v36
	v_max_u32_e32 v36, v37, v34
	v_min_u32_e32 v34, v37, v34
	v_max_u32_e32 v37, v33, v38
	v_min_u32_e32 v33, v33, v38
	v_max_u32_e32 v38, v40, v29
	v_min_u32_e32 v29, v40, v29
	v_max_u32_e32 v40, v35, v39
	v_min_u32_e32 v35, v35, v39
	v_add_u32_e32 v28, 63, v28
	v_max_u32_e32 v39, v41, v32
	v_min_u32_e32 v32, v41, v32
	v_max_u32_e32 v41, v30, v31
	v_min_u32_e32 v30, v30, v31
	v_max_u32_e32 v31, v34, v33
	v_min_u32_e32 v33, v34, v33
	v_max_u32_e32 v34, v36, v37
	v_min_u32_e32 v36, v36, v37
	v_max_u32_e32 v37, v38, v40
	v_min_u32_e32 v38, v38, v40
	v_max_u32_e32 v40, v29, v35
	v_min_u32_e32 v29, v29, v35
	v_max_u32_e32 v35, v39, v33
	v_min_u32_e32 v33, v39, v33
	v_max_u32_e32 v39, v32, v31
	v_min_u32_e32 v31, v32, v31
	v_max_u32_e32 v32, v41, v36
	v_min_u32_e32 v36, v41, v36
	v_max_u32_e32 v41, v30, v34
	v_min_u32_e32 v30, v30, v34
	v_max_u32_e32 v34, v29, v28
	v_min_u32_e32 v28, v29, v28
	v_max_u32_e32 v29, v35, v32
	v_min_u32_e32 v32, v35, v32
	v_max_u32_e32 v35, v39, v41
	v_min_u32_e32 v39, v39, v41
	v_max_u32_e32 v41, v33, v36
	v_min_u32_e32 v33, v33, v36
	v_max_u32_e32 v36, v31, v30
	v_min_u32_e32 v30, v31, v30
	v_max_u32_e32 v31, v37, v40
	v_min_u32_e32 v37, v37, v40
	v_max_u32_e32 v40, v38, v34
	v_min_u32_e32 v34, v38, v34
	v_max_u32_e32 v38, v29, v35
	v_min_u32_e32 v29, v29, v35
	v_max_u32_e32 v35, v32, v39
	v_min_u32_e32 v32, v32, v39
	v_max_u32_e32 v39, v41, v36
	v_min_u32_e32 v36, v41, v36
	v_max_u32_e32 v41, v33, v30
	v_min_u32_e32 v30, v33, v30
	v_max_u32_e32 v33, v37, v34
	v_min_u32_e32 v34, v37, v34
	v_max_u32_e32 v37, v31, v40
	v_min_u32_e32 v31, v31, v40
	v_max_u32_e32 v40, v32, v28
	v_min_u32_e32 v28, v32, v28
	v_max_u32_e32 v32, v39, v34
	v_min_u32_e32 v34, v39, v34
	v_max_u32_e32 v39, v36, v33
	v_min_u32_e32 v33, v36, v33
	v_max_u32_e32 v36, v41, v31
	v_min_u32_e32 v31, v41, v31
	v_max_u32_e32 v41, v30, v37
	v_min_u32_e32 v30, v30, v37
	v_max_u32_e32 v37, v38, v32
	v_min_u32_e32 v32, v38, v32
	v_max_u32_e32 v38, v29, v39
	v_min_u32_e32 v29, v29, v39
	v_max_u32_e32 v39, v35, v36
	v_min_u32_e32 v35, v35, v36
	v_max_u32_e32 v36, v40, v41
	v_min_u32_e32 v40, v40, v41
	v_max_u32_e32 v41, v28, v30
	v_min_u32_e32 v28, v28, v30
	v_max_u32_e32 v30, v37, v39
	v_min_u32_e32 v37, v37, v39
	v_max_u32_e32 v39, v38, v36
	v_min_u32_e32 v36, v38, v36
	v_max_u32_e32 v38, v32, v35
	v_min_u32_e32 v32, v32, v35
	v_max_u32_e32 v35, v29, v40
	v_min_u32_e32 v29, v29, v40
	v_max_u32_e32 v40, v34, v31
	v_min_u32_e32 v31, v34, v31
	v_max_u32_e32 v34, v33, v41
	v_min_u32_e32 v33, v33, v41
	v_max_u32_e32 v41, v30, v39
	v_min_u32_e32 v30, v30, v39
	v_max_u32_e32 v39, v37, v36
	v_min_u32_e32 v36, v37, v36
	v_max_u32_e32 v37, v38, v35
	v_min_u32_e32 v35, v38, v35
	v_max_u32_e32 v38, v32, v29
	v_min_u32_e32 v29, v32, v29
	v_max_u32_e32 v32, v40, v34
	v_min_u32_e32 v34, v40, v34
	v_max_u32_e32 v40, v31, v33
	v_min_u32_e32 v31, v31, v33
	v_max_u32_dpp v33, v3, v41 quad_perm:[1,0,3,2] row_mask:0xf bank_mask:0xf bound_ctrl:1
	v_max_u32_dpp v42, v3, v30 quad_perm:[1,0,3,2] row_mask:0xf bank_mask:0xf bound_ctrl:1
	v_max_u32_dpp v43, v3, v39 quad_perm:[1,0,3,2] row_mask:0xf bank_mask:0xf bound_ctrl:1
	v_max_u32_dpp v44, v28, v36 quad_perm:[1,0,3,2] row_mask:0xf bank_mask:0xf bound_ctrl:1
	v_max_u32_dpp v45, v31, v37 quad_perm:[1,0,3,2] row_mask:0xf bank_mask:0xf bound_ctrl:1
	v_max_u32_dpp v46, v40, v35 quad_perm:[1,0,3,2] row_mask:0xf bank_mask:0xf bound_ctrl:1
	v_max_u32_dpp v47, v34, v38 quad_perm:[1,0,3,2] row_mask:0xf bank_mask:0xf bound_ctrl:1
	v_max_u32_dpp v48, v32, v29 quad_perm:[1,0,3,2] row_mask:0xf bank_mask:0xf bound_ctrl:1
	v_max_u32_dpp v29, v29, v32 quad_perm:[1,0,3,2] row_mask:0xf bank_mask:0xf bound_ctrl:1
	v_max_u32_dpp v32, v38, v34 quad_perm:[1,0,3,2] row_mask:0xf bank_mask:0xf bound_ctrl:1
	v_max_u32_dpp v34, v35, v40 quad_perm:[1,0,3,2] row_mask:0xf bank_mask:0xf bound_ctrl:1
	v_max_u32_dpp v31, v37, v31 quad_perm:[1,0,3,2] row_mask:0xf bank_mask:0xf bound_ctrl:1
	v_max_u32_dpp v28, v36, v28 quad_perm:[1,0,3,2] row_mask:0xf bank_mask:0xf bound_ctrl:1
	v_max_u32_e32 v35, v33, v29
	v_min_u32_e32 v29, v33, v29
	v_max_u32_e32 v33, v42, v32
	v_min_u32_e32 v32, v42, v32
	v_max_u32_e32 v36, v43, v34
	v_min_u32_e32 v34, v43, v34
	v_max_u32_e32 v37, v44, v31
	v_min_u32_e32 v31, v44, v31
	v_max_u32_e32 v38, v45, v28
	v_min_u32_e32 v28, v45, v28
	v_max_u32_dpp v40, v39, v46 quad_perm:[1,0,3,2] row_mask:0xf bank_mask:0xf bound_ctrl:1
	v_min_u32_dpp v39, v39, v46 quad_perm:[1,0,3,2] row_mask:0xf bank_mask:0xf bound_ctrl:1
	v_max_u32_dpp v42, v30, v47 quad_perm:[1,0,3,2] row_mask:0xf bank_mask:0xf bound_ctrl:1
	v_min_u32_dpp v30, v30, v47 quad_perm:[1,0,3,2] row_mask:0xf bank_mask:0xf bound_ctrl:1
	v_max_u32_dpp v43, v41, v48 quad_perm:[1,0,3,2] row_mask:0xf bank_mask:0xf bound_ctrl:1
	v_min_u32_dpp v41, v41, v48 quad_perm:[1,0,3,2] row_mask:0xf bank_mask:0xf bound_ctrl:1
	v_max_u32_e32 v44, v35, v38
	v_min_u32_e32 v35, v35, v38
	v_max_u32_e32 v38, v33, v40
	v_min_u32_e32 v33, v33, v40
	v_max_u32_e32 v40, v36, v42
	v_min_u32_e32 v36, v36, v42
	v_max_u32_e32 v42, v37, v43
	v_min_u32_e32 v37, v37, v43
	v_max_u32_e32 v43, v29, v28
	v_min_u32_e32 v28, v29, v28
	v_max_u32_e32 v29, v32, v39
	v_min_u32_e32 v32, v32, v39
	v_max_u32_e32 v39, v34, v30
	v_min_u32_e32 v30, v34, v30
	v_max_u32_e32 v34, v31, v41
	v_min_u32_e32 v31, v31, v41
	v_max_u32_e32 v41, v44, v40
	v_min_u32_e32 v40, v44, v40
	v_max_u32_e32 v44, v38, v42
	v_min_u32_e32 v38, v38, v42
	v_max_u32_e32 v42, v35, v36
	v_min_u32_e32 v35, v35, v36
	v_max_u32_e32 v36, v33, v37
	v_min_u32_e32 v33, v33, v37
	v_max_u32_e32 v37, v43, v39
	v_min_u32_e32 v39, v43, v39
	v_max_u32_e32 v43, v29, v34
	v_min_u32_e32 v29, v29, v34
	v_max_u32_e32 v34, v28, v30
	v_min_u32_e32 v28, v28, v30
	v_max_u32_e32 v30, v32, v31
	v_min_u32_e32 v31, v32, v31
	v_max_u32_e32 v45, v41, v44
	v_min_u32_e32 v44, v41, v44
	v_max_u32_e32 v46, v40, v38
	v_min_u32_e32 v47, v40, v38
	v_max_u32_e32 v41, v42, v36
	v_min_u32_e32 v40, v42, v36
	v_max_u32_e32 v42, v35, v33
	v_min_u32_e32 v38, v35, v33
	v_max_u32_e32 v48, v37, v43
	v_min_u32_e32 v43, v37, v43
	v_max_u32_e32 v49, v39, v29
	v_min_u32_e32 v29, v39, v29
	v_max_u32_e32 v50, v34, v30
	v_min_u32_e32 v51, v34, v30
	v_max_u32_e32 v52, v28, v31
	v_min_u32_e32 v28, v28, v31
	v_max_u32_dpp v32, v51, v46 quad_perm:[2,3,0,1] row_mask:0xf bank_mask:0xf bound_ctrl:1
	v_max_u32_dpp v31, v52, v44 quad_perm:[2,3,0,1] row_mask:0xf bank_mask:0xf bound_ctrl:1
	v_max_u32_dpp v30, v28, v45 quad_perm:[2,3,0,1] row_mask:0xf bank_mask:0xf bound_ctrl:1
	v_max_u32_dpp v33, v50, v47 quad_perm:[2,3,0,1] row_mask:0xf bank_mask:0xf bound_ctrl:1
	v_max_u32_dpp v34, v29, v41 quad_perm:[2,3,0,1] row_mask:0xf bank_mask:0xf bound_ctrl:1
	v_max_u32_dpp v35, v49, v40 quad_perm:[2,3,0,1] row_mask:0xf bank_mask:0xf bound_ctrl:1
	v_max_u32_dpp v36, v43, v42 quad_perm:[2,3,0,1] row_mask:0xf bank_mask:0xf bound_ctrl:1
	v_max_u32_dpp v37, v48, v38 quad_perm:[2,3,0,1] row_mask:0xf bank_mask:0xf bound_ctrl:1
	v_max_u32_dpp v38, v38, v48 quad_perm:[2,3,0,1] row_mask:0xf bank_mask:0xf bound_ctrl:1
	v_max_u32_dpp v39, v42, v43 quad_perm:[2,3,0,1] row_mask:0xf bank_mask:0xf bound_ctrl:1
	v_max_u32_dpp v40, v40, v49 quad_perm:[2,3,0,1] row_mask:0xf bank_mask:0xf bound_ctrl:1
	v_max_u32_dpp v41, v41, v29 quad_perm:[2,3,0,1] row_mask:0xf bank_mask:0xf bound_ctrl:1
	v_max_u32_dpp v42, v47, v50 quad_perm:[2,3,0,1] row_mask:0xf bank_mask:0xf bound_ctrl:1
	v_max_u32_dpp v43, v46, v51 quad_perm:[2,3,0,1] row_mask:0xf bank_mask:0xf bound_ctrl:1
	v_max_u32_dpp v44, v44, v52 quad_perm:[2,3,0,1] row_mask:0xf bank_mask:0xf bound_ctrl:1
	v_max_u32_dpp v45, v45, v28 quad_perm:[2,3,0,1] row_mask:0xf bank_mask:0xf bound_ctrl:1
	v_max_u32_e32 v29, v30, v38
	v_max_u32_e32 v46, v31, v39
	v_max_u32_e32 v47, v32, v40
	v_max_u32_e32 v48, v33, v41
	v_max_u32_e32 v49, v34, v42
	v_max_u32_e32 v50, v35, v43
	v_max_u32_e32 v51, v36, v44
	v_max_u32_e32 v52, v37, v45
	v_max_u32_e32 v54, v29, v49
	v_max_u32_e32 v55, v46, v50
	v_max_u32_e32 v57, v47, v51
	v_max_u32_e32 v58, v48, v52
	v_max_u32_e32 v53, v54, v57
	v_max_u32_e32 v56, v55, v58
	s_and_saveexec_b64 s[8:9], s[48:49]
	s_xor_b64 s[8:9], exec, s[8:9]
	s_cbranch_execz .LBB0_733
	v_min_u32_e32 v28, v53, v56
	v_cmp_lt_i32_e32 vcc, 1, v182
	s_and_saveexec_b64 s[50:51], vcc
	s_cbranch_execz .LBB0_732
	v_min_u32_e32 v53, v54, v57
	v_min_u32_e32 v54, v55, v58
	v_cmp_ne_u32_e32 vcc, 2, v182
	s_and_saveexec_b64 s[52:53], vcc
	s_xor_b64 s[52:53], exec, s[52:53]
	v_min_u32_e32 v28, v53, v54
	s_andn2_saveexec_b64 s[52:53], s[52:53]
	v_max_u32_e32 v28, v53, v54
	s_or_b64 exec, exec, s[52:53]

.LBB0_759:
	s_or_b64 exec, exec, s[8:9]
	v_bitop3_b32 v32, v28, 63, v28 bitop3:0xc
	v_bitop3_b32 v33, v29, 63, v29 bitop3:0xc
	v_bitop3_b32 v34, v30, 63, v30 bitop3:0xc
	v_bitop3_b32 v35, v31, 63, v31 bitop3:0xc
	v_lshl_add_u32 v32, v32, 1, 0
	v_lshl_add_u32 v33, v33, 1, 0
	v_lshl_add_u32 v34, v34, 1, 0
	v_lshl_add_u32 v35, v35, 1, 0
	ds_read_u16 v32, v32 offset:40960
	ds_read_u16 v33, v33 offset:40960
	ds_read_u16 v34, v34 offset:40960
	ds_read_u16 v35, v35 offset:40960
	v_cmp_lt_i32_e32 vcc, -1, v28
	s_movk_i32 s6, 0x800
	s_waitcnt lgkmcnt(2)
	v_add_u32_sdwa v37, v231, v33 dst_sel:DWORD dst_unused:UNUSED_PAD src0_sel:DWORD src1_sel:BYTE_0
	v_add_u32_sdwa v36, v231, v32 dst_sel:DWORD dst_unused:UNUSED_PAD src0_sel:DWORD src1_sel:BYTE_0
	v_lshrrev_b32_e32 v32, 8, v32
	v_lshrrev_b32_e32 v33, 8, v33
	s_waitcnt lgkmcnt(1)
	v_add_u32_sdwa v38, v231, v34 dst_sel:DWORD dst_unused:UNUSED_PAD src0_sel:DWORD src1_sel:BYTE_0
	v_lshrrev_b32_e32 v34, 8, v34
	s_waitcnt lgkmcnt(0)
	v_add_u32_sdwa v39, v231, v35 dst_sel:DWORD dst_unused:UNUSED_PAD src0_sel:DWORD src1_sel:BYTE_0
	v_lshrrev_b32_e32 v35, 8, v35
	v_add_u32_e32 v32, v231, v32
	v_add_u32_e32 v33, v231, v33
	v_add_u32_e32 v34, v231, v34
	v_add_u32_e64 v35, v231, v35
	ds_read_b32 v36, v36
	ds_read_b32 v32, v32 offset:64
	ds_read_b32 v37, v37
	ds_read_b32 v33, v33 offset:64
	ds_read_b32 v38, v38
	ds_read_b32 v34, v34 offset:64
	ds_read_b32 v39, v39
	ds_read_b32 v35, v35 offset:64
	s_waitcnt lgkmcnt(7)
	v_lshlrev_b32_e32 v36, 7, v36
	v_and_b32_e32 v36, 0x3f80, v36
	s_waitcnt lgkmcnt(6)
	v_and_b32_e32 v32, 0x7f, v32
	v_bitop3_b32 v32, v32, s38, v36 bitop3:0x36
	v_cndmask_b32_e64 v36, v218, -1, vcc
	v_bitop3_b32 v28, v36, v28, s78 bitop3:0x78
	s_waitcnt lgkmcnt(5)
	v_lshlrev_b32_e64 v36, 7, v37
	v_and_b32_e32 v36, 0x3f80, v36
	s_waitcnt lgkmcnt(4)
	v_and_b32_e32 v33, 0x7f, v33
	v_cmp_lt_i32_e32 vcc, -1, v29
	v_bitop3_b32 v33, v33, s38, v36 bitop3:0x36
	s_waitcnt lgkmcnt(2)
	v_and_b32_e32 v34, 0x7f, v34
	v_cndmask_b32_e64 v36, v218, -1, vcc
	v_bitop3_b32 v29, v36, v29, s78 bitop3:0x78
	v_lshlrev_b32_e32 v36, 7, v38
	v_and_b32_e32 v36, 0x3f80, v36
	v_cmp_lt_i32_e32 vcc, -1, v30
	v_bitop3_b32 v34, v34, s38, v36 bitop3:0x36
	v_subrev_f32_dpp v29, v28, v29 quad_perm:[0,0,0,0] row_mask:0xf bank_mask:0xf bound_ctrl:1
	v_cndmask_b32_e64 v36, v218, -1, vcc
	v_cmp_lt_i32_e32 vcc, -1, v31
	v_bitop3_b32 v30, v36, v30, s78 bitop3:0x78
	v_mul_f32_e32 v29, 0x3fb8aa3b, v29
	v_cndmask_b32_e64 v37, v218, -1, vcc
	v_bitop3_b32 v31, v37, v31, s78 bitop3:0x78
	v_subrev_f32_dpp v30, v28, v30 quad_perm:[0,0,0,0] row_mask:0xf bank_mask:0xf bound_ctrl:1
	v_subrev_f32_dpp v37, v28, v28 quad_perm:[0,0,0,0] row_mask:0xf bank_mask:0xf bound_ctrl:1
	v_mul_f32_e32 v37, 0x3fb8aa3b, v37
	v_exp_f32_e32 v37, v37
	v_exp_f32_e32 v29, v29
	v_mul_f32_e32 v30, 0x3fb8aa3b, v30
	v_subrev_f32_dpp v28, v28, v31 quad_perm:[0,0,0,0] row_mask:0xf bank_mask:0xf bound_ctrl:1
	v_exp_f32_e64 v30, v30
	v_mul_f32_e32 v28, 0x3fb8aa3b, v28
	v_exp_f32_e32 v28, v28
	v_add_f32_e32 v31, 0, v37
	v_add_f32_e32 v31, v29, v31
	v_add_f32_e32 v31, v30, v31
	v_add_f32_e32 v31, v28, v31
	s_waitcnt lgkmcnt(1)
	v_lshlrev_b32_e64 v36, 7, v39
	v_and_b32_e32 v36, 0x3f80, v36
	v_add_f32_dpp v31, v31, v31 quad_perm:[1,0,3,2] row_mask:0xf bank_mask:0xf bound_ctrl:1
	s_waitcnt lgkmcnt(0)
	v_and_b32_e32 v35, 0x7f, v35
	v_bitop3_b32 v35, v35, s38, v36 bitop3:0x36
	v_add_f32_dpp v31, v31, v31 quad_perm:[2,3,0,1] row_mask:0xf bank_mask:0xf bound_ctrl:1
	v_div_scale_f32 v38, s[8:9], v31, v31, 1.0
	v_rcp_f32_e32 v39, v38
	s_nop 0
	v_fma_f32 v36, -v38, v39, 1.0
	v_fmac_f32_e32 v39, v36, v39
	v_div_scale_f32 v36, vcc, 1.0, v31, 1.0
	v_mul_f32_e64 v40, v36, v39
	v_fma_f32 v41, -v38, v40, v36
	v_fmac_f32_e32 v40, v41, v39
	v_fma_f32 v36, -v38, v40, v36
	v_div_fmas_f32 v36, v36, v39, v40
	v_div_fixup_f32 v31, v36, v31, 1.0
	v_mul_f32_e32 v36, v37, v31
	v_mul_f32_e64 v29, v29, v31
	v_add_u32_e32 v37, 0xc00, v245
	ds_write2_b32 v37, v36, v29 offset0:192 offset1:196
	ds_write2_b32 v37, v32, v33 offset0:64 offset1:68
	v_mul_f32_e32 v29, v30, v31
	v_mul_f32_e32 v28, v28, v31
	ds_write2_b32 v37, v29, v28 offset0:200 offset1:204
	ds_write2_b32 v37, v34, v35 offset0:72 offset1:76
	s_waitcnt lgkmcnt(0)
	ds_read2st64_b32 v[28:29], v177 offset0:13 offset1:14
	ds_read2st64_b32 v[30:31], v177 offset0:15 offset1:16
	v_mov_b32_e32 v32, 0
	s_waitcnt lgkmcnt(1)
	v_cmp_gt_u32_e64 s[50:51], s6, v28
	v_cmp_gt_u32_e32 vcc, s6, v29
	s_and_saveexec_b64 s[8:9], s[50:51]
	v_mbcnt_lo_u32_b32 v32, s50, 0
	v_mbcnt_hi_u32_b32 v32, s51, v32
	s_or_b64 exec, exec, s[8:9]
	v_ashrrev_i32_e64 v33, 11, v28
	v_ashrrev_i32_e32 v34, 11, v29
	s_bcnt1_i32_b64 s6, s[50:51]
	s_bcnt1_i32_b64 s76, vcc
	s_add_i32 s76, s76, s6
	v_cmp_eq_u32_e64 s[52:53], 1, v33
	v_cmp_eq_u32_e64 s[50:51], 1, v34
	s_and_saveexec_b64 s[8:9], s[52:53]
	v_mbcnt_lo_u32_b32 v32, s52, 0
	v_mbcnt_hi_u32_b32 v32, s53, v32
	v_add_u32_e32 v32, s76, v32
	s_or_b64 exec, exec, s[8:9]
	s_bcnt1_i32_b64 s8, s[52:53]
	s_bcnt1_i32_b64 s9, s[50:51]
	s_add_i32 s76, s76, s8
	s_add_i32 s80, s76, s9
	v_cmp_eq_u32_e64 s[54:55], 2, v33
	v_cmp_eq_u32_e64 s[52:53], 2, v34
	s_and_saveexec_b64 s[8:9], s[54:55]
	v_mbcnt_lo_u32_b32 v32, s54, 0
	v_mbcnt_hi_u32_b32 v32, s55, v32
	v_add_u32_e32 v32, s80, v32
	s_or_b64 exec, exec, s[8:9]
	s_bcnt1_i32_b64 s8, s[54:55]
	s_bcnt1_i32_b64 s9, s[52:53]
	s_add_i32 s80, s80, s8
	s_add_i32 s81, s80, s9
	v_cmp_eq_u32_e64 s[56:57], 3, v33
	v_cmp_eq_u32_e64 s[54:55], 3, v34
	s_and_saveexec_b64 s[8:9], s[56:57]
	v_mbcnt_lo_u32_b32 v32, s56, 0
	v_mbcnt_hi_u32_b32 v32, s57, v32
	v_add_u32_e32 v32, s81, v32
	s_or_b64 exec, exec, s[8:9]
	s_bcnt1_i32_b64 s8, s[56:57]
	s_bcnt1_i32_b64 s9, s[54:55]
	s_add_i32 s81, s81, s8
	s_add_i32 s82, s81, s9
	v_cmp_eq_u32_e64 s[58:59], 4, v33
	v_cmp_eq_u32_e64 s[56:57], 4, v34
	s_and_saveexec_b64 s[8:9], s[58:59]
	v_mbcnt_lo_u32_b32 v32, s58, 0
	v_mbcnt_hi_u32_b32 v32, s59, v32
	v_add_u32_e32 v32, s82, v32
	s_or_b64 exec, exec, s[8:9]
	s_bcnt1_i32_b64 s8, s[58:59]
	s_bcnt1_i32_b64 s9, s[56:57]
	s_add_i32 s82, s82, s8
	s_add_i32 s84, s82, s9
	v_cmp_eq_u32_e64 s[60:61], 5, v33
	v_cmp_eq_u32_e64 s[58:59], 5, v34
	s_and_saveexec_b64 s[8:9], s[60:61]
	v_mbcnt_lo_u32_b32 v32, s60, 0
	v_mbcnt_hi_u32_b32 v32, s61, v32
	v_add_u32_e32 v32, s84, v32
	s_or_b64 exec, exec, s[8:9]
	s_bcnt1_i32_b64 s8, s[60:61]
	s_bcnt1_i32_b64 s9, s[58:59]
	s_add_i32 s84, s84, s8
	s_add_i32 s85, s84, s9
	v_cmp_eq_u32_e64 s[62:63], 6, v33
	v_cmp_eq_u32_e64 s[60:61], 6, v34
	s_and_saveexec_b64 s[8:9], s[62:63]
	v_mbcnt_lo_u32_b32 v32, s62, 0
	v_mbcnt_hi_u32_b32 v32, s63, v32
	v_add_u32_e32 v32, s85, v32
	s_or_b64 exec, exec, s[8:9]
	s_bcnt1_i32_b64 s8, s[62:63]
	s_bcnt1_i32_b64 s9, s[60:61]
	s_add_i32 s85, s85, s8
	s_add_i32 s83, s85, s9
	v_cmp_eq_u32_e64 s[64:65], 7, v33
	v_cmp_eq_u32_e64 s[62:63], 7, v34
	s_and_saveexec_b64 s[8:9], s[64:65]
	v_mbcnt_lo_u32_b32 v32, s64, 0
	v_mbcnt_hi_u32_b32 v32, s65, v32
	v_add_u32_e32 v32, s83, v32
	s_or_b64 exec, exec, s[8:9]
	v_mbcnt_lo_u32_b32 v40, vcc_lo, 0
	v_mbcnt_lo_u32_b32 v39, s50, 0
	v_mbcnt_hi_u32_b32 v40, vcc_hi, v40
	v_mbcnt_lo_u32_b32 v38, s52, 0
	v_mbcnt_hi_u32_b32 v39, s51, v39
	v_add_u32_e32 v40, s6, v40
	v_mbcnt_lo_u32_b32 v37, s54, 0
	v_mbcnt_hi_u32_b32 v38, s53, v38
	v_add_u32_e32 v39, s76, v39
	v_cndmask_b32_e32 v40, 0, v40, vcc
	v_mbcnt_lo_u32_b32 v36, s56, 0
	v_mbcnt_hi_u32_b32 v37, s55, v37
	v_add_u32_e64 v38, s80, v38
	v_cndmask_b32_e64 v39, v40, v39, s[50:51]
	v_mbcnt_lo_u32_b32 v35, s58, 0
	v_mbcnt_hi_u32_b32 v36, s57, v36
	v_add_u32_e64 v37, s81, v37
	v_cndmask_b32_e64 v38, v39, v38, s[52:53]
	v_mbcnt_lo_u32_b32 v34, s60, 0
	v_mbcnt_hi_u32_b32 v35, s59, v35
	v_add_u32_e64 v36, s82, v36
	v_cndmask_b32_e64 v37, v38, v37, s[54:55]
	v_mbcnt_lo_u32_b32 v33, s62, 0
	s_bcnt1_i32_b64 s8, s[64:65]
	v_mbcnt_hi_u32_b32 v34, s61, v34
	v_add_u32_e32 v35, s84, v35
	v_cndmask_b32_e64 v36, v37, v36, s[56:57]
	v_mbcnt_hi_u32_b32 v33, s63, v33
	v_add_u32_e64 v34, s85, v34
	v_cndmask_b32_e64 v35, v36, v35, s[58:59]
	s_add_i32 s83, s83, s8
	v_cndmask_b32_e64 v34, v35, v34, s[60:61]
	v_add_u32_e32 v33, s83, v33
	v_cndmask_b32_e64 v33, v34, v33, s[62:63]
	v_lshl_add_u32 v32, v32, 2, s27
	s_waitcnt lgkmcnt(0)
	ds_write2st64_b32 v32, v28, v30 offset0:13 offset1:15
	v_lshl_add_u32 v28, v33, 2, s27
	v_mov_b32_e32 v34, s27
	ds_write2st64_b32 v28, v29, v31 offset0:13 offset1:15
	s_waitcnt lgkmcnt(0)
	ds_read_b128 v[28:31], v34 offset:3328
	ds_read_b128 v[32:35], v34 offset:3344
	v_mov_b32_e32 v152, 0
	s_mov_b32 s6, -12
	v_mov_b32_e32 v153, v152
	s_waitcnt lgkmcnt(1)
	v_readfirstlane_b32 s8, v28
	s_ashr_i32 s9, s8, 31
	s_lshl_b64 s[8:9], s[8:9], 10
	v_lshl_add_u64 v[36:37], v[124:125], 0, s[8:9]
	v_lshl_add_u64 v[38:39], v[126:127], 0, s[8:9]
	v_readfirstlane_b32 s8, v29
	s_ashr_i32 s9, s8, 31
	s_lshl_b64 s[8:9], s[8:9], 10
	global_load_dwordx4 v[88:91], v[36:37], off
	global_load_dwordx4 v[56:59], v[38:39], off
	v_lshl_add_u64 v[28:29], v[124:125], 0, s[8:9]
	v_lshl_add_u64 v[36:37], v[126:127], 0, s[8:9]
	v_readfirstlane_b32 s8, v30
	s_ashr_i32 s9, s8, 31
	s_lshl_b64 s[8:9], s[8:9], 10
	global_load_dwordx4 v[84:87], v[28:29], off
	global_load_dwordx4 v[52:55], v[36:37], off
	v_lshl_add_u64 v[28:29], v[124:125], 0, s[8:9]
	v_lshl_add_u64 v[36:37], v[126:127], 0, s[8:9]
	global_load_dwordx4 v[80:83], v[28:29], off
	global_load_dwordx4 v[44:47], v[36:37], off
	v_add_u32_e32 v28, 0xc00, v184
	ds_read2_b32 v[28:29], v28 offset0:64 offset1:68
	v_readfirstlane_b32 s8, v31
	s_ashr_i32 s9, s8, 31
	s_lshl_b64 s[8:9], s[8:9], 10
	v_lshl_add_u64 v[30:31], v[124:125], 0, s[8:9]
	v_lshl_add_u64 v[36:37], v[126:127], 0, s[8:9]
	global_load_dwordx4 v[76:79], v[30:31], off
	s_nop 0
	global_load_dwordx4 v[36:39], v[36:37], off
	s_waitcnt lgkmcnt(0)
	v_lshlrev_b32_e32 v30, 1, v28
	v_readfirstlane_b32 s8, v32
	v_ashrrev_i32_e32 v31, 31, v30
	s_ashr_i32 s9, s8, 31
	v_lshl_add_u64 v[30:31], v[30:31], 2, s[4:5]
	s_lshl_b64 s[8:9], s[8:9], 10
	v_lshl_add_u64 v[40:41], v[124:125], 0, s[8:9]
	global_load_dwordx2 v[140:141], v[30:31], off
	global_load_dwordx4 v[72:75], v[40:41], off
	v_lshl_add_u64 v[30:31], v[126:127], 0, s[8:9]
	v_readfirstlane_b32 s8, v33
	s_ashr_i32 s9, s8, 31
	s_lshl_b64 s[8:9], s[8:9], 10
	v_lshl_add_u64 v[32:33], v[124:125], 0, s[8:9]
	global_load_dwordx4 v[48:51], v[30:31], off
	global_load_dwordx4 v[68:71], v[32:33], off
	v_lshl_add_u64 v[30:31], v[126:127], 0, s[8:9]
	v_readfirstlane_b32 s8, v34
	s_ashr_i32 s9, s8, 31
	s_lshl_b64 s[8:9], s[8:9], 10
	v_lshl_add_u64 v[32:33], v[124:125], 0, s[8:9]
	global_load_dwordx4 v[40:43], v[30:31], off
	global_load_dwordx4 v[64:67], v[32:33], off
	v_lshl_add_u64 v[30:31], v[126:127], 0, s[8:9]
	v_readfirstlane_b32 s8, v35
	s_ashr_i32 s9, s8, 31
	s_lshl_b64 s[8:9], s[8:9], 10
	v_lshl_add_u64 v[60:61], v[124:125], 0, s[8:9]
	v_lshlrev_b32_e32 v28, 1, v29
	global_load_dwordx4 v[32:35], v[30:31], off
	s_nop 0
	global_load_dwordx4 v[60:63], v[60:61], off
	v_lshl_add_u64 v[30:31], v[126:127], 0, s[8:9]
	v_ashrrev_i32_e32 v29, 31, v28
	v_lshl_add_u64 v[92:93], v[28:29], 2, s[4:5]
	global_load_dwordx4 v[28:31], v[30:31], off
	s_nop 0
	global_load_dwordx2 v[138:139], v[92:93], off
	s_mov_b32 s8, s72
	v_mov_b32_e32 v174, v152
	v_mov_b32_e32 v175, v152
	v_mov_b32_e32 v172, v152
	v_mov_b32_e32 v173, v152
	v_mov_b32_e32 v170, v152
	v_mov_b32_e32 v171, v152
	v_mov_b32_e32 v168, v152
	v_mov_b32_e32 v169, v152
	v_mov_b32_e32 v166, v152
	v_mov_b32_e32 v167, v152
	v_mov_b32_e32 v164, v152
	v_mov_b32_e32 v165, v152
	v_mov_b32_e32 v162, v152
	v_mov_b32_e32 v163, v152
	v_mov_b32_e32 v160, v152
	v_mov_b32_e32 v161, v152
	v_mov_b32_e32 v158, v152
	v_mov_b32_e32 v159, v152
	v_mov_b32_e32 v156, v152
	v_mov_b32_e32 v157, v152
	v_mov_b32_e32 v154, v152
	v_mov_b32_e32 v155, v152
	v_mov_b32_e32 v150, v152
	v_mov_b32_e32 v151, v152
	v_mov_b32_e32 v148, v152
	v_mov_b32_e32 v149, v152
	v_mov_b32_e32 v146, v152
	v_mov_b32_e32 v147, v152
	v_mov_b32_e32 v144, v152
	v_mov_b32_e32 v145, v152
.LBB0_776:
	v_mov_b32_e64 v250, s8
	ds_read_b128 v[92:95], v250
	v_add_u32_e64 v249, s8, v183
	ds_read_b32 v142, v249
	v_mov_b32_e32 v251, 0
	v_mov_b32_e32 v252, 0
	s_waitcnt lgkmcnt(1)
	v_readfirstlane_b32 s50, v92
	s_ashr_i32 s51, s50, 31
	s_lshl_b64 s[50:51], s[50:51], 10
	v_lshl_add_u64 v[96:97], v[124:125], 0, s[50:51]
	v_lshl_add_u64 v[98:99], v[126:127], 0, s[50:51]
	v_readfirstlane_b32 s50, v93
	s_ashr_i32 s51, s50, 31
	s_lshl_b64 s[50:51], s[50:51], 10
	global_load_dwordx4 v[120:123], v[96:97], off
	global_load_dwordx4 v[104:107], v[98:99], off
	v_lshl_add_u64 v[92:93], v[124:125], 0, s[50:51]
	v_lshl_add_u64 v[96:97], v[126:127], 0, s[50:51]
	v_readfirstlane_b32 s50, v94
	s_ashr_i32 s51, s50, 31
	s_lshl_b64 s[50:51], s[50:51], 10
	global_load_dwordx4 v[116:119], v[92:93], off
	global_load_dwordx4 v[100:103], v[96:97], off
	v_lshl_add_u64 v[92:93], v[124:125], 0, s[50:51]
	v_lshl_add_u64 v[96:97], v[126:127], 0, s[50:51]
	v_readfirstlane_b32 s50, v95
	s_ashr_i32 s51, s50, 31
	s_lshl_b64 s[50:51], s[50:51], 10
	s_waitcnt lgkmcnt(0)
	v_lshlrev_b32_e64 v142, 1, v142
	global_load_dwordx4 v[112:115], v[92:93], off
	s_nop 0
	global_load_dwordx4 v[96:99], v[96:97], off
	v_lshl_add_u64 v[92:93], v[124:125], 0, s[50:51]
	v_lshl_add_u64 v[94:95], v[126:127], 0, s[50:51]
	v_ashrrev_i32_e32 v143, 31, v142
	global_load_dwordx4 v[108:111], v[92:93], off
	s_nop 0
	global_load_dwordx4 v[92:95], v[94:95], off
	v_lshl_add_u64 v[142:143], v[142:143], 2, s[4:5]
	global_load_dwordx2 v[142:143], v[142:143], off
	s_waitcnt vmcnt(26)
	v_dot8c_i32_i4_e32 v251, v88, v24
	v_dot8c_i32_i4_e32 v252, v88, v20
	v_dot8c_i32_i4_e32 v251, v89, v25
	v_dot8c_i32_i4_e32 v252, v89, v21
	v_dot8c_i32_i4_e32 v251, v90, v26
	v_dot8c_i32_i4_e32 v252, v90, v22
	v_mov_b32_e32 v89, 0
	v_mov_b32_e32 v90, 0
	s_waitcnt vmcnt(24)
	v_dot8c_i32_i4_e32 v89, v84, v24
	v_dot8c_i32_i4_e32 v90, v84, v20
	v_dot8c_i32_i4_e32 v89, v85, v25
	v_dot8c_i32_i4_e32 v90, v85, v21
	v_dot8c_i32_i4_e32 v89, v86, v26
	v_dot8c_i32_i4_e32 v90, v86, v22
	v_mov_b32_e32 v85, 0
	v_mov_b32_e32 v86, 0
	s_waitcnt vmcnt(21)
	v_dot8c_i32_i4_e32 v85, v80, v24
	v_dot8c_i32_i4_e32 v86, v80, v20
	v_dot8c_i32_i4_e32 v85, v81, v25
	v_dot8c_i32_i4_e32 v86, v81, v21
	v_dot8c_i32_i4_e32 v85, v82, v26
	v_dot8c_i32_i4_e32 v86, v82, v22
	v_mov_b32_e64 v81, 0
	v_mov_b32_e32 v82, 0
	s_waitcnt vmcnt(19)
	v_dot8c_i32_i4_e32 v81, v76, v24
	v_dot8c_i32_i4_e32 v82, v76, v20
	v_dot8c_i32_i4_e32 v81, v77, v25
	v_dot8c_i32_i4_e32 v82, v77, v21
	v_dot8c_i32_i4_e32 v251, v91, v27
	v_dot8c_i32_i4_e32 v252, v91, v23
	v_dot8c_i32_i4_e32 v89, v87, v27
	v_dot8c_i32_i4_e32 v90, v87, v23
	v_dot8c_i32_i4_e32 v81, v78, v26
	v_dot8c_i32_i4_e32 v82, v78, v22
	v_lshl_add_u32 v88, v251, 4, v252
	v_lshl_add_u32 v84, v89, 4, v90
	v_dot8c_i32_i4_e32 v85, v83, v27
	v_dot8c_i32_i4_e32 v86, v83, v23
	v_dot8c_i32_i4_e32 v81, v79, v27
	v_dot8c_i32_i4_e32 v82, v79, v23
	v_cvt_f32_i32_e32 v88, v88
	v_cvt_f32_i32_e32 v84, v84
	v_lshl_add_u32 v80, v85, 4, v86
	v_lshl_add_u32 v76, v81, 4, v82
	v_cvt_f32_i32_e32 v80, v80
	v_cvt_f32_i32_e32 v76, v76
	v_cndmask_b32_e64 v77, v84, v88, s[42:43]
	v_cndmask_b32_e64 v78, v88, v84, s[42:43]
	s_nop 1
	v_add_f32_dpp v77, v78, v77 quad_perm:[1,0,3,2] row_mask:0xf bank_mask:0xf bound_ctrl:1
	v_cndmask_b32_e64 v78, v76, v80, s[42:43]
	v_cndmask_b32_e64 v76, v80, v76, s[42:43]
	s_nop 1
	v_add_f32_dpp v76, v76, v78 quad_perm:[1,0,3,2] row_mask:0xf bank_mask:0xf bound_ctrl:1
	v_cndmask_b32_e64 v78, v76, v77, s[44:45]
	v_cndmask_b32_e64 v76, v77, v76, s[44:45]
	s_nop 1
	v_add_f32_dpp v76, v76, v78 quad_perm:[2,3,0,1] row_mask:0xf bank_mask:0xf bound_ctrl:1
	s_nop 1
	v_add_f32_dpp v76, v76, v76 row_ror:4 row_mask:0xf bank_mask:0xf bound_ctrl:1
	s_nop 1
	v_add_f32_dpp v76, v76, v76 row_ror:8 row_mask:0xf bank_mask:0xf bound_ctrl:1
	v_mov_b32_e32 v77, v76
	s_nop 1
	v_permlane32_swap_b32_e32 v76, v77
	v_add_f32_e32 v76, v76, v77
	v_mov_b32_e32 v77, v76
	s_nop 1
	v_permlane16_swap_b32_e32 v76, v77
	v_add_f32_e32 v76, v76, v77
	s_waitcnt vmcnt(18)
	v_mul_f32_e32 v77, v248, v140
	v_mul_f32_e32 v76, v77, v76
	v_fma_f32 v77, |v76|, s39, 1.0
	v_rcp_f32_e32 v77, v77
	v_mul_f32_e32 v80, v76, v76
	v_mul_f32_e32 v80, 0xbf38aa3b, v80
	v_exp_f32_e64 v80, v80
	v_fmamk_f32 v79, v77, 0x3f07dc22, v210
	v_fmaak_f32 v79, v77, v79, 0x3f35f0e3
	v_fmaak_f32 v79, v77, v79, 0xbe11a98e
	ds_read_b32 v78, v249 offset:480
	v_fmaak_f32 v79, v77, v79, 0x3e027906
	v_mul_f32_e32 v77, v77, v79
	v_mul_f32_e32 v77, v80, v77
	v_mul_f32_e64 v79, v76, v77
	v_fma_f32 v77, -v76, v77, v76
	v_cmp_gt_f32_e32 vcc, 0, v76
	s_nop 1
	v_cndmask_b32_e32 v76, v77, v79, vcc
	s_waitcnt lgkmcnt(0)
	v_mul_f32_e64 v76, v78, v76
	v_mul_f32_e32 v251, v141, v76
	s_nop 0
	v_readlane_b32 s50, v251, 0
	v_cvt_scalef32_pk_f32_fp4 v[76:77], v56, 1.0
	v_cvt_scalef32_pk_f32_fp4 v[78:79], v56, 1.0 op_sel:[1,0,0]
	v_cvt_scalef32_pk_f32_fp4 v[80:81], v56, 1.0 op_sel:[0,1,0]
	v_cvt_scalef32_pk_f32_fp4 v[82:83], v56, 1.0 op_sel:[1,1,0]
	v_pk_fma_f32 v[76:77], v[76:77], s[50:51], v[152:153] op_sel_hi:[1,0,1]
	v_cvt_scalef32_pk_f32_fp4 v[84:85], v57, 1.0
	v_cvt_scalef32_pk_f32_fp4 v[86:87], v57, 1.0 op_sel:[1,0,0]
	v_cvt_scalef32_pk_f32_fp4 v[88:89], v57, 1.0 op_sel:[0,1,0]
	v_cvt_scalef32_pk_f32_fp4 v[56:57], v57, 1.0 op_sel:[1,1,0]
	v_cvt_scalef32_pk_f32_fp4 v[90:91], v58, 1.0
	v_cvt_scalef32_pk_f32_fp4 v[140:141], v58, 1.0 op_sel:[1,0,0]
	v_cvt_scalef32_pk_f32_fp4 v[152:153], v58, 1.0 op_sel:[0,1,0]
	v_pk_fma_f32 v[56:57], v[56:57], s[50:51], v[162:163] op_sel_hi:[1,0,1]
	v_cvt_scalef32_pk_f32_fp4 v[162:163], v58, 1.0 op_sel:[1,1,0]
	v_pk_fma_f32 v[90:91], v[90:91], s[50:51], v[160:161] op_sel_hi:[1,0,1]
	v_pk_fma_f32 v[140:141], v[140:141], s[50:51], v[158:159] op_sel_hi:[1,0,1]
	v_pk_fma_f32 v[152:153], v[152:153], s[50:51], v[156:157] op_sel_hi:[1,0,1]
	v_cvt_scalef32_pk_f32_fp4 v[156:157], v59, 1.0
	v_cvt_scalef32_pk_f32_fp4 v[158:159], v59, 1.0 op_sel:[1,0,0]
	v_cvt_scalef32_pk_f32_fp4 v[160:161], v59, 1.0 op_sel:[0,1,0]
	v_cvt_scalef32_pk_f32_fp4 v[58:59], v59, 1.0 op_sel:[1,1,0]
	v_pk_fma_f32 v[78:79], v[78:79], s[50:51], v[174:175] op_sel_hi:[1,0,1]
	v_pk_fma_f32 v[80:81], v[80:81], s[50:51], v[172:173] op_sel_hi:[1,0,1]
	v_pk_fma_f32 v[82:83], v[82:83], s[50:51], v[170:171] op_sel_hi:[1,0,1]
	v_pk_fma_f32 v[84:85], v[84:85], s[50:51], v[168:169] op_sel_hi:[1,0,1]
	v_pk_fma_f32 v[86:87], v[86:87], s[50:51], v[166:167] op_sel_hi:[1,0,1]
	v_pk_fma_f32 v[88:89], v[88:89], s[50:51], v[164:165] op_sel_hi:[1,0,1]
	v_pk_fma_f32 v[154:155], v[162:163], s[50:51], v[154:155] op_sel_hi:[1,0,1]
	v_pk_fma_f32 v[150:151], v[156:157], s[50:51], v[150:151] op_sel_hi:[1,0,1]
	v_pk_fma_f32 v[148:149], v[158:159], s[50:51], v[148:149] op_sel_hi:[1,0,1]
	v_pk_fma_f32 v[146:147], v[160:161], s[50:51], v[146:147] op_sel_hi:[1,0,1]
	v_pk_fma_f32 v[58:59], v[58:59], s[50:51], v[144:145] op_sel_hi:[1,0,1]
	v_readlane_b32 s50, v251, 1
	v_cvt_scalef32_pk_f32_fp4 v[144:145], v52, 1.0
	v_cvt_scalef32_pk_f32_fp4 v[156:157], v52, 1.0 op_sel:[1,0,0]
	v_cvt_scalef32_pk_f32_fp4 v[158:159], v52, 1.0 op_sel:[0,1,0]
	v_cvt_scalef32_pk_f32_fp4 v[160:161], v52, 1.0 op_sel:[1,1,0]
	v_pk_fma_f32 v[76:77], v[144:145], s[50:51], v[76:77] op_sel_hi:[1,0,1]
	v_pk_fma_f32 v[78:79], v[156:157], s[50:51], v[78:79] op_sel_hi:[1,0,1]
	v_pk_fma_f32 v[80:81], v[158:159], s[50:51], v[80:81] op_sel_hi:[1,0,1]
	v_cvt_scalef32_pk_f32_fp4 v[144:145], v53, 1.0
	v_cvt_scalef32_pk_f32_fp4 v[156:157], v53, 1.0 op_sel:[1,0,0]
	v_cvt_scalef32_pk_f32_fp4 v[158:159], v53, 1.0 op_sel:[0,1,0]
	v_cvt_scalef32_pk_f32_fp4 v[52:53], v53, 1.0 op_sel:[1,1,0]
	v_pk_fma_f32 v[84:85], v[144:145], s[50:51], v[84:85] op_sel_hi:[1,0,1]
	v_pk_fma_f32 v[86:87], v[156:157], s[50:51], v[86:87] op_sel_hi:[1,0,1]
	v_pk_fma_f32 v[88:89], v[158:159], s[50:51], v[88:89] op_sel_hi:[1,0,1]
	v_pk_fma_f32 v[52:53], v[52:53], s[50:51], v[56:57] op_sel_hi:[1,0,1]
	v_cvt_scalef32_pk_f32_fp4 v[56:57], v54, 1.0
	v_cvt_scalef32_pk_f32_fp4 v[144:145], v54, 1.0 op_sel:[1,0,0]
	v_cvt_scalef32_pk_f32_fp4 v[156:157], v54, 1.0 op_sel:[0,1,0]
	v_cvt_scalef32_pk_f32_fp4 v[158:159], v54, 1.0 op_sel:[1,1,0]
	v_pk_fma_f32 v[56:57], v[56:57], s[50:51], v[90:91] op_sel_hi:[1,0,1]
	v_pk_fma_f32 v[90:91], v[144:145], s[50:51], v[140:141] op_sel_hi:[1,0,1]
	v_pk_fma_f32 v[140:141], v[156:157], s[50:51], v[152:153] op_sel_hi:[1,0,1]
	v_pk_fma_f32 v[144:145], v[158:159], s[50:51], v[154:155] op_sel_hi:[1,0,1]
	v_cvt_scalef32_pk_f32_fp4 v[152:153], v55, 1.0
	v_cvt_scalef32_pk_f32_fp4 v[154:155], v55, 1.0 op_sel:[1,0,0]
	v_cvt_scalef32_pk_f32_fp4 v[156:157], v55, 1.0 op_sel:[0,1,0]
	v_cvt_scalef32_pk_f32_fp4 v[54:55], v55, 1.0 op_sel:[1,1,0]
	v_pk_fma_f32 v[82:83], v[160:161], s[50:51], v[82:83] op_sel_hi:[1,0,1]
	v_pk_fma_f32 v[150:151], v[152:153], s[50:51], v[150:151] op_sel_hi:[1,0,1]
	v_pk_fma_f32 v[148:149], v[154:155], s[50:51], v[148:149] op_sel_hi:[1,0,1]
	v_pk_fma_f32 v[146:147], v[156:157], s[50:51], v[146:147] op_sel_hi:[1,0,1]
	v_pk_fma_f32 v[54:55], v[54:55], s[50:51], v[58:59] op_sel_hi:[1,0,1]
	v_readlane_b32 s50, v251, 2
	v_cvt_scalef32_pk_f32_fp4 v[58:59], v44, 1.0
	v_cvt_scalef32_pk_f32_fp4 v[152:153], v44, 1.0 op_sel:[1,0,0]
	v_cvt_scalef32_pk_f32_fp4 v[154:155], v44, 1.0 op_sel:[0,1,0]
	v_cvt_scalef32_pk_f32_fp4 v[156:157], v44, 1.0 op_sel:[1,1,0]
	v_pk_fma_f32 v[58:59], v[58:59], s[50:51], v[76:77] op_sel_hi:[1,0,1]
	v_pk_fma_f32 v[76:77], v[152:153], s[50:51], v[78:79] op_sel_hi:[1,0,1]
	v_pk_fma_f32 v[78:79], v[154:155], s[50:51], v[80:81] op_sel_hi:[1,0,1]
	v_pk_fma_f32 v[80:81], v[156:157], s[50:51], v[82:83] op_sel_hi:[1,0,1]
	v_cvt_scalef32_pk_f32_fp4 v[82:83], v45, 1.0
	v_cvt_scalef32_pk_f32_fp4 v[152:153], v45, 1.0 op_sel:[1,0,0]
	v_cvt_scalef32_pk_f32_fp4 v[154:155], v45, 1.0 op_sel:[0,1,0]
	v_cvt_scalef32_pk_f32_fp4 v[44:45], v45, 1.0 op_sel:[1,1,0]
	v_pk_fma_f32 v[82:83], v[82:83], s[50:51], v[84:85] op_sel_hi:[1,0,1]
	v_pk_fma_f32 v[84:85], v[152:153], s[50:51], v[86:87] op_sel_hi:[1,0,1]
	v_pk_fma_f32 v[86:87], v[154:155], s[50:51], v[88:89] op_sel_hi:[1,0,1]
	v_pk_fma_f32 v[44:45], v[44:45], s[50:51], v[52:53] op_sel_hi:[1,0,1]
	v_cvt_scalef32_pk_f32_fp4 v[52:53], v46, 1.0
	v_cvt_scalef32_pk_f32_fp4 v[88:89], v46, 1.0 op_sel:[1,0,0]
	v_cvt_scalef32_pk_f32_fp4 v[152:153], v46, 1.0 op_sel:[0,1,0]
	v_cvt_scalef32_pk_f32_fp4 v[154:155], v46, 1.0 op_sel:[1,1,0]
	v_pk_fma_f32 v[52:53], v[52:53], s[50:51], v[56:57] op_sel_hi:[1,0,1]
	v_pk_fma_f32 v[56:57], v[88:89], s[50:51], v[90:91] op_sel_hi:[1,0,1]
	v_pk_fma_f32 v[88:89], v[152:153], s[50:51], v[140:141] op_sel_hi:[1,0,1]
	v_pk_fma_f32 v[90:91], v[154:155], s[50:51], v[144:145] op_sel_hi:[1,0,1]
	v_cvt_scalef32_pk_f32_fp4 v[140:141], v47, 1.0
	v_cvt_scalef32_pk_f32_fp4 v[144:145], v47, 1.0 op_sel:[1,0,0]
	v_cvt_scalef32_pk_f32_fp4 v[152:153], v47, 1.0 op_sel:[0,1,0]
	v_cvt_scalef32_pk_f32_fp4 v[46:47], v47, 1.0 op_sel:[1,1,0]
	v_pk_fma_f32 v[140:141], v[140:141], s[50:51], v[150:151] op_sel_hi:[1,0,1]
	v_pk_fma_f32 v[170:171], v[144:145], s[50:51], v[148:149] op_sel_hi:[1,0,1]
	v_pk_fma_f32 v[172:173], v[152:153], s[50:51], v[146:147] op_sel_hi:[1,0,1]
	v_pk_fma_f32 v[46:47], v[46:47], s[50:51], v[54:55] op_sel_hi:[1,0,1]
	v_readlane_b32 s50, v251, 3
	v_cvt_scalef32_pk_f32_fp4 v[54:55], v36, 1.0
	v_cvt_scalef32_pk_f32_fp4 v[146:147], v36, 1.0 op_sel:[1,0,0]
	v_cvt_scalef32_pk_f32_fp4 v[148:149], v36, 1.0 op_sel:[0,1,0]
	v_cvt_scalef32_pk_f32_fp4 v[150:151], v36, 1.0 op_sel:[1,1,0]
	v_pk_fma_f32 v[144:145], v[54:55], s[50:51], v[58:59] op_sel_hi:[1,0,1]
	v_pk_fma_f32 v[146:147], v[146:147], s[50:51], v[76:77] op_sel_hi:[1,0,1]
	v_cvt_scalef32_pk_f32_fp4 v[54:55], v37, 1.0
	v_cvt_scalef32_pk_f32_fp4 v[58:59], v37, 1.0 op_sel:[1,0,0]
	v_cvt_scalef32_pk_f32_fp4 v[76:77], v37, 1.0 op_sel:[0,1,0]
	v_cvt_scalef32_pk_f32_fp4 v[36:37], v37, 1.0 op_sel:[1,1,0]
	v_pk_fma_f32 v[158:159], v[36:37], s[50:51], v[44:45] op_sel_hi:[1,0,1]
	v_cvt_scalef32_pk_f32_fp4 v[36:37], v38, 1.0
	v_cvt_scalef32_pk_f32_fp4 v[44:45], v38, 1.0 op_sel:[1,0,0]
	v_pk_fma_f32 v[152:153], v[54:55], s[50:51], v[82:83] op_sel_hi:[1,0,1]
	v_pk_fma_f32 v[154:155], v[58:59], s[50:51], v[84:85] op_sel_hi:[1,0,1]
	v_cvt_scalef32_pk_f32_fp4 v[54:55], v38, 1.0 op_sel:[0,1,0]
	v_cvt_scalef32_pk_f32_fp4 v[58:59], v38, 1.0 op_sel:[1,1,0]
	v_pk_fma_f32 v[160:161], v[36:37], s[50:51], v[52:53] op_sel_hi:[1,0,1]
	v_pk_fma_f32 v[162:163], v[44:45], s[50:51], v[56:57] op_sel_hi:[1,0,1]
	v_cvt_scalef32_pk_f32_fp4 v[36:37], v39, 1.0
	v_cvt_scalef32_pk_f32_fp4 v[44:45], v39, 1.0 op_sel:[1,0,0]
	v_cvt_scalef32_pk_f32_fp4 v[52:53], v39, 1.0 op_sel:[0,1,0]
	v_cvt_scalef32_pk_f32_fp4 v[38:39], v39, 1.0 op_sel:[1,1,0]
	v_pk_fma_f32 v[148:149], v[148:149], s[50:51], v[78:79] op_sel_hi:[1,0,1]
	v_pk_fma_f32 v[150:151], v[150:151], s[50:51], v[80:81] op_sel_hi:[1,0,1]
	v_pk_fma_f32 v[156:157], v[76:77], s[50:51], v[86:87] op_sel_hi:[1,0,1]
	v_pk_fma_f32 v[164:165], v[54:55], s[50:51], v[88:89] op_sel_hi:[1,0,1]
	v_pk_fma_f32 v[166:167], v[58:59], s[50:51], v[90:91] op_sel_hi:[1,0,1]
	v_pk_fma_f32 v[168:169], v[36:37], s[50:51], v[140:141] op_sel_hi:[1,0,1]
	v_pk_fma_f32 v[170:171], v[44:45], s[50:51], v[170:171] op_sel_hi:[1,0,1]
	v_pk_fma_f32 v[172:173], v[52:53], s[50:51], v[172:173] op_sel_hi:[1,0,1]
	v_pk_fma_f32 v[174:175], v[38:39], s[50:51], v[46:47] op_sel_hi:[1,0,1]
	ds_read_b128 v[36:39], v250 offset:16
	ds_read_b32 v140, v249 offset:16
	v_mov_b32_e32 v251, 0
	v_mov_b32_e32 v252, 0
	s_waitcnt vmcnt(17)
	v_dot8c_i32_i4_e32 v251, v72, v24
	s_waitcnt lgkmcnt(1)
	v_readfirstlane_b32 s50, v36
	s_ashr_i32 s51, s50, 31
	s_lshl_b64 s[50:51], s[50:51], 10
	v_lshl_add_u64 v[44:45], v[124:125], 0, s[50:51]
	global_load_dwordx4 v[88:91], v[44:45], off
	v_lshl_add_u64 v[44:45], v[126:127], 0, s[50:51]
	v_readfirstlane_b32 s50, v37
	s_ashr_i32 s51, s50, 31
	s_lshl_b64 s[50:51], s[50:51], 10
	v_lshl_add_u64 v[36:37], v[124:125], 0, s[50:51]
	global_load_dwordx4 v[56:59], v[44:45], off
	global_load_dwordx4 v[84:87], v[36:37], off
	v_lshl_add_u64 v[36:37], v[126:127], 0, s[50:51]
	v_readfirstlane_b32 s50, v38
	s_waitcnt lgkmcnt(0)
	v_lshlrev_b32_e32 v140, 1, v140
	s_ashr_i32 s51, s50, 31
	v_ashrrev_i32_e32 v141, 31, v140
	s_lshl_b64 s[50:51], s[50:51], 10
	v_lshl_add_u64 v[140:141], v[140:141], 2, s[4:5]
	global_load_dwordx4 v[52:55], v[36:37], off
	v_dot8c_i32_i4_e32 v252, v72, v20
	global_load_dwordx2 v[140:141], v[140:141], off
	v_lshl_add_u64 v[36:37], v[124:125], 0, s[50:51]
	global_load_dwordx4 v[80:83], v[36:37], off
	v_lshl_add_u64 v[36:37], v[126:127], 0, s[50:51]
	v_readfirstlane_b32 s50, v39
	s_ashr_i32 s51, s50, 31
	s_lshl_b64 s[50:51], s[50:51], 10
	global_load_dwordx4 v[44:47], v[36:37], off
	v_lshl_add_u64 v[36:37], v[124:125], 0, s[50:51]
	global_load_dwordx4 v[76:79], v[36:37], off
	v_lshl_add_u64 v[36:37], v[126:127], 0, s[50:51]
	global_load_dwordx4 v[36:39], v[36:37], off
	v_dot8c_i32_i4_e32 v251, v73, v25
	v_dot8c_i32_i4_e32 v252, v73, v21
	v_dot8c_i32_i4_e32 v251, v74, v26
	v_dot8c_i32_i4_e32 v252, v74, v22
	v_mov_b32_e32 v73, 0
	v_mov_b32_e32 v74, 0
	s_waitcnt vmcnt(24)
	v_dot8c_i32_i4_e32 v73, v68, v24
	v_dot8c_i32_i4_e32 v74, v68, v20
	v_dot8c_i32_i4_e32 v73, v69, v25
	v_dot8c_i32_i4_e32 v74, v69, v21
	v_dot8c_i32_i4_e32 v73, v70, v26
	v_dot8c_i32_i4_e32 v74, v70, v22
	v_mov_b32_e32 v69, 0
	v_mov_b32_e32 v70, 0
	s_waitcnt vmcnt(21)
	v_dot8c_i32_i4_e32 v69, v64, v24
	v_dot8c_i32_i4_e32 v70, v64, v20
	v_dot8c_i32_i4_e32 v69, v65, v25
	v_dot8c_i32_i4_e32 v70, v65, v21
	v_dot8c_i32_i4_e32 v69, v66, v26
	v_dot8c_i32_i4_e32 v70, v66, v22
	v_mov_b32_e32 v65, 0
	v_mov_b32_e32 v66, 0
	s_waitcnt vmcnt(19)
	v_dot8c_i32_i4_e32 v65, v60, v24
	v_dot8c_i32_i4_e32 v66, v60, v20
	v_dot8c_i32_i4_e32 v65, v61, v25
	v_dot8c_i32_i4_e32 v66, v61, v21
	v_dot8c_i32_i4_e32 v251, v75, v27
	v_dot8c_i32_i4_e32 v252, v75, v23
	v_dot8c_i32_i4_e32 v73, v71, v27
	v_dot8c_i32_i4_e32 v74, v71, v23
	v_dot8c_i32_i4_e32 v65, v62, v26
	v_dot8c_i32_i4_e32 v66, v62, v22
	v_lshl_add_u32 v72, v251, 4, v252
	v_lshl_add_u32 v68, v73, 4, v74
	v_dot8c_i32_i4_e32 v69, v67, v27
	v_dot8c_i32_i4_e32 v70, v67, v23
	v_dot8c_i32_i4_e32 v65, v63, v27
	v_dot8c_i32_i4_e32 v66, v63, v23
	v_cvt_f32_i32_e32 v72, v72
	v_cvt_f32_i32_e32 v68, v68
	v_lshl_add_u32 v64, v69, 4, v70
	v_lshl_add_u32 v60, v65, 4, v66
	v_cvt_f32_i32_e32 v64, v64
	v_cvt_f32_i32_e32 v60, v60
	v_cndmask_b32_e64 v61, v68, v72, s[42:43]
	v_cndmask_b32_e64 v62, v72, v68, s[42:43]
	s_nop 1
	v_add_f32_dpp v61, v62, v61 quad_perm:[1,0,3,2] row_mask:0xf bank_mask:0xf bound_ctrl:1
	v_cndmask_b32_e64 v62, v60, v64, s[42:43]
	v_cndmask_b32_e64 v60, v64, v60, s[42:43]
	s_nop 1
	v_add_f32_dpp v60, v60, v62 quad_perm:[1,0,3,2] row_mask:0xf bank_mask:0xf bound_ctrl:1
	v_cndmask_b32_e64 v62, v60, v61, s[44:45]
	v_cndmask_b32_e64 v60, v61, v60, s[44:45]
	s_nop 1
	v_add_f32_dpp v60, v60, v62 quad_perm:[2,3,0,1] row_mask:0xf bank_mask:0xf bound_ctrl:1
	s_waitcnt vmcnt(18)
	v_mul_f32_e64 v62, v248, v138
	v_add_f32_dpp v60, v60, v60 row_ror:4 row_mask:0xf bank_mask:0xf bound_ctrl:1
	s_nop 1
	v_add_f32_dpp v60, v60, v60 row_ror:8 row_mask:0xf bank_mask:0xf bound_ctrl:1
	v_mov_b32_e32 v61, v60
	s_nop 1
	v_permlane32_swap_b32_e32 v60, v61
	v_add_f32_e32 v60, v60, v61
	v_mov_b32_e32 v61, v60
	s_nop 1
	v_permlane16_swap_b32_e32 v60, v61
	v_add_f32_e64 v60, v60, v61
	ds_read_b32 v61, v249 offset:496
	v_mul_f32_e64 v60, v62, v60
	v_fma_f32 v62, |v60|, s39, 1.0
	v_rcp_f32_e32 v62, v62
	v_cmp_gt_f32_e32 vcc, 0, v60
	v_fmamk_f32 v63, v62, 0x3f07dc22, v210
	v_fmaak_f32 v63, v62, v63, 0x3f35f0e3
	v_fmaak_f32 v63, v62, v63, 0xbe11a98e
	v_fmaak_f32 v63, v62, v63, 0x3e027906
	v_mul_f32_e32 v62, v62, v63
	v_mul_f32_e32 v63, v60, v60
	v_mul_f32_e32 v63, 0xbf38aa3b, v63
	v_exp_f32_e32 v63, v63
	s_nop 0
	v_mul_f32_e32 v62, v63, v62
	v_mul_f32_e32 v63, v60, v62
	v_fma_f32 v60, -v60, v62, v60
	v_cndmask_b32_e32 v60, v60, v63, vcc
	s_waitcnt lgkmcnt(0)
	v_mul_f32_e64 v60, v61, v60
	v_mul_f32_e32 v251, v139, v60
	s_nop 0
	v_readlane_b32 s50, v251, 0
	v_cvt_scalef32_pk_f32_fp4 v[60:61], v48, 1.0
	v_cvt_scalef32_pk_f32_fp4 v[62:63], v48, 1.0 op_sel:[1,0,0]
	v_cvt_scalef32_pk_f32_fp4 v[64:65], v48, 1.0 op_sel:[0,1,0]
	v_cvt_scalef32_pk_f32_fp4 v[66:67], v48, 1.0 op_sel:[1,1,0]
	v_cvt_scalef32_pk_f32_fp4 v[68:69], v49, 1.0
	v_pk_fma_f32 v[60:61], v[60:61], s[50:51], v[144:145] op_sel_hi:[1,0,1]
	v_pk_fma_f32 v[62:63], v[62:63], s[50:51], v[146:147] op_sel_hi:[1,0,1]
	v_pk_fma_f32 v[64:65], v[64:65], s[50:51], v[148:149] op_sel_hi:[1,0,1]
	v_pk_fma_f32 v[66:67], v[66:67], s[50:51], v[150:151] op_sel_hi:[1,0,1]
	v_cvt_scalef32_pk_f32_fp4 v[70:71], v49, 1.0 op_sel:[1,0,0]
	v_cvt_scalef32_pk_f32_fp4 v[72:73], v49, 1.0 op_sel:[0,1,0]
	v_cvt_scalef32_pk_f32_fp4 v[48:49], v49, 1.0 op_sel:[1,1,0]
	v_pk_fma_f32 v[68:69], v[68:69], s[50:51], v[152:153] op_sel_hi:[1,0,1]
	v_cvt_scalef32_pk_f32_fp4 v[74:75], v50, 1.0
	v_cvt_scalef32_pk_f32_fp4 v[138:139], v50, 1.0 op_sel:[1,0,0]
	v_cvt_scalef32_pk_f32_fp4 v[144:145], v50, 1.0 op_sel:[0,1,0]
	v_cvt_scalef32_pk_f32_fp4 v[146:147], v50, 1.0 op_sel:[1,1,0]
	v_cvt_scalef32_pk_f32_fp4 v[148:149], v51, 1.0
	v_cvt_scalef32_pk_f32_fp4 v[150:151], v51, 1.0 op_sel:[1,0,0]
	v_cvt_scalef32_pk_f32_fp4 v[152:153], v51, 1.0 op_sel:[0,1,0]
	v_cvt_scalef32_pk_f32_fp4 v[50:51], v51, 1.0 op_sel:[1,1,0]
	v_pk_fma_f32 v[70:71], v[70:71], s[50:51], v[154:155] op_sel_hi:[1,0,1]
	v_pk_fma_f32 v[72:73], v[72:73], s[50:51], v[156:157] op_sel_hi:[1,0,1]
	v_pk_fma_f32 v[48:49], v[48:49], s[50:51], v[158:159] op_sel_hi:[1,0,1]
	v_pk_fma_f32 v[74:75], v[74:75], s[50:51], v[160:161] op_sel_hi:[1,0,1]
	v_pk_fma_f32 v[138:139], v[138:139], s[50:51], v[162:163] op_sel_hi:[1,0,1]
	v_pk_fma_f32 v[144:145], v[144:145], s[50:51], v[164:165] op_sel_hi:[1,0,1]
	v_pk_fma_f32 v[146:147], v[146:147], s[50:51], v[166:167] op_sel_hi:[1,0,1]
	v_pk_fma_f32 v[148:149], v[148:149], s[50:51], v[168:169] op_sel_hi:[1,0,1]
	v_pk_fma_f32 v[150:151], v[150:151], s[50:51], v[170:171] op_sel_hi:[1,0,1]
	v_pk_fma_f32 v[152:153], v[152:153], s[50:51], v[172:173] op_sel_hi:[1,0,1]
	v_pk_fma_f32 v[50:51], v[50:51], s[50:51], v[174:175] op_sel_hi:[1,0,1]
	v_readlane_b32 s50, v251, 1
	v_cvt_scalef32_pk_f32_fp4 v[154:155], v40, 1.0
	v_cvt_scalef32_pk_f32_fp4 v[156:157], v40, 1.0 op_sel:[1,0,0]
	v_cvt_scalef32_pk_f32_fp4 v[158:159], v40, 1.0 op_sel:[0,1,0]
	v_cvt_scalef32_pk_f32_fp4 v[160:161], v40, 1.0 op_sel:[1,1,0]
	v_pk_fma_f32 v[60:61], v[154:155], s[50:51], v[60:61] op_sel_hi:[1,0,1]
	v_pk_fma_f32 v[62:63], v[156:157], s[50:51], v[62:63] op_sel_hi:[1,0,1]
	v_pk_fma_f32 v[64:65], v[158:159], s[50:51], v[64:65] op_sel_hi:[1,0,1]
	v_cvt_scalef32_pk_f32_fp4 v[154:155], v41, 1.0
	v_cvt_scalef32_pk_f32_fp4 v[156:157], v41, 1.0 op_sel:[1,0,0]
	v_cvt_scalef32_pk_f32_fp4 v[158:159], v41, 1.0 op_sel:[0,1,0]
	v_cvt_scalef32_pk_f32_fp4 v[40:41], v41, 1.0 op_sel:[1,1,0]
	v_pk_fma_f32 v[68:69], v[154:155], s[50:51], v[68:69] op_sel_hi:[1,0,1]
	v_pk_fma_f32 v[70:71], v[156:157], s[50:51], v[70:71] op_sel_hi:[1,0,1]
	v_pk_fma_f32 v[72:73], v[158:159], s[50:51], v[72:73] op_sel_hi:[1,0,1]
	v_pk_fma_f32 v[40:41], v[40:41], s[50:51], v[48:49] op_sel_hi:[1,0,1]
	v_cvt_scalef32_pk_f32_fp4 v[48:49], v42, 1.0
	v_cvt_scalef32_pk_f32_fp4 v[154:155], v42, 1.0 op_sel:[1,0,0]
	v_cvt_scalef32_pk_f32_fp4 v[156:157], v42, 1.0 op_sel:[0,1,0]
	v_cvt_scalef32_pk_f32_fp4 v[158:159], v42, 1.0 op_sel:[1,1,0]
	v_pk_fma_f32 v[48:49], v[48:49], s[50:51], v[74:75] op_sel_hi:[1,0,1]
	v_pk_fma_f32 v[74:75], v[154:155], s[50:51], v[138:139] op_sel_hi:[1,0,1]
	v_pk_fma_f32 v[138:139], v[156:157], s[50:51], v[144:145] op_sel_hi:[1,0,1]
	v_pk_fma_f32 v[144:145], v[158:159], s[50:51], v[146:147] op_sel_hi:[1,0,1]
	v_cvt_scalef32_pk_f32_fp4 v[146:147], v43, 1.0
	v_cvt_scalef32_pk_f32_fp4 v[154:155], v43, 1.0 op_sel:[1,0,0]
	v_cvt_scalef32_pk_f32_fp4 v[156:157], v43, 1.0 op_sel:[0,1,0]
	v_cvt_scalef32_pk_f32_fp4 v[42:43], v43, 1.0 op_sel:[1,1,0]
	v_pk_fma_f32 v[66:67], v[160:161], s[50:51], v[66:67] op_sel_hi:[1,0,1]
	v_pk_fma_f32 v[146:147], v[146:147], s[50:51], v[148:149] op_sel_hi:[1,0,1]
	v_pk_fma_f32 v[148:149], v[154:155], s[50:51], v[150:151] op_sel_hi:[1,0,1]
	v_pk_fma_f32 v[150:151], v[156:157], s[50:51], v[152:153] op_sel_hi:[1,0,1]
	v_pk_fma_f32 v[42:43], v[42:43], s[50:51], v[50:51] op_sel_hi:[1,0,1]
	v_readlane_b32 s50, v251, 2
	v_cvt_scalef32_pk_f32_fp4 v[50:51], v32, 1.0
	v_cvt_scalef32_pk_f32_fp4 v[152:153], v32, 1.0 op_sel:[1,0,0]
	v_cvt_scalef32_pk_f32_fp4 v[154:155], v32, 1.0 op_sel:[0,1,0]
	v_cvt_scalef32_pk_f32_fp4 v[156:157], v32, 1.0 op_sel:[1,1,0]
	v_pk_fma_f32 v[50:51], v[50:51], s[50:51], v[60:61] op_sel_hi:[1,0,1]
	v_pk_fma_f32 v[60:61], v[152:153], s[50:51], v[62:63] op_sel_hi:[1,0,1]
	v_pk_fma_f32 v[62:63], v[154:155], s[50:51], v[64:65] op_sel_hi:[1,0,1]
	v_pk_fma_f32 v[64:65], v[156:157], s[50:51], v[66:67] op_sel_hi:[1,0,1]
	v_cvt_scalef32_pk_f32_fp4 v[66:67], v33, 1.0
	v_cvt_scalef32_pk_f32_fp4 v[152:153], v33, 1.0 op_sel:[1,0,0]
	v_cvt_scalef32_pk_f32_fp4 v[154:155], v33, 1.0 op_sel:[0,1,0]
	v_cvt_scalef32_pk_f32_fp4 v[32:33], v33, 1.0 op_sel:[1,1,0]
	v_pk_fma_f32 v[66:67], v[66:67], s[50:51], v[68:69] op_sel_hi:[1,0,1]
	v_pk_fma_f32 v[68:69], v[152:153], s[50:51], v[70:71] op_sel_hi:[1,0,1]
	v_pk_fma_f32 v[70:71], v[154:155], s[50:51], v[72:73] op_sel_hi:[1,0,1]
	v_pk_fma_f32 v[32:33], v[32:33], s[50:51], v[40:41] op_sel_hi:[1,0,1]
	v_cvt_scalef32_pk_f32_fp4 v[40:41], v34, 1.0
	v_cvt_scalef32_pk_f32_fp4 v[72:73], v34, 1.0 op_sel:[1,0,0]
	v_cvt_scalef32_pk_f32_fp4 v[152:153], v34, 1.0 op_sel:[0,1,0]
	v_cvt_scalef32_pk_f32_fp4 v[154:155], v34, 1.0 op_sel:[1,1,0]
	v_pk_fma_f32 v[40:41], v[40:41], s[50:51], v[48:49] op_sel_hi:[1,0,1]
	v_pk_fma_f32 v[48:49], v[72:73], s[50:51], v[74:75] op_sel_hi:[1,0,1]
	v_pk_fma_f32 v[72:73], v[152:153], s[50:51], v[138:139] op_sel_hi:[1,0,1]
	v_pk_fma_f32 v[74:75], v[154:155], s[50:51], v[144:145] op_sel_hi:[1,0,1]
	v_cvt_scalef32_pk_f32_fp4 v[138:139], v35, 1.0
	v_cvt_scalef32_pk_f32_fp4 v[144:145], v35, 1.0 op_sel:[1,0,0]
	v_cvt_scalef32_pk_f32_fp4 v[152:153], v35, 1.0 op_sel:[0,1,0]
	v_cvt_scalef32_pk_f32_fp4 v[34:35], v35, 1.0 op_sel:[1,1,0]
	v_pk_fma_f32 v[138:139], v[138:139], s[50:51], v[146:147] op_sel_hi:[1,0,1]
	v_pk_fma_f32 v[170:171], v[144:145], s[50:51], v[148:149] op_sel_hi:[1,0,1]
	v_pk_fma_f32 v[172:173], v[152:153], s[50:51], v[150:151] op_sel_hi:[1,0,1]
	v_pk_fma_f32 v[34:35], v[34:35], s[50:51], v[42:43] op_sel_hi:[1,0,1]
	v_readlane_b32 s50, v251, 3
	v_cvt_scalef32_pk_f32_fp4 v[42:43], v28, 1.0
	v_cvt_scalef32_pk_f32_fp4 v[146:147], v28, 1.0 op_sel:[1,0,0]
	v_cvt_scalef32_pk_f32_fp4 v[148:149], v28, 1.0 op_sel:[0,1,0]
	v_cvt_scalef32_pk_f32_fp4 v[150:151], v28, 1.0 op_sel:[1,1,0]
	v_pk_fma_f32 v[144:145], v[42:43], s[50:51], v[50:51] op_sel_hi:[1,0,1]
	v_pk_fma_f32 v[146:147], v[146:147], s[50:51], v[60:61] op_sel_hi:[1,0,1]
	v_cvt_scalef32_pk_f32_fp4 v[42:43], v29, 1.0
	v_cvt_scalef32_pk_f32_fp4 v[50:51], v29, 1.0 op_sel:[1,0,0]
	v_cvt_scalef32_pk_f32_fp4 v[60:61], v29, 1.0 op_sel:[0,1,0]
	v_cvt_scalef32_pk_f32_fp4 v[28:29], v29, 1.0 op_sel:[1,1,0]
	v_pk_fma_f32 v[158:159], v[28:29], s[50:51], v[32:33] op_sel_hi:[1,0,1]
	v_cvt_scalef32_pk_f32_fp4 v[28:29], v30, 1.0
	v_cvt_scalef32_pk_f32_fp4 v[32:33], v30, 1.0 op_sel:[1,0,0]
	v_pk_fma_f32 v[152:153], v[42:43], s[50:51], v[66:67] op_sel_hi:[1,0,1]
	v_pk_fma_f32 v[154:155], v[50:51], s[50:51], v[68:69] op_sel_hi:[1,0,1]
	v_cvt_scalef32_pk_f32_fp4 v[42:43], v30, 1.0 op_sel:[0,1,0]
	v_cvt_scalef32_pk_f32_fp4 v[50:51], v30, 1.0 op_sel:[1,1,0]
	v_pk_fma_f32 v[160:161], v[28:29], s[50:51], v[40:41] op_sel_hi:[1,0,1]
	v_pk_fma_f32 v[162:163], v[32:33], s[50:51], v[48:49] op_sel_hi:[1,0,1]
	v_cvt_scalef32_pk_f32_fp4 v[28:29], v31, 1.0
	v_cvt_scalef32_pk_f32_fp4 v[32:33], v31, 1.0 op_sel:[1,0,0]
	v_cvt_scalef32_pk_f32_fp4 v[40:41], v31, 1.0 op_sel:[0,1,0]
	v_cvt_scalef32_pk_f32_fp4 v[30:31], v31, 1.0 op_sel:[1,1,0]
	v_pk_fma_f32 v[148:149], v[148:149], s[50:51], v[62:63] op_sel_hi:[1,0,1]
	v_pk_fma_f32 v[150:151], v[150:151], s[50:51], v[64:65] op_sel_hi:[1,0,1]
	v_pk_fma_f32 v[156:157], v[60:61], s[50:51], v[70:71] op_sel_hi:[1,0,1]
	v_pk_fma_f32 v[164:165], v[42:43], s[50:51], v[72:73] op_sel_hi:[1,0,1]
	v_pk_fma_f32 v[166:167], v[50:51], s[50:51], v[74:75] op_sel_hi:[1,0,1]
	v_pk_fma_f32 v[168:169], v[28:29], s[50:51], v[138:139] op_sel_hi:[1,0,1]
	v_pk_fma_f32 v[170:171], v[32:33], s[50:51], v[170:171] op_sel_hi:[1,0,1]
	v_pk_fma_f32 v[172:173], v[40:41], s[50:51], v[172:173] op_sel_hi:[1,0,1]
	v_pk_fma_f32 v[174:175], v[30:31], s[50:51], v[34:35] op_sel_hi:[1,0,1]
	ds_read_b128 v[28:31], v250 offset:32
	ds_read_b32 v138, v249 offset:32
	v_mov_b32_e32 v250, 0
	v_mov_b32_e32 v251, 0
	s_waitcnt vmcnt(17)
	v_dot8c_i32_i4_e32 v250, v120, v24
	s_waitcnt lgkmcnt(1)
	v_readfirstlane_b32 s50, v28
	s_ashr_i32 s51, s50, 31
	s_lshl_b64 s[50:51], s[50:51], 10
	v_lshl_add_u64 v[32:33], v[124:125], 0, s[50:51]
	global_load_dwordx4 v[72:75], v[32:33], off
	v_lshl_add_u64 v[32:33], v[126:127], 0, s[50:51]
	v_readfirstlane_b32 s50, v29
	s_ashr_i32 s51, s50, 31
	s_lshl_b64 s[50:51], s[50:51], 10
	v_lshl_add_u64 v[28:29], v[124:125], 0, s[50:51]
	global_load_dwordx4 v[48:51], v[32:33], off
	global_load_dwordx4 v[68:71], v[28:29], off
	v_lshl_add_u64 v[28:29], v[126:127], 0, s[50:51]
	v_readfirstlane_b32 s50, v30
	s_waitcnt lgkmcnt(0)
	v_lshlrev_b32_e32 v138, 1, v138
	s_ashr_i32 s51, s50, 31
	v_ashrrev_i32_e32 v139, 31, v138
	s_lshl_b64 s[50:51], s[50:51], 10
	v_lshl_add_u64 v[138:139], v[138:139], 2, s[4:5]
	global_load_dwordx4 v[40:43], v[28:29], off
	v_dot8c_i32_i4_e32 v251, v120, v20
	global_load_dwordx2 v[138:139], v[138:139], off
	v_lshl_add_u64 v[28:29], v[124:125], 0, s[50:51]
	global_load_dwordx4 v[64:67], v[28:29], off
	v_lshl_add_u64 v[28:29], v[126:127], 0, s[50:51]
	v_readfirstlane_b32 s50, v31
	s_ashr_i32 s51, s50, 31
	s_lshl_b64 s[50:51], s[50:51], 10
	global_load_dwordx4 v[32:35], v[28:29], off
	v_lshl_add_u64 v[28:29], v[124:125], 0, s[50:51]
	global_load_dwordx4 v[60:63], v[28:29], off
	v_lshl_add_u64 v[28:29], v[126:127], 0, s[50:51]
	global_load_dwordx4 v[28:31], v[28:29], off
	v_dot8c_i32_i4_e32 v250, v121, v25
	v_dot8c_i32_i4_e32 v251, v121, v21
	v_dot8c_i32_i4_e32 v250, v122, v26
	v_dot8c_i32_i4_e32 v251, v122, v22
	v_mov_b32_e32 v121, 0
	v_mov_b32_e32 v122, 0
	s_waitcnt vmcnt(24)
	v_dot8c_i32_i4_e32 v121, v116, v24
	v_dot8c_i32_i4_e32 v122, v116, v20
	v_dot8c_i32_i4_e32 v121, v117, v25
	v_dot8c_i32_i4_e32 v122, v117, v21
	v_dot8c_i32_i4_e32 v121, v118, v26
	v_dot8c_i32_i4_e32 v122, v118, v22
	v_mov_b32_e32 v117, 0
	v_mov_b32_e32 v118, 0
	s_waitcnt vmcnt(22)
	v_dot8c_i32_i4_e32 v117, v112, v24
	v_dot8c_i32_i4_e32 v118, v112, v20
	v_dot8c_i32_i4_e32 v117, v113, v25
	v_dot8c_i32_i4_e32 v118, v113, v21
	v_dot8c_i32_i4_e32 v117, v114, v26
	v_dot8c_i32_i4_e32 v118, v114, v22
	v_mov_b32_e32 v113, 0
	v_mov_b32_e32 v114, 0
	s_waitcnt vmcnt(20)
	v_dot8c_i32_i4_e32 v113, v108, v24
	v_dot8c_i32_i4_e32 v114, v108, v20
	v_dot8c_i32_i4_e32 v113, v109, v25
	v_dot8c_i32_i4_e32 v114, v109, v21
	v_dot8c_i32_i4_e32 v250, v123, v27
	v_dot8c_i32_i4_e32 v251, v123, v23
	v_dot8c_i32_i4_e32 v121, v119, v27
	v_dot8c_i32_i4_e32 v122, v119, v23
	v_dot8c_i32_i4_e32 v113, v110, v26
	v_dot8c_i32_i4_e32 v114, v110, v22
	v_lshl_add_u32 v120, v250, 4, v251
	v_lshl_add_u32 v116, v121, 4, v122
	v_dot8c_i32_i4_e32 v117, v115, v27
	v_dot8c_i32_i4_e32 v118, v115, v23
	v_dot8c_i32_i4_e32 v113, v111, v27
	v_dot8c_i32_i4_e32 v114, v111, v23
	v_cvt_f32_i32_e32 v120, v120
	v_cvt_f32_i32_e32 v116, v116
	v_lshl_add_u32 v112, v117, 4, v118
	v_lshl_add_u32 v108, v113, 4, v114
	v_cvt_f32_i32_e32 v112, v112
	v_cvt_f32_i32_e32 v108, v108
	v_cndmask_b32_e64 v109, v116, v120, s[42:43]
	v_cndmask_b32_e64 v110, v120, v116, s[42:43]
	s_nop 1
	v_add_f32_dpp v109, v110, v109 quad_perm:[1,0,3,2] row_mask:0xf bank_mask:0xf bound_ctrl:1
	v_cndmask_b32_e64 v110, v108, v112, s[42:43]
	v_cndmask_b32_e64 v108, v112, v108, s[42:43]
	s_nop 1
	v_add_f32_dpp v108, v108, v110 quad_perm:[1,0,3,2] row_mask:0xf bank_mask:0xf bound_ctrl:1
	v_cndmask_b32_e64 v110, v108, v109, s[44:45]
	v_cndmask_b32_e64 v108, v109, v108, s[44:45]
	s_nop 1
	v_add_f32_dpp v108, v108, v110 quad_perm:[2,3,0,1] row_mask:0xf bank_mask:0xf bound_ctrl:1
	s_waitcnt vmcnt(18)
	v_mul_f32_e64 v110, v248, v142
	v_add_f32_dpp v108, v108, v108 row_ror:4 row_mask:0xf bank_mask:0xf bound_ctrl:1
	s_nop 1
	v_add_f32_dpp v108, v108, v108 row_ror:8 row_mask:0xf bank_mask:0xf bound_ctrl:1
	v_mov_b32_e32 v109, v108
	s_nop 1
	v_permlane32_swap_b32_e32 v108, v109
	v_add_f32_e32 v108, v108, v109
	v_mov_b32_e32 v109, v108
	s_nop 1
	v_permlane16_swap_b32_e32 v108, v109
	v_add_f32_e64 v108, v108, v109
	ds_read_b32 v109, v249 offset:512
	v_mul_f32_e64 v108, v110, v108
	v_fma_f32 v110, |v108|, s39, 1.0
	v_rcp_f32_e32 v110, v110
	v_cmp_gt_f32_e32 vcc, 0, v108
	v_fmamk_f32 v111, v110, 0x3f07dc22, v210
	v_fmaak_f32 v111, v110, v111, 0x3f35f0e3
	v_fmaak_f32 v111, v110, v111, 0xbe11a98e
	v_fmaak_f32 v111, v110, v111, 0x3e027906
	v_mul_f32_e32 v110, v110, v111
	v_mul_f32_e32 v111, v108, v108
	v_mul_f32_e32 v111, 0xbf38aa3b, v111
	v_exp_f32_e32 v111, v111
	s_nop 0
	v_mul_f32_e32 v110, v111, v110
	v_mul_f32_e32 v111, v108, v110
	v_fma_f32 v108, -v108, v110, v108
	v_cndmask_b32_e32 v108, v108, v111, vcc
	s_waitcnt lgkmcnt(0)
	v_mul_f32_e64 v108, v109, v108
	v_mul_f32_e32 v249, v143, v108
	s_nop 0
	v_readlane_b32 s50, v249, 0
	v_cvt_scalef32_pk_f32_fp4 v[108:109], v104, 1.0
	v_cvt_scalef32_pk_f32_fp4 v[110:111], v104, 1.0 op_sel:[1,0,0]
	v_cvt_scalef32_pk_f32_fp4 v[112:113], v104, 1.0 op_sel:[0,1,0]
	v_cvt_scalef32_pk_f32_fp4 v[114:115], v104, 1.0 op_sel:[1,1,0]
	v_cvt_scalef32_pk_f32_fp4 v[116:117], v105, 1.0
	v_pk_fma_f32 v[108:109], v[108:109], s[50:51], v[144:145] op_sel_hi:[1,0,1]
	v_pk_fma_f32 v[110:111], v[110:111], s[50:51], v[146:147] op_sel_hi:[1,0,1]
	v_pk_fma_f32 v[112:113], v[112:113], s[50:51], v[148:149] op_sel_hi:[1,0,1]
	v_pk_fma_f32 v[114:115], v[114:115], s[50:51], v[150:151] op_sel_hi:[1,0,1]
	v_pk_fma_f32 v[116:117], v[116:117], s[50:51], v[152:153] op_sel_hi:[1,0,1]
	v_cvt_scalef32_pk_f32_fp4 v[144:145], v106, 1.0 op_sel:[0,1,0]
	v_cvt_scalef32_pk_f32_fp4 v[146:147], v106, 1.0 op_sel:[1,1,0]
	v_cvt_scalef32_pk_f32_fp4 v[148:149], v107, 1.0
	v_cvt_scalef32_pk_f32_fp4 v[150:151], v107, 1.0 op_sel:[1,0,0]
	v_cvt_scalef32_pk_f32_fp4 v[152:153], v107, 1.0 op_sel:[0,1,0]
	v_cvt_scalef32_pk_f32_fp4 v[118:119], v105, 1.0 op_sel:[1,0,0]
	v_cvt_scalef32_pk_f32_fp4 v[120:121], v105, 1.0 op_sel:[0,1,0]
	v_cvt_scalef32_pk_f32_fp4 v[104:105], v105, 1.0 op_sel:[1,1,0]
	v_cvt_scalef32_pk_f32_fp4 v[122:123], v106, 1.0
	v_cvt_scalef32_pk_f32_fp4 v[142:143], v106, 1.0 op_sel:[1,0,0]
	v_pk_fma_f32 v[144:145], v[144:145], s[50:51], v[164:165] op_sel_hi:[1,0,1]
	v_pk_fma_f32 v[146:147], v[146:147], s[50:51], v[166:167] op_sel_hi:[1,0,1]
	v_cvt_scalef32_pk_f32_fp4 v[106:107], v107, 1.0 op_sel:[1,1,0]
	v_pk_fma_f32 v[148:149], v[148:149], s[50:51], v[168:169] op_sel_hi:[1,0,1]
	v_pk_fma_f32 v[150:151], v[150:151], s[50:51], v[170:171] op_sel_hi:[1,0,1]
	v_pk_fma_f32 v[152:153], v[152:153], s[50:51], v[172:173] op_sel_hi:[1,0,1]
	v_pk_fma_f32 v[118:119], v[118:119], s[50:51], v[154:155] op_sel_hi:[1,0,1]
	v_pk_fma_f32 v[120:121], v[120:121], s[50:51], v[156:157] op_sel_hi:[1,0,1]
	v_pk_fma_f32 v[104:105], v[104:105], s[50:51], v[158:159] op_sel_hi:[1,0,1]
	v_pk_fma_f32 v[122:123], v[122:123], s[50:51], v[160:161] op_sel_hi:[1,0,1]
	v_pk_fma_f32 v[142:143], v[142:143], s[50:51], v[162:163] op_sel_hi:[1,0,1]
	v_pk_fma_f32 v[106:107], v[106:107], s[50:51], v[174:175] op_sel_hi:[1,0,1]
	v_readlane_b32 s50, v249, 1
	v_cvt_scalef32_pk_f32_fp4 v[154:155], v100, 1.0
	v_cvt_scalef32_pk_f32_fp4 v[156:157], v100, 1.0 op_sel:[1,0,0]
	v_cvt_scalef32_pk_f32_fp4 v[158:159], v100, 1.0 op_sel:[0,1,0]
	v_cvt_scalef32_pk_f32_fp4 v[160:161], v100, 1.0 op_sel:[1,1,0]
	v_pk_fma_f32 v[108:109], v[154:155], s[50:51], v[108:109] op_sel_hi:[1,0,1]
	v_pk_fma_f32 v[110:111], v[156:157], s[50:51], v[110:111] op_sel_hi:[1,0,1]
	v_pk_fma_f32 v[112:113], v[158:159], s[50:51], v[112:113] op_sel_hi:[1,0,1]
	v_cvt_scalef32_pk_f32_fp4 v[154:155], v101, 1.0
	v_cvt_scalef32_pk_f32_fp4 v[156:157], v101, 1.0 op_sel:[1,0,0]
	v_cvt_scalef32_pk_f32_fp4 v[158:159], v101, 1.0 op_sel:[0,1,0]
	v_cvt_scalef32_pk_f32_fp4 v[100:101], v101, 1.0 op_sel:[1,1,0]
	v_pk_fma_f32 v[116:117], v[154:155], s[50:51], v[116:117] op_sel_hi:[1,0,1]
	v_pk_fma_f32 v[118:119], v[156:157], s[50:51], v[118:119] op_sel_hi:[1,0,1]
	v_pk_fma_f32 v[120:121], v[158:159], s[50:51], v[120:121] op_sel_hi:[1,0,1]
	v_pk_fma_f32 v[100:101], v[100:101], s[50:51], v[104:105] op_sel_hi:[1,0,1]
	v_cvt_scalef32_pk_f32_fp4 v[104:105], v102, 1.0
	v_cvt_scalef32_pk_f32_fp4 v[154:155], v102, 1.0 op_sel:[1,0,0]
	v_cvt_scalef32_pk_f32_fp4 v[156:157], v102, 1.0 op_sel:[0,1,0]
	v_cvt_scalef32_pk_f32_fp4 v[158:159], v102, 1.0 op_sel:[1,1,0]
	v_pk_fma_f32 v[104:105], v[104:105], s[50:51], v[122:123] op_sel_hi:[1,0,1]
	v_pk_fma_f32 v[122:123], v[154:155], s[50:51], v[142:143] op_sel_hi:[1,0,1]
	v_pk_fma_f32 v[142:143], v[156:157], s[50:51], v[144:145] op_sel_hi:[1,0,1]
	v_pk_fma_f32 v[144:145], v[158:159], s[50:51], v[146:147] op_sel_hi:[1,0,1]
	v_cvt_scalef32_pk_f32_fp4 v[146:147], v103, 1.0
	v_cvt_scalef32_pk_f32_fp4 v[154:155], v103, 1.0 op_sel:[1,0,0]
	v_cvt_scalef32_pk_f32_fp4 v[156:157], v103, 1.0 op_sel:[0,1,0]
	v_cvt_scalef32_pk_f32_fp4 v[102:103], v103, 1.0 op_sel:[1,1,0]
	v_pk_fma_f32 v[146:147], v[146:147], s[50:51], v[148:149] op_sel_hi:[1,0,1]
	v_pk_fma_f32 v[148:149], v[154:155], s[50:51], v[150:151] op_sel_hi:[1,0,1]
	v_pk_fma_f32 v[150:151], v[156:157], s[50:51], v[152:153] op_sel_hi:[1,0,1]
	v_pk_fma_f32 v[114:115], v[160:161], s[50:51], v[114:115] op_sel_hi:[1,0,1]
	v_pk_fma_f32 v[102:103], v[102:103], s[50:51], v[106:107] op_sel_hi:[1,0,1]
	v_readlane_b32 s50, v249, 2
	v_cvt_scalef32_pk_f32_fp4 v[106:107], v96, 1.0
	v_cvt_scalef32_pk_f32_fp4 v[152:153], v96, 1.0 op_sel:[1,0,0]
	v_cvt_scalef32_pk_f32_fp4 v[154:155], v96, 1.0 op_sel:[0,1,0]
	v_cvt_scalef32_pk_f32_fp4 v[156:157], v96, 1.0 op_sel:[1,1,0]
	v_pk_fma_f32 v[106:107], v[106:107], s[50:51], v[108:109] op_sel_hi:[1,0,1]
	v_pk_fma_f32 v[108:109], v[152:153], s[50:51], v[110:111] op_sel_hi:[1,0,1]
	v_pk_fma_f32 v[110:111], v[154:155], s[50:51], v[112:113] op_sel_hi:[1,0,1]
	v_pk_fma_f32 v[112:113], v[156:157], s[50:51], v[114:115] op_sel_hi:[1,0,1]
	v_cvt_scalef32_pk_f32_fp4 v[114:115], v97, 1.0
	v_cvt_scalef32_pk_f32_fp4 v[152:153], v97, 1.0 op_sel:[1,0,0]
	v_cvt_scalef32_pk_f32_fp4 v[154:155], v97, 1.0 op_sel:[0,1,0]
	v_cvt_scalef32_pk_f32_fp4 v[96:97], v97, 1.0 op_sel:[1,1,0]
	v_pk_fma_f32 v[114:115], v[114:115], s[50:51], v[116:117] op_sel_hi:[1,0,1]
	v_pk_fma_f32 v[116:117], v[152:153], s[50:51], v[118:119] op_sel_hi:[1,0,1]
	v_pk_fma_f32 v[118:119], v[154:155], s[50:51], v[120:121] op_sel_hi:[1,0,1]
	v_pk_fma_f32 v[96:97], v[96:97], s[50:51], v[100:101] op_sel_hi:[1,0,1]
	v_cvt_scalef32_pk_f32_fp4 v[100:101], v98, 1.0
	v_cvt_scalef32_pk_f32_fp4 v[120:121], v98, 1.0 op_sel:[1,0,0]
	v_cvt_scalef32_pk_f32_fp4 v[152:153], v98, 1.0 op_sel:[0,1,0]
	v_cvt_scalef32_pk_f32_fp4 v[154:155], v98, 1.0 op_sel:[1,1,0]
	v_pk_fma_f32 v[100:101], v[100:101], s[50:51], v[104:105] op_sel_hi:[1,0,1]
	v_pk_fma_f32 v[104:105], v[120:121], s[50:51], v[122:123] op_sel_hi:[1,0,1]
	v_pk_fma_f32 v[120:121], v[152:153], s[50:51], v[142:143] op_sel_hi:[1,0,1]
	v_pk_fma_f32 v[122:123], v[154:155], s[50:51], v[144:145] op_sel_hi:[1,0,1]
	v_cvt_scalef32_pk_f32_fp4 v[142:143], v99, 1.0
	v_cvt_scalef32_pk_f32_fp4 v[144:145], v99, 1.0 op_sel:[1,0,0]
	v_cvt_scalef32_pk_f32_fp4 v[152:153], v99, 1.0 op_sel:[0,1,0]
	v_cvt_scalef32_pk_f32_fp4 v[98:99], v99, 1.0 op_sel:[1,1,0]
	v_pk_fma_f32 v[142:143], v[142:143], s[50:51], v[146:147] op_sel_hi:[1,0,1]
	v_pk_fma_f32 v[144:145], v[144:145], s[50:51], v[148:149] op_sel_hi:[1,0,1]
	v_pk_fma_f32 v[146:147], v[152:153], s[50:51], v[150:151] op_sel_hi:[1,0,1]
	v_pk_fma_f32 v[98:99], v[98:99], s[50:51], v[102:103] op_sel_hi:[1,0,1]
	v_readlane_b32 s50, v249, 3
	v_cvt_scalef32_pk_f32_fp4 v[102:103], v92, 1.0
	v_cvt_scalef32_pk_f32_fp4 v[148:149], v92, 1.0 op_sel:[1,0,0]
	v_cvt_scalef32_pk_f32_fp4 v[150:151], v92, 1.0 op_sel:[0,1,0]
	v_cvt_scalef32_pk_f32_fp4 v[154:155], v92, 1.0 op_sel:[1,1,0]
	v_pk_fma_f32 v[152:153], v[102:103], s[50:51], v[106:107] op_sel_hi:[1,0,1]
	v_pk_fma_f32 v[174:175], v[148:149], s[50:51], v[108:109] op_sel_hi:[1,0,1]
	v_cvt_scalef32_pk_f32_fp4 v[102:103], v93, 1.0
	v_cvt_scalef32_pk_f32_fp4 v[106:107], v93, 1.0 op_sel:[1,0,0]
	v_cvt_scalef32_pk_f32_fp4 v[108:109], v93, 1.0 op_sel:[0,1,0]
	v_cvt_scalef32_pk_f32_fp4 v[92:93], v93, 1.0 op_sel:[1,1,0]
	v_pk_fma_f32 v[162:163], v[92:93], s[50:51], v[96:97] op_sel_hi:[1,0,1]
	v_cvt_scalef32_pk_f32_fp4 v[92:93], v94, 1.0
	v_cvt_scalef32_pk_f32_fp4 v[96:97], v94, 1.0 op_sel:[1,0,0]
	v_pk_fma_f32 v[168:169], v[102:103], s[50:51], v[114:115] op_sel_hi:[1,0,1]
	v_pk_fma_f32 v[166:167], v[106:107], s[50:51], v[116:117] op_sel_hi:[1,0,1]
	v_cvt_scalef32_pk_f32_fp4 v[102:103], v94, 1.0 op_sel:[0,1,0]
	v_cvt_scalef32_pk_f32_fp4 v[106:107], v94, 1.0 op_sel:[1,1,0]
	v_pk_fma_f32 v[160:161], v[92:93], s[50:51], v[100:101] op_sel_hi:[1,0,1]
	v_pk_fma_f32 v[158:159], v[96:97], s[50:51], v[104:105] op_sel_hi:[1,0,1]
	v_cvt_scalef32_pk_f32_fp4 v[92:93], v95, 1.0
	v_cvt_scalef32_pk_f32_fp4 v[96:97], v95, 1.0 op_sel:[1,0,0]
	v_cvt_scalef32_pk_f32_fp4 v[100:101], v95, 1.0 op_sel:[0,1,0]
	v_cvt_scalef32_pk_f32_fp4 v[94:95], v95, 1.0 op_sel:[1,1,0]
	v_pk_fma_f32 v[172:173], v[150:151], s[50:51], v[110:111] op_sel_hi:[1,0,1]
	v_pk_fma_f32 v[170:171], v[154:155], s[50:51], v[112:113] op_sel_hi:[1,0,1]
	v_pk_fma_f32 v[164:165], v[108:109], s[50:51], v[118:119] op_sel_hi:[1,0,1]
	v_pk_fma_f32 v[156:157], v[102:103], s[50:51], v[120:121] op_sel_hi:[1,0,1]
	v_pk_fma_f32 v[154:155], v[106:107], s[50:51], v[122:123] op_sel_hi:[1,0,1]
	v_pk_fma_f32 v[150:151], v[92:93], s[50:51], v[142:143] op_sel_hi:[1,0,1]
	v_pk_fma_f32 v[148:149], v[96:97], s[50:51], v[144:145] op_sel_hi:[1,0,1]
	v_pk_fma_f32 v[146:147], v[100:101], s[50:51], v[146:147] op_sel_hi:[1,0,1]
	v_pk_fma_f32 v[144:145], v[94:95], s[50:51], v[98:99] op_sel_hi:[1,0,1]
	s_add_i32 s8, s8, 48
	s_add_i32 s6, s6, 12
	s_cmpk_gt_u32 s6, 0x6b
	s_cbranch_scc0 .LBB0_776
	v_mov_b32_e32 v92, v3
	v_mov_b32_e32 v93, v3
	s_waitcnt vmcnt(17)
	v_dot8c_i32_i4_e32 v92, v88, v24
	v_dot8c_i32_i4_e32 v93, v88, v20
	v_dot8c_i32_i4_e32 v92, v89, v25
	v_dot8c_i32_i4_e32 v93, v89, v21
	v_dot8c_i32_i4_e32 v92, v90, v26
	v_dot8c_i32_i4_e32 v93, v90, v22
	v_mov_b32_e32 v89, v3
	v_mov_b32_e32 v90, v3
	s_waitcnt vmcnt(15)
	v_dot8c_i32_i4_e32 v89, v84, v24
	v_dot8c_i32_i4_e32 v90, v84, v20
	v_dot8c_i32_i4_e32 v89, v85, v25
	v_dot8c_i32_i4_e32 v90, v85, v21
	v_dot8c_i32_i4_e32 v89, v86, v26
	v_dot8c_i32_i4_e32 v90, v86, v22
	v_mov_b32_e32 v85, v3
	v_mov_b32_e32 v86, v3
	s_waitcnt vmcnt(12)
	v_dot8c_i32_i4_e32 v85, v80, v24
	v_dot8c_i32_i4_e32 v86, v80, v20
	v_dot8c_i32_i4_e32 v85, v81, v25
	v_dot8c_i32_i4_e32 v86, v81, v21
	v_dot8c_i32_i4_e32 v85, v82, v26
	v_dot8c_i32_i4_e32 v86, v82, v22
	v_mov_b32_e32 v81, v3
	v_mov_b32_e32 v82, v3
	s_waitcnt vmcnt(10)
	v_dot8c_i32_i4_e32 v81, v76, v24
	v_dot8c_i32_i4_e32 v82, v76, v20
	v_dot8c_i32_i4_e32 v81, v77, v25
	v_dot8c_i32_i4_e32 v82, v77, v21
	v_dot8c_i32_i4_e32 v92, v91, v27
	v_dot8c_i32_i4_e32 v93, v91, v23
	v_dot8c_i32_i4_e32 v89, v87, v27
	v_dot8c_i32_i4_e32 v90, v87, v23
	v_dot8c_i32_i4_e32 v81, v78, v26
	v_dot8c_i32_i4_e32 v82, v78, v22
	v_lshl_add_u32 v88, v92, 4, v93
	v_lshl_add_u32 v84, v89, 4, v90
	v_dot8c_i32_i4_e32 v85, v83, v27
	v_dot8c_i32_i4_e32 v86, v83, v23
	v_dot8c_i32_i4_e32 v81, v79, v27
	v_dot8c_i32_i4_e32 v82, v79, v23
	v_cvt_f32_i32_e32 v88, v88
	v_cvt_f32_i32_e32 v84, v84
	v_lshl_add_u32 v80, v85, 4, v86
	v_lshl_add_u32 v76, v81, 4, v82
	v_cvt_f32_i32_e32 v80, v80
	v_cvt_f32_i32_e32 v76, v76
	v_cndmask_b32_e64 v77, v84, v88, s[42:43]
	v_cndmask_b32_e64 v78, v88, v84, s[42:43]
	s_nop 1
	v_add_f32_dpp v77, v78, v77 quad_perm:[1,0,3,2] row_mask:0xf bank_mask:0xf bound_ctrl:1
	v_cndmask_b32_e64 v78, v76, v80, s[42:43]
	v_cndmask_b32_e64 v76, v80, v76, s[42:43]
	s_nop 1
	v_add_f32_dpp v76, v76, v78 quad_perm:[1,0,3,2] row_mask:0xf bank_mask:0xf bound_ctrl:1
	v_cndmask_b32_e64 v78, v76, v77, s[44:45]
	v_cndmask_b32_e64 v76, v77, v76, s[44:45]
	s_nop 1
	v_add_f32_dpp v76, v76, v78 quad_perm:[2,3,0,1] row_mask:0xf bank_mask:0xf bound_ctrl:1
	s_nop 1
	v_add_f32_dpp v76, v76, v76 row_ror:4 row_mask:0xf bank_mask:0xf bound_ctrl:1
	s_nop 1
	v_add_f32_dpp v76, v76, v76 row_ror:8 row_mask:0xf bank_mask:0xf bound_ctrl:1
	v_mov_b32_e32 v77, v76
	s_nop 1
	v_permlane32_swap_b32_e32 v76, v77
	v_add_f32_e32 v76, v76, v77
	v_mov_b32_e32 v77, v76
	s_nop 1
	v_permlane16_swap_b32_e32 v76, v77
	v_add_f32_e32 v76, v76, v77
	v_mul_f32_e32 v77, v248, v140
	v_mul_f32_e64 v76, v77, v76
	v_fma_f32 v77, |v76|, s39, 1.0
	v_rcp_f32_e32 v77, v77
	v_mul_f32_e32 v80, v76, v76
	v_mul_f32_e32 v80, 0xbf38aa3b, v80
	v_exp_f32_e64 v80, v80
	v_fmamk_f32 v79, v77, 0x3f07dc22, v210
	v_fmaak_f32 v79, v77, v79, 0x3f35f0e3
	v_fmaak_f32 v79, v77, v79, 0xbe11a98e
	ds_read_b32 v78, v184 offset:4320
	v_fmaak_f32 v79, v77, v79, 0x3e027906
	v_mul_f32_e32 v77, v77, v79
	v_mul_f32_e32 v77, v80, v77
	v_mul_f32_e64 v79, v76, v77
	v_fma_f32 v77, -v76, v77, v76
	v_cmp_gt_f32_e32 vcc, 0, v76
	s_nop 1
	v_cndmask_b32_e32 v76, v77, v79, vcc
	s_waitcnt lgkmcnt(0)
	v_mul_f32_e64 v76, v78, v76
	v_mul_f32_e32 v76, v141, v76
	s_nop 0
	v_readlane_b32 s8, v76, 0
	v_readlane_b32 s62, v76, 1
	v_readlane_b32 s58, v76, 2
	v_readlane_b32 s56, v76, 3
	v_mov_b32_e32 v76, v3
	v_mov_b32_e32 v77, v3
	s_waitcnt vmcnt(8)
	v_dot8c_i32_i4_e32 v76, v72, v24
	v_dot8c_i32_i4_e32 v77, v72, v20
	v_dot8c_i32_i4_e32 v76, v73, v25
	v_dot8c_i32_i4_e32 v77, v73, v21
	v_dot8c_i32_i4_e32 v76, v74, v26
	v_dot8c_i32_i4_e32 v77, v74, v22
	v_mov_b32_e32 v73, v3
	v_mov_b32_e32 v74, v3
	s_waitcnt vmcnt(6)
	v_dot8c_i32_i4_e32 v73, v68, v24
	v_dot8c_i32_i4_e32 v74, v68, v20
	v_dot8c_i32_i4_e32 v73, v69, v25
	v_dot8c_i32_i4_e32 v74, v69, v21
	v_dot8c_i32_i4_e32 v73, v70, v26
	v_dot8c_i32_i4_e32 v74, v70, v22
	v_mov_b32_e32 v69, v3
	v_mov_b32_e32 v70, v3
	s_waitcnt vmcnt(3)
	v_dot8c_i32_i4_e32 v69, v64, v24
	v_dot8c_i32_i4_e32 v70, v64, v20
	v_dot8c_i32_i4_e32 v69, v65, v25
	v_dot8c_i32_i4_e32 v70, v65, v21
	v_mov_b32_e32 v65, v3
	s_waitcnt vmcnt(1)
	v_dot8c_i32_i4_e32 v65, v60, v24
	v_mov_b32_e32 v24, v3
	v_dot8c_i32_i4_e32 v24, v60, v20
	v_dot8c_i32_i4_e32 v65, v61, v25
	v_dot8c_i32_i4_e32 v24, v61, v21
	v_dot8c_i32_i4_e32 v76, v75, v27
	v_dot8c_i32_i4_e32 v77, v75, v23
	v_dot8c_i32_i4_e32 v73, v71, v27
	v_dot8c_i32_i4_e32 v74, v71, v23
	v_dot8c_i32_i4_e32 v69, v66, v26
	v_dot8c_i32_i4_e32 v70, v66, v22
	v_dot8c_i32_i4_e32 v65, v62, v26
	v_dot8c_i32_i4_e32 v24, v62, v22
	v_lshl_add_u32 v72, v76, 4, v77
	v_lshl_add_u32 v68, v73, 4, v74
	v_dot8c_i32_i4_e32 v69, v67, v27
	v_dot8c_i32_i4_e32 v70, v67, v23
	v_dot8c_i32_i4_e32 v65, v63, v27
	v_dot8c_i32_i4_e32 v24, v63, v23
	v_cvt_f32_i32_e32 v72, v72
	v_cvt_f32_i32_e32 v68, v68
	v_lshl_add_u32 v64, v69, 4, v70
	v_lshl_add_u32 v20, v65, 4, v24
	v_cvt_f32_i32_e32 v64, v64
	v_cvt_f32_i32_e32 v20, v20
	v_cndmask_b32_e64 v21, v68, v72, s[42:43]
	v_cndmask_b32_e64 v22, v72, v68, s[42:43]
	s_nop 1
	v_add_f32_dpp v21, v22, v21 quad_perm:[1,0,3,2] row_mask:0xf bank_mask:0xf bound_ctrl:1
	v_cndmask_b32_e64 v22, v20, v64, s[42:43]
	v_cndmask_b32_e64 v20, v64, v20, s[42:43]
	s_nop 1
	v_add_f32_dpp v20, v20, v22 quad_perm:[1,0,3,2] row_mask:0xf bank_mask:0xf bound_ctrl:1
	v_cndmask_b32_e64 v22, v20, v21, s[44:45]
	v_cndmask_b32_e64 v20, v21, v20, s[44:45]
	s_nop 1
	v_add_f32_dpp v20, v20, v22 quad_perm:[2,3,0,1] row_mask:0xf bank_mask:0xf bound_ctrl:1
	s_nop 1
	v_add_f32_dpp v20, v20, v20 row_ror:4 row_mask:0xf bank_mask:0xf bound_ctrl:1
	s_nop 1
	v_add_f32_dpp v20, v20, v20 row_ror:8 row_mask:0xf bank_mask:0xf bound_ctrl:1
	v_mov_b32_e32 v21, v20
	s_nop 1
	v_permlane32_swap_b32_e32 v20, v21
	v_add_f32_e32 v20, v20, v21
	v_mov_b32_e32 v21, v20
	s_nop 1
	v_permlane16_swap_b32_e32 v20, v21
	v_add_f32_e32 v20, v20, v21
	v_mul_f32_e32 v21, v248, v138
	v_mul_f32_e64 v20, v21, v20
	v_fma_f32 v21, |v20|, s39, 1.0
	v_rcp_f32_e32 v21, v21
	v_mul_f32_e32 v24, v20, v20
	v_mul_f32_e32 v24, 0xbf38aa3b, v24
	v_exp_f32_e64 v24, v24
	v_fmamk_f32 v23, v21, 0x3f07dc22, v210
	v_fmaak_f32 v23, v21, v23, 0x3f35f0e3
	v_fmaak_f32 v23, v21, v23, 0xbe11a98e
	ds_read_b32 v22, v184 offset:4336
	v_fmaak_f32 v23, v21, v23, 0x3e027906
	v_mul_f32_e32 v21, v21, v23
	v_mul_f32_e32 v21, v24, v21
	v_mul_f32_e64 v23, v20, v21
	v_fma_f32 v21, -v20, v21, v20
	v_cmp_gt_f32_e32 vcc, 0, v20
	s_nop 1
	v_cndmask_b32_e32 v20, v21, v23, vcc
	s_waitcnt lgkmcnt(0)
	v_mul_f32_e64 v20, v22, v20
	v_mul_f32_e32 v20, v139, v20
	s_nop 0
	v_readlane_b32 s64, v20, 0
	v_readlane_b32 s60, v20, 1
	v_readlane_b32 s50, v20, 2
	v_readlane_b32 s6, v20, 3
	v_readfirstlane_b32 s52, v247
	s_cmp_ge_i32 s52, s26
	s_cselect_b64 s[54:55], -1, 0
	s_cmp_lt_i32 s52, s26
	s_cbranch_scc0 .LBB0_779
	s_ashr_i32 s53, s52, 31
	s_lshl_b64 s[80:81], s[52:53], 12
	v_lshl_add_u64 v[4:5], v[132:133], 0, s[80:81]
	global_load_dwordx4 v[8:11], v[4:5], off offset:48
	global_load_dwordx4 v[12:15], v[4:5], off offset:32
	global_load_dwordx4 v[16:19], v[4:5], off offset:16
	s_nop 0
	global_load_dwordx4 v[4:7], v[4:5], off
.LBB0_779:
	v_cvt_scalef32_pk_f32_fp4 v[20:21], v56, 1.0
	v_cvt_scalef32_pk_f32_fp4 v[22:23], v56, 1.0 op_sel:[1,0,0]
	v_cvt_scalef32_pk_f32_fp4 v[24:25], v56, 1.0 op_sel:[0,1,0]
	v_cvt_scalef32_pk_f32_fp4 v[26:27], v56, 1.0 op_sel:[1,1,0]
	v_pk_fma_f32 v[20:21], v[20:21], s[8:9], v[152:153] op_sel_hi:[1,0,1]
	v_pk_fma_f32 v[22:23], v[22:23], s[8:9], v[174:175] op_sel_hi:[1,0,1]
	v_pk_fma_f32 v[24:25], v[24:25], s[8:9], v[172:173] op_sel_hi:[1,0,1]
	v_cvt_scalef32_pk_f32_fp4 v[60:61], v57, 1.0
	v_cvt_scalef32_pk_f32_fp4 v[62:63], v57, 1.0 op_sel:[1,0,0]
	v_cvt_scalef32_pk_f32_fp4 v[64:65], v57, 1.0 op_sel:[0,1,0]
	v_cvt_scalef32_pk_f32_fp4 v[56:57], v57, 1.0 op_sel:[1,1,0]
	v_cvt_scalef32_pk_f32_fp4 v[80:81], v52, 1.0
	v_cvt_scalef32_pk_f32_fp4 v[82:83], v52, 1.0 op_sel:[1,0,0]
	v_cvt_scalef32_pk_f32_fp4 v[84:85], v52, 1.0 op_sel:[0,1,0]
	v_pk_fma_f32 v[60:61], v[60:61], s[8:9], v[168:169] op_sel_hi:[1,0,1]
	v_pk_fma_f32 v[62:63], v[62:63], s[8:9], v[166:167] op_sel_hi:[1,0,1]
	v_pk_fma_f32 v[64:65], v[64:65], s[8:9], v[164:165] op_sel_hi:[1,0,1]
	v_pk_fma_f32 v[56:57], v[56:57], s[8:9], v[162:163] op_sel_hi:[1,0,1]
	v_cvt_scalef32_pk_f32_fp4 v[66:67], v58, 1.0
	v_cvt_scalef32_pk_f32_fp4 v[68:69], v58, 1.0 op_sel:[1,0,0]
	v_cvt_scalef32_pk_f32_fp4 v[70:71], v58, 1.0 op_sel:[0,1,0]
	v_cvt_scalef32_pk_f32_fp4 v[72:73], v58, 1.0 op_sel:[1,1,0]
	v_cvt_scalef32_pk_f32_fp4 v[86:87], v52, 1.0 op_sel:[1,1,0]
	v_pk_fma_f32 v[20:21], v[80:81], s[62:63], v[20:21] op_sel_hi:[1,0,1]
	v_pk_fma_f32 v[22:23], v[82:83], s[62:63], v[22:23] op_sel_hi:[1,0,1]
	v_pk_fma_f32 v[24:25], v[84:85], s[62:63], v[24:25] op_sel_hi:[1,0,1]
	v_cvt_scalef32_pk_f32_fp4 v[80:81], v53, 1.0
	v_cvt_scalef32_pk_f32_fp4 v[82:83], v53, 1.0 op_sel:[1,0,0]
	v_cvt_scalef32_pk_f32_fp4 v[84:85], v53, 1.0 op_sel:[0,1,0]
	v_cvt_scalef32_pk_f32_fp4 v[52:53], v53, 1.0 op_sel:[1,1,0]
	v_pk_fma_f32 v[66:67], v[66:67], s[8:9], v[160:161] op_sel_hi:[1,0,1]
	v_pk_fma_f32 v[68:69], v[68:69], s[8:9], v[158:159] op_sel_hi:[1,0,1]
	v_pk_fma_f32 v[70:71], v[70:71], s[8:9], v[156:157] op_sel_hi:[1,0,1]
	v_pk_fma_f32 v[72:73], v[72:73], s[8:9], v[154:155] op_sel_hi:[1,0,1]
	v_cvt_scalef32_pk_f32_fp4 v[74:75], v59, 1.0
	v_cvt_scalef32_pk_f32_fp4 v[76:77], v59, 1.0 op_sel:[1,0,0]
	v_cvt_scalef32_pk_f32_fp4 v[78:79], v59, 1.0 op_sel:[0,1,0]
	v_cvt_scalef32_pk_f32_fp4 v[58:59], v59, 1.0 op_sel:[1,1,0]
	v_pk_fma_f32 v[60:61], v[80:81], s[62:63], v[60:61] op_sel_hi:[1,0,1]
	v_pk_fma_f32 v[62:63], v[82:83], s[62:63], v[62:63] op_sel_hi:[1,0,1]
	v_pk_fma_f32 v[64:65], v[84:85], s[62:63], v[64:65] op_sel_hi:[1,0,1]
	v_pk_fma_f32 v[52:53], v[52:53], s[62:63], v[56:57] op_sel_hi:[1,0,1]
	v_cvt_scalef32_pk_f32_fp4 v[56:57], v54, 1.0
	v_cvt_scalef32_pk_f32_fp4 v[80:81], v54, 1.0 op_sel:[1,0,0]
	v_cvt_scalef32_pk_f32_fp4 v[82:83], v54, 1.0 op_sel:[0,1,0]
	v_cvt_scalef32_pk_f32_fp4 v[84:85], v54, 1.0 op_sel:[1,1,0]
	v_pk_fma_f32 v[74:75], v[74:75], s[8:9], v[150:151] op_sel_hi:[1,0,1]
	v_pk_fma_f32 v[76:77], v[76:77], s[8:9], v[148:149] op_sel_hi:[1,0,1]
	v_pk_fma_f32 v[78:79], v[78:79], s[8:9], v[146:147] op_sel_hi:[1,0,1]
	v_pk_fma_f32 v[58:59], v[58:59], s[8:9], v[144:145] op_sel_hi:[1,0,1]
	v_pk_fma_f32 v[56:57], v[56:57], s[62:63], v[66:67] op_sel_hi:[1,0,1]
	v_pk_fma_f32 v[66:67], v[80:81], s[62:63], v[68:69] op_sel_hi:[1,0,1]
	v_pk_fma_f32 v[68:69], v[82:83], s[62:63], v[70:71] op_sel_hi:[1,0,1]
	v_pk_fma_f32 v[70:71], v[84:85], s[62:63], v[72:73] op_sel_hi:[1,0,1]
	v_cvt_scalef32_pk_f32_fp4 v[72:73], v55, 1.0
	v_cvt_scalef32_pk_f32_fp4 v[80:81], v55, 1.0 op_sel:[1,0,0]
	v_cvt_scalef32_pk_f32_fp4 v[82:83], v55, 1.0 op_sel:[0,1,0]
	v_cvt_scalef32_pk_f32_fp4 v[54:55], v55, 1.0 op_sel:[1,1,0]
	v_pk_fma_f32 v[72:73], v[72:73], s[62:63], v[74:75] op_sel_hi:[1,0,1]
	v_pk_fma_f32 v[74:75], v[80:81], s[62:63], v[76:77] op_sel_hi:[1,0,1]
	v_pk_fma_f32 v[76:77], v[82:83], s[62:63], v[78:79] op_sel_hi:[1,0,1]
	v_pk_fma_f32 v[54:55], v[54:55], s[62:63], v[58:59] op_sel_hi:[1,0,1]
	v_cvt_scalef32_pk_f32_fp4 v[58:59], v44, 1.0
	v_cvt_scalef32_pk_f32_fp4 v[78:79], v44, 1.0 op_sel:[1,0,0]
	v_cvt_scalef32_pk_f32_fp4 v[80:81], v44, 1.0 op_sel:[0,1,0]
	v_cvt_scalef32_pk_f32_fp4 v[82:83], v44, 1.0 op_sel:[1,1,0]
	v_pk_fma_f32 v[20:21], v[58:59], s[58:59], v[20:21] op_sel_hi:[1,0,1]
	v_pk_fma_f32 v[22:23], v[78:79], s[58:59], v[22:23] op_sel_hi:[1,0,1]
	v_pk_fma_f32 v[24:25], v[80:81], s[58:59], v[24:25] op_sel_hi:[1,0,1]
	v_cvt_scalef32_pk_f32_fp4 v[58:59], v45, 1.0
	v_cvt_scalef32_pk_f32_fp4 v[78:79], v45, 1.0 op_sel:[1,0,0]
	v_cvt_scalef32_pk_f32_fp4 v[80:81], v45, 1.0 op_sel:[0,1,0]
	v_cvt_scalef32_pk_f32_fp4 v[44:45], v45, 1.0 op_sel:[1,1,0]
	v_pk_fma_f32 v[58:59], v[58:59], s[58:59], v[60:61] op_sel_hi:[1,0,1]
	v_pk_fma_f32 v[60:61], v[78:79], s[58:59], v[62:63] op_sel_hi:[1,0,1]
	v_pk_fma_f32 v[62:63], v[80:81], s[58:59], v[64:65] op_sel_hi:[1,0,1]
	v_pk_fma_f32 v[44:45], v[44:45], s[58:59], v[52:53] op_sel_hi:[1,0,1]
	v_cvt_scalef32_pk_f32_fp4 v[52:53], v46, 1.0
	v_cvt_scalef32_pk_f32_fp4 v[64:65], v46, 1.0 op_sel:[1,0,0]
	v_cvt_scalef32_pk_f32_fp4 v[78:79], v46, 1.0 op_sel:[0,1,0]
	v_cvt_scalef32_pk_f32_fp4 v[80:81], v46, 1.0 op_sel:[1,1,0]
	v_pk_fma_f32 v[52:53], v[52:53], s[58:59], v[56:57] op_sel_hi:[1,0,1]
	v_pk_fma_f32 v[56:57], v[64:65], s[58:59], v[66:67] op_sel_hi:[1,0,1]
	v_pk_fma_f32 v[64:65], v[78:79], s[58:59], v[68:69] op_sel_hi:[1,0,1]
	v_pk_fma_f32 v[66:67], v[80:81], s[58:59], v[70:71] op_sel_hi:[1,0,1]
	v_cvt_scalef32_pk_f32_fp4 v[68:69], v47, 1.0
	v_cvt_scalef32_pk_f32_fp4 v[70:71], v47, 1.0 op_sel:[1,0,0]
	v_cvt_scalef32_pk_f32_fp4 v[78:79], v47, 1.0 op_sel:[0,1,0]
	v_cvt_scalef32_pk_f32_fp4 v[46:47], v47, 1.0 op_sel:[1,1,0]
	v_pk_fma_f32 v[68:69], v[68:69], s[58:59], v[72:73] op_sel_hi:[1,0,1]
	v_pk_fma_f32 v[70:71], v[70:71], s[58:59], v[74:75] op_sel_hi:[1,0,1]
	v_pk_fma_f32 v[72:73], v[78:79], s[58:59], v[76:77] op_sel_hi:[1,0,1]
	v_pk_fma_f32 v[46:47], v[46:47], s[58:59], v[54:55] op_sel_hi:[1,0,1]
	v_cvt_scalef32_pk_f32_fp4 v[54:55], v36, 1.0
	v_cvt_scalef32_pk_f32_fp4 v[74:75], v36, 1.0 op_sel:[1,0,0]
	v_cvt_scalef32_pk_f32_fp4 v[76:77], v36, 1.0 op_sel:[0,1,0]
	v_cvt_scalef32_pk_f32_fp4 v[78:79], v36, 1.0 op_sel:[1,1,0]
	v_pk_fma_f32 v[20:21], v[54:55], s[56:57], v[20:21] op_sel_hi:[1,0,1]
	v_pk_fma_f32 v[22:23], v[74:75], s[56:57], v[22:23] op_sel_hi:[1,0,1]
	v_pk_fma_f32 v[24:25], v[76:77], s[56:57], v[24:25] op_sel_hi:[1,0,1]
	v_cvt_scalef32_pk_f32_fp4 v[54:55], v37, 1.0
	v_cvt_scalef32_pk_f32_fp4 v[74:75], v37, 1.0 op_sel:[1,0,0]
	v_cvt_scalef32_pk_f32_fp4 v[76:77], v37, 1.0 op_sel:[0,1,0]
	v_cvt_scalef32_pk_f32_fp4 v[36:37], v37, 1.0 op_sel:[1,1,0]
	v_pk_fma_f32 v[54:55], v[54:55], s[56:57], v[58:59] op_sel_hi:[1,0,1]
	v_pk_fma_f32 v[58:59], v[74:75], s[56:57], v[60:61] op_sel_hi:[1,0,1]
	v_pk_fma_f32 v[60:61], v[76:77], s[56:57], v[62:63] op_sel_hi:[1,0,1]
	v_pk_fma_f32 v[36:37], v[36:37], s[56:57], v[44:45] op_sel_hi:[1,0,1]
	v_cvt_scalef32_pk_f32_fp4 v[44:45], v38, 1.0
	v_cvt_scalef32_pk_f32_fp4 v[62:63], v38, 1.0 op_sel:[1,0,0]
	v_cvt_scalef32_pk_f32_fp4 v[74:75], v38, 1.0 op_sel:[0,1,0]
	v_cvt_scalef32_pk_f32_fp4 v[76:77], v38, 1.0 op_sel:[1,1,0]
	v_pk_fma_f32 v[44:45], v[44:45], s[56:57], v[52:53] op_sel_hi:[1,0,1]
	v_pk_fma_f32 v[52:53], v[62:63], s[56:57], v[56:57] op_sel_hi:[1,0,1]
	v_pk_fma_f32 v[56:57], v[74:75], s[56:57], v[64:65] op_sel_hi:[1,0,1]
	v_pk_fma_f32 v[62:63], v[76:77], s[56:57], v[66:67] op_sel_hi:[1,0,1]
	v_cvt_scalef32_pk_f32_fp4 v[64:65], v39, 1.0
	v_cvt_scalef32_pk_f32_fp4 v[66:67], v39, 1.0 op_sel:[1,0,0]
	v_cvt_scalef32_pk_f32_fp4 v[74:75], v39, 1.0 op_sel:[0,1,0]
	v_cvt_scalef32_pk_f32_fp4 v[38:39], v39, 1.0 op_sel:[1,1,0]
	v_pk_fma_f32 v[26:27], v[26:27], s[8:9], v[170:171] op_sel_hi:[1,0,1]
	v_pk_fma_f32 v[64:65], v[64:65], s[56:57], v[68:69] op_sel_hi:[1,0,1]
	v_pk_fma_f32 v[66:67], v[66:67], s[56:57], v[70:71] op_sel_hi:[1,0,1]
	v_pk_fma_f32 v[68:69], v[74:75], s[56:57], v[72:73] op_sel_hi:[1,0,1]
	v_pk_fma_f32 v[38:39], v[38:39], s[56:57], v[46:47] op_sel_hi:[1,0,1]
	v_cvt_scalef32_pk_f32_fp4 v[46:47], v48, 1.0
	v_cvt_scalef32_pk_f32_fp4 v[70:71], v48, 1.0 op_sel:[1,0,0]
	v_cvt_scalef32_pk_f32_fp4 v[72:73], v48, 1.0 op_sel:[0,1,0]
	v_pk_fma_f32 v[26:27], v[86:87], s[62:63], v[26:27] op_sel_hi:[1,0,1]
	v_cvt_scalef32_pk_f32_fp4 v[74:75], v48, 1.0 op_sel:[1,1,0]
	v_pk_fma_f32 v[20:21], v[46:47], s[64:65], v[20:21] op_sel_hi:[1,0,1]
	v_pk_fma_f32 v[22:23], v[70:71], s[64:65], v[22:23] op_sel_hi:[1,0,1]
	v_pk_fma_f32 v[24:25], v[72:73], s[64:65], v[24:25] op_sel_hi:[1,0,1]
	v_cvt_scalef32_pk_f32_fp4 v[46:47], v49, 1.0
	v_cvt_scalef32_pk_f32_fp4 v[70:71], v49, 1.0 op_sel:[1,0,0]
	v_cvt_scalef32_pk_f32_fp4 v[72:73], v49, 1.0 op_sel:[0,1,0]
	v_cvt_scalef32_pk_f32_fp4 v[48:49], v49, 1.0 op_sel:[1,1,0]
	v_pk_fma_f32 v[26:27], v[82:83], s[58:59], v[26:27] op_sel_hi:[1,0,1]
	v_pk_fma_f32 v[46:47], v[46:47], s[64:65], v[54:55] op_sel_hi:[1,0,1]
	v_pk_fma_f32 v[54:55], v[70:71], s[64:65], v[58:59] op_sel_hi:[1,0,1]
	v_pk_fma_f32 v[58:59], v[72:73], s[64:65], v[60:61] op_sel_hi:[1,0,1]
	v_pk_fma_f32 v[36:37], v[48:49], s[64:65], v[36:37] op_sel_hi:[1,0,1]
	v_cvt_scalef32_pk_f32_fp4 v[48:49], v50, 1.0
	v_cvt_scalef32_pk_f32_fp4 v[60:61], v50, 1.0 op_sel:[1,0,0]
	v_cvt_scalef32_pk_f32_fp4 v[70:71], v50, 1.0 op_sel:[0,1,0]
	v_cvt_scalef32_pk_f32_fp4 v[72:73], v50, 1.0 op_sel:[1,1,0]
	v_pk_fma_f32 v[26:27], v[78:79], s[56:57], v[26:27] op_sel_hi:[1,0,1]
	v_pk_fma_f32 v[44:45], v[48:49], s[64:65], v[44:45] op_sel_hi:[1,0,1]
	v_pk_fma_f32 v[48:49], v[60:61], s[64:65], v[52:53] op_sel_hi:[1,0,1]
	v_pk_fma_f32 v[52:53], v[70:71], s[64:65], v[56:57] op_sel_hi:[1,0,1]
	v_pk_fma_f32 v[56:57], v[72:73], s[64:65], v[62:63] op_sel_hi:[1,0,1]
	v_cvt_scalef32_pk_f32_fp4 v[60:61], v51, 1.0
	v_cvt_scalef32_pk_f32_fp4 v[62:63], v51, 1.0 op_sel:[1,0,0]
	v_cvt_scalef32_pk_f32_fp4 v[70:71], v51, 1.0 op_sel:[0,1,0]
	v_cvt_scalef32_pk_f32_fp4 v[50:51], v51, 1.0 op_sel:[1,1,0]
	v_pk_fma_f32 v[26:27], v[74:75], s[64:65], v[26:27] op_sel_hi:[1,0,1]
	v_pk_fma_f32 v[60:61], v[60:61], s[64:65], v[64:65] op_sel_hi:[1,0,1]
	v_pk_fma_f32 v[62:63], v[62:63], s[64:65], v[66:67] op_sel_hi:[1,0,1]
	v_pk_fma_f32 v[64:65], v[70:71], s[64:65], v[68:69] op_sel_hi:[1,0,1]
	v_pk_fma_f32 v[38:39], v[50:51], s[64:65], v[38:39] op_sel_hi:[1,0,1]
	v_cvt_scalef32_pk_f32_fp4 v[50:51], v40, 1.0
	v_cvt_scalef32_pk_f32_fp4 v[66:67], v40, 1.0 op_sel:[1,0,0]
	v_cvt_scalef32_pk_f32_fp4 v[68:69], v40, 1.0 op_sel:[0,1,0]
	v_cvt_scalef32_pk_f32_fp4 v[70:71], v40, 1.0 op_sel:[1,1,0]
	v_pk_fma_f32 v[50:51], v[50:51], s[60:61], v[20:21] op_sel_hi:[1,0,1]
	v_pk_fma_f32 v[66:67], v[66:67], s[60:61], v[22:23] op_sel_hi:[1,0,1]
	v_pk_fma_f32 v[68:69], v[68:69], s[60:61], v[24:25] op_sel_hi:[1,0,1]
	v_pk_fma_f32 v[70:71], v[70:71], s[60:61], v[26:27] op_sel_hi:[1,0,1]
	v_cvt_scalef32_pk_f32_fp4 v[20:21], v41, 1.0
	v_cvt_scalef32_pk_f32_fp4 v[22:23], v41, 1.0 op_sel:[1,0,0]
	v_cvt_scalef32_pk_f32_fp4 v[24:25], v41, 1.0 op_sel:[0,1,0]
	v_cvt_scalef32_pk_f32_fp4 v[26:27], v41, 1.0 op_sel:[1,1,0]
	v_pk_fma_f32 v[40:41], v[20:21], s[60:61], v[46:47] op_sel_hi:[1,0,1]
	v_pk_fma_f32 v[46:47], v[22:23], s[60:61], v[54:55] op_sel_hi:[1,0,1]
	v_pk_fma_f32 v[54:55], v[24:25], s[60:61], v[58:59] op_sel_hi:[1,0,1]
	v_pk_fma_f32 v[36:37], v[26:27], s[60:61], v[36:37] op_sel_hi:[1,0,1]
	v_cvt_scalef32_pk_f32_fp4 v[20:21], v42, 1.0
	v_cvt_scalef32_pk_f32_fp4 v[22:23], v42, 1.0 op_sel:[1,0,0]
	v_cvt_scalef32_pk_f32_fp4 v[24:25], v42, 1.0 op_sel:[0,1,0]
	v_cvt_scalef32_pk_f32_fp4 v[26:27], v42, 1.0 op_sel:[1,1,0]
	v_pk_fma_f32 v[44:45], v[20:21], s[60:61], v[44:45] op_sel_hi:[1,0,1]
	v_pk_fma_f32 v[48:49], v[22:23], s[60:61], v[48:49] op_sel_hi:[1,0,1]
	v_pk_fma_f32 v[58:59], v[24:25], s[60:61], v[52:53] op_sel_hi:[1,0,1]
	v_pk_fma_f32 v[56:57], v[26:27], s[60:61], v[56:57] op_sel_hi:[1,0,1]
	v_cvt_scalef32_pk_f32_fp4 v[20:21], v43, 1.0
	v_cvt_scalef32_pk_f32_fp4 v[22:23], v43, 1.0 op_sel:[1,0,0]
	v_cvt_scalef32_pk_f32_fp4 v[24:25], v43, 1.0 op_sel:[0,1,0]
	v_cvt_scalef32_pk_f32_fp4 v[26:27], v43, 1.0 op_sel:[1,1,0]
	v_lshl_add_u64 v[52:53], s[74:75], 1, v[134:135]
	v_pk_fma_f32 v[42:43], v[20:21], s[60:61], v[60:61] op_sel_hi:[1,0,1]
	v_pk_fma_f32 v[60:61], v[22:23], s[60:61], v[62:63] op_sel_hi:[1,0,1]
	v_pk_fma_f32 v[62:63], v[24:25], s[60:61], v[64:65] op_sel_hi:[1,0,1]
	v_pk_fma_f32 v[38:39], v[26:27], s[60:61], v[38:39] op_sel_hi:[1,0,1]
	global_load_dwordx4 v[20:23], v[52:53], off offset:16
	global_load_dwordx4 v[24:27], v[52:53], off
	v_cvt_scalef32_pk_f32_fp4 v[64:65], v32, 1.0
	v_cvt_scalef32_pk_f32_fp4 v[72:73], v32, 1.0 op_sel:[1,0,0]
	v_cvt_scalef32_pk_f32_fp4 v[74:75], v32, 1.0 op_sel:[0,1,0]
	v_cvt_scalef32_pk_f32_fp4 v[76:77], v32, 1.0 op_sel:[1,1,0]
	v_pk_fma_f32 v[50:51], v[64:65], s[50:51], v[50:51] op_sel_hi:[1,0,1]
	v_pk_fma_f32 v[64:65], v[72:73], s[50:51], v[66:67] op_sel_hi:[1,0,1]
	v_pk_fma_f32 v[66:67], v[74:75], s[50:51], v[68:69] op_sel_hi:[1,0,1]
	v_pk_fma_f32 v[68:69], v[76:77], s[50:51], v[70:71] op_sel_hi:[1,0,1]
	v_cvt_scalef32_pk_f32_fp4 v[70:71], v33, 1.0
	v_cvt_scalef32_pk_f32_fp4 v[72:73], v33, 1.0 op_sel:[1,0,0]
	v_cvt_scalef32_pk_f32_fp4 v[74:75], v33, 1.0 op_sel:[0,1,0]
	v_cvt_scalef32_pk_f32_fp4 v[32:33], v33, 1.0 op_sel:[1,1,0]
	v_pk_fma_f32 v[40:41], v[70:71], s[50:51], v[40:41] op_sel_hi:[1,0,1]
	v_pk_fma_f32 v[46:47], v[72:73], s[50:51], v[46:47] op_sel_hi:[1,0,1]
	v_pk_fma_f32 v[32:33], v[32:33], s[50:51], v[36:37] op_sel_hi:[1,0,1]
	v_cvt_scalef32_pk_f32_fp4 v[36:37], v34, 1.0
	v_cvt_scalef32_pk_f32_fp4 v[70:71], v34, 1.0 op_sel:[1,0,0]
	v_cvt_scalef32_pk_f32_fp4 v[72:73], v34, 1.0 op_sel:[0,1,0]
	v_pk_fma_f32 v[54:55], v[74:75], s[50:51], v[54:55] op_sel_hi:[1,0,1]
	v_cvt_scalef32_pk_f32_fp4 v[74:75], v34, 1.0 op_sel:[1,1,0]
	v_pk_fma_f32 v[44:45], v[36:37], s[50:51], v[44:45] op_sel_hi:[1,0,1]
	v_pk_fma_f32 v[48:49], v[70:71], s[50:51], v[48:49] op_sel_hi:[1,0,1]
	v_pk_fma_f32 v[58:59], v[72:73], s[50:51], v[58:59] op_sel_hi:[1,0,1]
	v_cvt_scalef32_pk_f32_fp4 v[36:37], v35, 1.0
	v_cvt_scalef32_pk_f32_fp4 v[70:71], v35, 1.0 op_sel:[1,0,0]
	v_cvt_scalef32_pk_f32_fp4 v[72:73], v35, 1.0 op_sel:[0,1,0]
	v_cvt_scalef32_pk_f32_fp4 v[34:35], v35, 1.0 op_sel:[1,1,0]
	v_pk_fma_f32 v[42:43], v[36:37], s[50:51], v[42:43] op_sel_hi:[1,0,1]
	v_pk_fma_f32 v[60:61], v[70:71], s[50:51], v[60:61] op_sel_hi:[1,0,1]
	v_pk_fma_f32 v[70:71], v[34:35], s[50:51], v[38:39] op_sel_hi:[1,0,1]
	s_waitcnt vmcnt(2)
	v_cvt_scalef32_pk_f32_fp4 v[34:35], v28, 1.0
	v_cvt_scalef32_pk_f32_fp4 v[36:37], v28, 1.0 op_sel:[1,0,0]
	v_cvt_scalef32_pk_f32_fp4 v[38:39], v28, 1.0 op_sel:[0,1,0]
	v_pk_fma_f32 v[56:57], v[74:75], s[50:51], v[56:57] op_sel_hi:[1,0,1]
	v_pk_fma_f32 v[62:63], v[72:73], s[50:51], v[62:63] op_sel_hi:[1,0,1]
	v_cvt_scalef32_pk_f32_fp4 v[72:73], v28, 1.0 op_sel:[1,1,0]
	v_pk_fma_f32 v[74:75], v[34:35], s[6:7], v[50:51] op_sel_hi:[1,0,1]
	v_pk_fma_f32 v[76:77], v[36:37], s[6:7], v[64:65] op_sel_hi:[1,0,1]
	v_pk_fma_f32 v[78:79], v[38:39], s[6:7], v[66:67] op_sel_hi:[1,0,1]
	v_cvt_scalef32_pk_f32_fp4 v[34:35], v29, 1.0
	v_cvt_scalef32_pk_f32_fp4 v[36:37], v29, 1.0 op_sel:[1,0,0]
	v_cvt_scalef32_pk_f32_fp4 v[38:39], v29, 1.0 op_sel:[0,1,0]
	v_cvt_scalef32_pk_f32_fp4 v[28:29], v29, 1.0 op_sel:[1,1,0]
	v_pk_fma_f32 v[82:83], v[34:35], s[6:7], v[40:41] op_sel_hi:[1,0,1]
	v_pk_fma_f32 v[84:85], v[36:37], s[6:7], v[46:47] op_sel_hi:[1,0,1]
	v_pk_fma_f32 v[54:55], v[38:39], s[6:7], v[54:55] op_sel_hi:[1,0,1]
	v_pk_fma_f32 v[86:87], v[28:29], s[6:7], v[32:33] op_sel_hi:[1,0,1]
	global_load_dwordx4 v[32:35], v[52:53], off offset:48
	global_load_dwordx4 v[36:39], v[52:53], off offset:32
	v_cvt_scalef32_pk_f32_fp4 v[28:29], v30, 1.0
	v_cvt_scalef32_pk_f32_fp4 v[40:41], v30, 1.0 op_sel:[1,0,0]
	v_cvt_scalef32_pk_f32_fp4 v[46:47], v30, 1.0 op_sel:[0,1,0]
	v_cvt_scalef32_pk_f32_fp4 v[50:51], v30, 1.0 op_sel:[1,1,0]
	v_pk_fma_f32 v[88:89], v[28:29], s[6:7], v[44:45] op_sel_hi:[1,0,1]
	v_pk_fma_f32 v[90:91], v[40:41], s[6:7], v[48:49] op_sel_hi:[1,0,1]
	v_cvt_scalef32_pk_f32_fp4 v[28:29], v31, 1.0
	v_cvt_scalef32_pk_f32_fp4 v[40:41], v31, 1.0 op_sel:[1,0,0]
	v_cvt_scalef32_pk_f32_fp4 v[44:45], v31, 1.0 op_sel:[0,1,0]
	v_cvt_scalef32_pk_f32_fp4 v[30:31], v31, 1.0 op_sel:[1,1,0]
	v_pk_fma_f32 v[80:81], v[72:73], s[6:7], v[68:69] op_sel_hi:[1,0,1]
	v_pk_fma_f32 v[92:93], v[46:47], s[6:7], v[58:59] op_sel_hi:[1,0,1]
	v_pk_fma_f32 v[94:95], v[50:51], s[6:7], v[56:57] op_sel_hi:[1,0,1]
	v_pk_fma_f32 v[96:97], v[28:29], s[6:7], v[42:43] op_sel_hi:[1,0,1]
	v_pk_fma_f32 v[98:99], v[40:41], s[6:7], v[60:61] op_sel_hi:[1,0,1]
	v_pk_fma_f32 v[100:101], v[44:45], s[6:7], v[62:63] op_sel_hi:[1,0,1]
	v_pk_fma_f32 v[102:103], v[30:31], s[6:7], v[70:71] op_sel_hi:[1,0,1]
	s_lshr_b32 s6, s89, 19
	s_add_i32 s6, s88, s6
	s_and_b32 s6, s6, 0xffffe000
	s_cmpk_lt_i32 s88, 0x4000
	s_cselect_b64 s[56:57], -1, 0
	s_and_b64 s[8:9], s[56:57], exec
	s_cselect_b32 s6, s6, 0x4000
	v_add_u32_e64 v56, s6, v176
	ds_read_b128 v[28:31], v56 offset:41472
	ds_read_b128 v[40:43], v56 offset:42496
	ds_read_b128 v[44:47], v56 offset:43520
	ds_read_b128 v[48:51], v56 offset:44544
	ds_read_b128 v[58:61], v56 offset:45568
	ds_read_b128 v[62:65], v56 offset:46592
	ds_read_b128 v[66:69], v56 offset:47616
	ds_read_b128 v[70:73], v56 offset:48640
	s_waitcnt lgkmcnt(6)
	v_pk_mul_f32 v[42:43], v[80:81], v[42:43]
	s_waitcnt vmcnt(2)
	v_lshlrev_b32_e64 v104, 16, v27
	v_and_b32_e32 v105, 0xffff0000, v27
	v_lshlrev_b32_e64 v80, 16, v26
	v_and_b32_e32 v81, 0xffff0000, v26
	v_pk_mul_f32 v[26:27], v[78:79], v[40:41]
	v_lshlrev_b32_e64 v40, 16, v25
	v_and_b32_e32 v41, 0xffff0000, v25
	v_pk_mul_f32 v[40:41], v[40:41], s[34:35] op_sel_hi:[1,0]
	v_pk_fma_f32 v[26:27], v[80:81], s[34:35], v[26:27] op_sel_hi:[1,0,1]
	v_pk_fma_f32 v[30:31], v[76:77], v[30:31], v[40:41]
	v_lshlrev_b32_e64 v40, 16, v24
	v_and_b32_e32 v41, 0xffff0000, v24
	v_pk_mul_f32 v[24:25], v[40:41], s[34:35] op_sel_hi:[1,0]
	v_pk_fma_f32 v[42:43], v[104:105], s[34:35], v[42:43] op_sel_hi:[1,0,1]
	v_pk_fma_f32 v[24:25], v[74:75], v[28:29], v[24:25]
	v_and_b32_e32 v29, 0xffff0000, v23
	v_add_f32_e32 v28, 0, v24
	v_add_f32_e32 v28, v25, v28
	v_add_f32_e32 v28, v30, v28
	v_add_f32_e32 v28, v31, v28
	v_add_f32_e32 v28, v26, v28
	v_add_f32_e32 v28, v27, v28
	v_add_f32_e32 v28, v42, v28
	v_add_f32_e32 v57, v43, v28
	v_lshlrev_b32_e32 v28, 16, v23
	s_waitcnt lgkmcnt(4)
	v_pk_mul_f32 v[40:41], v[86:87], v[50:51]
	s_nop 0
	v_pk_fma_f32 v[28:29], v[28:29], s[34:35], v[40:41] op_sel_hi:[1,0,1]
	v_lshlrev_b32_e32 v40, 16, v22
	v_and_b32_e32 v41, 0xffff0000, v22
	v_pk_mul_f32 v[22:23], v[54:55], v[48:49]
	s_nop 0
	v_pk_fma_f32 v[22:23], v[40:41], s[34:35], v[22:23] op_sel_hi:[1,0,1]
	v_lshlrev_b32_e32 v40, 16, v21
	v_and_b32_e32 v41, 0xffff0000, v21
	v_pk_mul_f32 v[40:41], v[40:41], s[34:35] op_sel_hi:[1,0]
	s_nop 0
	v_pk_fma_f32 v[46:47], v[84:85], v[46:47], v[40:41]
	v_lshlrev_b32_e32 v40, 16, v20
	v_and_b32_e32 v41, 0xffff0000, v20
	v_pk_mul_f32 v[20:21], v[40:41], s[34:35] op_sel_hi:[1,0]
	s_waitcnt vmcnt(0)
	v_and_b32_e32 v41, 0xffff0000, v39
	v_pk_fma_f32 v[20:21], v[82:83], v[44:45], v[20:21]
	s_waitcnt lgkmcnt(2)
	v_pk_mul_f32 v[44:45], v[94:95], v[64:65]
	v_add_f32_e32 v40, v20, v57
	v_add_f32_e32 v40, v21, v40
	v_add_f32_e32 v40, v46, v40
	v_add_f32_e32 v40, v47, v40
	v_add_f32_e32 v40, v22, v40
	v_add_f32_e32 v40, v23, v40
	v_add_f32_e32 v40, v28, v40
	v_add_f32_e32 v57, v29, v40
	v_lshlrev_b32_e64 v40, 16, v39
	v_pk_fma_f32 v[44:45], v[40:41], s[34:35], v[44:45] op_sel_hi:[1,0,1]
	v_lshlrev_b32_e64 v40, 16, v38
	v_and_b32_e32 v41, 0xffff0000, v38
	v_pk_mul_f32 v[38:39], v[92:93], v[62:63]
	s_nop 0
	v_pk_fma_f32 v[48:49], v[40:41], s[34:35], v[38:39] op_sel_hi:[1,0,1]
	v_lshlrev_b32_e32 v38, 16, v37
	v_and_b32_e32 v39, 0xffff0000, v37
	v_pk_mul_f32 v[38:39], v[38:39], s[34:35] op_sel_hi:[1,0]
	s_nop 0
	v_pk_fma_f32 v[50:51], v[90:91], v[60:61], v[38:39]
	v_lshlrev_b32_e32 v38, 16, v36
	v_and_b32_e32 v39, 0xffff0000, v36
	v_pk_mul_f32 v[36:37], v[38:39], s[34:35] op_sel_hi:[1,0]
	s_waitcnt lgkmcnt(0)
	v_pk_mul_f32 v[38:39], v[102:103], v[72:73]
	v_pk_fma_f32 v[54:55], v[88:89], v[58:59], v[36:37]
	v_and_b32_e32 v37, 0xffff0000, v35
	v_add_f32_e32 v36, v54, v57
	v_add_f32_e32 v36, v55, v36
	v_add_f32_e32 v36, v50, v36
	v_add_f32_e32 v36, v51, v36
	v_add_f32_e32 v36, v48, v36
	v_add_f32_e32 v36, v49, v36
	v_add_f32_e32 v36, v44, v36
	v_add_f32_e32 v40, v45, v36
	v_lshlrev_b32_e32 v36, 16, v35
	v_pk_fma_f32 v[58:59], v[36:37], s[34:35], v[38:39] op_sel_hi:[1,0,1]
	v_lshlrev_b32_e64 v36, 16, v34
	v_and_b32_e32 v37, 0xffff0000, v34
	v_pk_mul_f32 v[34:35], v[100:101], v[70:71]
	s_nop 0
	v_pk_fma_f32 v[60:61], v[36:37], s[34:35], v[34:35] op_sel_hi:[1,0,1]
	v_lshlrev_b32_e32 v34, 16, v33
	v_and_b32_e32 v35, 0xffff0000, v33
	v_pk_mul_f32 v[34:35], v[34:35], s[34:35] op_sel_hi:[1,0]
	s_nop 0
	v_pk_fma_f32 v[62:63], v[98:99], v[68:69], v[34:35]
	v_lshlrev_b32_e32 v34, 16, v32
	v_and_b32_e32 v35, 0xffff0000, v32
	v_pk_mul_f32 v[32:33], v[34:35], s[34:35] op_sel_hi:[1,0]
	s_nop 0
	v_pk_fma_f32 v[64:65], v[96:97], v[66:67], v[32:33]
	s_nop 0
	v_add_f32_e32 v32, v64, v40
	v_add_f32_e32 v32, v65, v32
	v_add_f32_e32 v32, v62, v32
	v_add_f32_e32 v32, v63, v32
	v_add_f32_e32 v32, v60, v32
	v_add_f32_e32 v32, v61, v32
	v_add_f32_e64 v32, v58, v32
	v_add_f32_e32 v32, v59, v32
	s_nop 1
	v_add_f32_dpp v32, v32, v32 quad_perm:[1,0,3,2] row_mask:0xf bank_mask:0xf bound_ctrl:1
	s_nop 1
	v_add_f32_dpp v32, v32, v32 quad_perm:[2,3,0,1] row_mask:0xf bank_mask:0xf bound_ctrl:1
	s_nop 1
	v_add_f32_dpp v32, v32, v32 row_ror:4 row_mask:0xf bank_mask:0xf bound_ctrl:1
	s_nop 1
	v_add_f32_dpp v32, v32, v32 row_ror:8 row_mask:0xf bank_mask:0xf bound_ctrl:1
	s_nop 0
	v_readlane_b32 s6, v32, 16
	v_readlane_b32 s50, v32, 48
	v_readlane_b32 s8, v32, 0
	v_readlane_b32 s9, v32, 32
	v_mov_b32_e32 v32, s6
	v_mov_b32_e32 v33, s50
	v_pk_add_f32 v[32:33], s[8:9], v[32:33]
	s_nop 0
	v_add_f32_e32 v32, v32, v33
	v_mul_f32_e32 v66, 0x3a000000, v32
	v_pk_add_f32 v[68:69], v[24:25], v[66:67] op_sel_hi:[1,0] neg_lo:[0,1] neg_hi:[0,1]
	v_pk_add_f32 v[72:73], v[30:31], v[66:67] op_sel_hi:[1,0] neg_lo:[0,1] neg_hi:[0,1]
	v_pk_mul_f32 v[70:71], v[68:69], v[68:69]
	v_pk_mul_f32 v[74:75], v[72:73], v[72:73]
	v_add_f32_e64 v57, v70, v71
	v_pk_add_f32 v[40:41], v[26:27], v[66:67] op_sel_hi:[1,0] neg_lo:[0,1] neg_hi:[0,1]
	v_add_f32_e64 v57, v74, v57
	v_pk_mul_f32 v[76:77], v[40:41], v[40:41]
	v_add_f32_e64 v57, v75, v57
	v_pk_add_f32 v[42:43], v[42:43], v[66:67] op_sel_hi:[1,0] neg_lo:[0,1] neg_hi:[0,1]
	v_add_f32_e64 v57, v76, v57
	v_pk_mul_f32 v[78:79], v[42:43], v[42:43]
	v_add_f32_e64 v57, v77, v57
	v_pk_add_f32 v[36:37], v[20:21], v[66:67] op_sel_hi:[1,0] neg_lo:[0,1] neg_hi:[0,1]
	v_add_f32_e64 v57, v78, v57
	v_pk_mul_f32 v[80:81], v[36:37], v[36:37]
	v_add_f32_e64 v57, v79, v57
	v_pk_add_f32 v[38:39], v[46:47], v[66:67] op_sel_hi:[1,0] neg_lo:[0,1] neg_hi:[0,1]
	v_add_f32_e64 v57, v80, v57
	v_pk_mul_f32 v[46:47], v[38:39], v[38:39]
	v_add_f32_e64 v57, v81, v57
	v_pk_add_f32 v[32:33], v[22:23], v[66:67] op_sel_hi:[1,0] neg_lo:[0,1] neg_hi:[0,1]
	v_add_f32_e64 v46, v46, v57
	v_pk_mul_f32 v[82:83], v[32:33], v[32:33]
	v_add_f32_e64 v46, v47, v46
	v_pk_add_f32 v[34:35], v[28:29], v[66:67] op_sel_hi:[1,0] neg_lo:[0,1] neg_hi:[0,1]
	v_add_f32_e64 v46, v82, v46
	v_pk_mul_f32 v[84:85], v[34:35], v[34:35]
	v_add_f32_e64 v46, v83, v46
	v_pk_add_f32 v[28:29], v[54:55], v[66:67] op_sel_hi:[1,0] neg_lo:[0,1] neg_hi:[0,1]
	v_add_f32_e64 v46, v84, v46
	v_pk_mul_f32 v[54:55], v[28:29], v[28:29]
	v_add_f32_e64 v46, v85, v46
	v_pk_add_f32 v[30:31], v[50:51], v[66:67] op_sel_hi:[1,0] neg_lo:[0,1] neg_hi:[0,1]
	v_add_f32_e64 v46, v54, v46
	v_pk_mul_f32 v[86:87], v[30:31], v[30:31]
	v_add_f32_e64 v46, v55, v46
	v_pk_add_f32 v[24:25], v[48:49], v[66:67] op_sel_hi:[1,0] neg_lo:[0,1] neg_hi:[0,1]
	v_add_f32_e64 v46, v86, v46
	v_pk_mul_f32 v[88:89], v[24:25], v[24:25]
	v_add_f32_e64 v46, v87, v46
	v_pk_add_f32 v[26:27], v[44:45], v[66:67] op_sel_hi:[1,0] neg_lo:[0,1] neg_hi:[0,1]
	v_add_f32_e64 v46, v88, v46
	v_pk_mul_f32 v[44:45], v[26:27], v[26:27]
	v_add_f32_e64 v46, v89, v46
	v_pk_add_f32 v[20:21], v[64:65], v[66:67] op_sel_hi:[1,0] neg_lo:[0,1] neg_hi:[0,1]
	v_add_f32_e64 v44, v44, v46
	v_pk_mul_f32 v[64:65], v[20:21], v[20:21]
	v_add_f32_e64 v44, v45, v44
	v_pk_add_f32 v[22:23], v[62:63], v[66:67] op_sel_hi:[1,0] neg_lo:[0,1] neg_hi:[0,1]
	v_add_f32_e64 v44, v64, v44
	v_pk_mul_f32 v[62:63], v[22:23], v[22:23]
	v_add_f32_e64 v44, v65, v44
	v_pk_add_f32 v[48:49], v[60:61], v[66:67] op_sel_hi:[1,0] neg_lo:[0,1] neg_hi:[0,1]
	v_add_f32_e64 v44, v62, v44
	v_pk_mul_f32 v[60:61], v[48:49], v[48:49]
	v_add_f32_e64 v44, v63, v44
	v_pk_add_f32 v[50:51], v[58:59], v[66:67] op_sel_hi:[1,0] neg_lo:[0,1] neg_hi:[0,1]
	v_add_f32_e64 v44, v60, v44
	v_pk_mul_f32 v[58:59], v[50:51], v[50:51]
	v_add_f32_e32 v44, v61, v44
	v_add_f32_e32 v44, v58, v44
	v_add_f32_e32 v44, v59, v44
	s_nop 1
	v_add_f32_dpp v44, v44, v44 quad_perm:[1,0,3,2] row_mask:0xf bank_mask:0xf bound_ctrl:1
	s_nop 1
	v_add_f32_dpp v44, v44, v44 quad_perm:[2,3,0,1] row_mask:0xf bank_mask:0xf bound_ctrl:1
	s_nop 1
	v_add_f32_dpp v44, v44, v44 row_ror:4 row_mask:0xf bank_mask:0xf bound_ctrl:1
	s_nop 1
	v_add_f32_dpp v44, v44, v44 row_ror:8 row_mask:0xf bank_mask:0xf bound_ctrl:1
	s_nop 0
	v_readlane_b32 s6, v44, 16
	v_readlane_b32 s50, v44, 48
	v_readlane_b32 s8, v44, 0
	v_readlane_b32 s9, v44, 32
	v_mov_b32_e32 v44, s6
	v_mov_b32_e32 v45, s50
	v_pk_add_f32 v[44:45], s[8:9], v[44:45]
	s_nop 0
	v_add_f32_e32 v44, v44, v45
	v_fmamk_f32 v44, v44, 0x3a000000, v207
	v_mul_f32_e32 v45, 0x4f800000, v44
	v_cmp_gt_f32_e32 vcc, s10, v44
	s_nop 1
	v_cndmask_b32_e32 v44, v44, v45, vcc
	v_sqrt_f32_e32 v45, v44
	s_nop 0
	v_add_u32_e32 v46, -1, v45
	v_fma_f32 v47, -v46, v45, v44
	v_cmp_ge_f32_e64 s[50:51], 0, v47
	v_add_u32_e32 v47, 1, v45
	s_nop 0
	v_cndmask_b32_e64 v46, v45, v46, s[50:51]
	v_fma_f32 v45, -v47, v45, v44
	v_cmp_lt_f32_e64 s[50:51], 0, v45
	s_nop 1
	v_cndmask_b32_e64 v45, v46, v47, s[50:51]
	v_mul_f32_e32 v46, 0x37800000, v45
	v_cndmask_b32_e32 v45, v45, v46, vcc
	v_cmp_class_f32_e32 vcc, v44, v208
	s_nop 1
	v_cndmask_b32_e64 v54, v45, v44, vcc
	v_div_scale_f32 v55, s[8:9], v54, v54, 1.0
	v_rcp_f32_e64 v57, v55
	ds_read_b128 v[44:47], v185
	ds_read_b128 v[58:61], v186
	s_and_b64 s[8:9], s[92:93], s[56:57]
	v_fma_f32 v62, -v55, v57, 1.0
	v_fmac_f32_e32 v57, v62, v57
	v_div_scale_f32 v62, vcc, 1.0, v54, 1.0
	v_mul_f32_e64 v63, v62, v57
	v_fma_f32 v64, -v55, v63, v62
	v_fmac_f32_e32 v63, v64, v57
	v_fma_f32 v55, -v55, v63, v62
	v_div_fmas_f32 v55, v55, v57, v63
	v_div_fixup_f32 v54, v55, v54, 1.0
	v_pk_mul_f32 v[62:63], v[68:69], v[54:55] op_sel_hi:[1,0]
	s_and_b64 vcc, exec, s[8:9]
	s_waitcnt lgkmcnt(0)
	v_pk_fma_f32 v[44:45], v[44:45], v[62:63], v[58:59]
	v_pk_mul_f32 v[58:59], v[72:73], v[54:55] op_sel_hi:[1,0]
	v_lshlrev_b32_e32 v57, 2, v2
	v_pk_fma_f32 v[46:47], v[46:47], v[58:59], v[60:61]
	s_cbranch_vccz .LBB0_781
	s_load_dwordx2 s[50:51], s[0:1], 0xa0
	s_lshl_b64 s[56:57], s[74:75], 2
	s_waitcnt lgkmcnt(0)
	s_add_u32 s50, s50, s56
	s_addc_u32 s51, s51, s57
	global_store_dwordx4 v57, v[44:47], s[50:51]

.LBB0_796:
	v_add_f32_e32 v54, 0, v44
	v_add_f32_e32 v54, v45, v54
	v_add_f32_e32 v54, v46, v54
	v_add_f32_e32 v54, v47, v54
	v_add_f32_e32 v54, v54, v40
	v_add_f32_e32 v54, v41, v54
	v_add_f32_e32 v54, v42, v54
	v_add_f32_e32 v54, v43, v54
	v_add_f32_e32 v54, v54, v36
	v_add_f32_e32 v54, v37, v54
	v_add_f32_e32 v54, v38, v54
	v_add_f32_e32 v54, v39, v54
	v_add_f32_e32 v54, v54, v32
	v_add_f32_e32 v54, v33, v54
	v_add_f32_e32 v54, v34, v54
	v_add_f32_e32 v54, v35, v54
	v_add_f32_e32 v54, v54, v28
	v_add_f32_e32 v54, v29, v54
	v_add_f32_e32 v54, v30, v54
	v_add_f32_e32 v54, v31, v54
	v_add_f32_e32 v54, v54, v24
	v_add_f32_e32 v54, v25, v54
	v_add_f32_e32 v54, v26, v54
	v_add_f32_e32 v54, v27, v54
	v_add_f32_e32 v54, v54, v20
	v_add_f32_e32 v54, v21, v54
	v_add_f32_e32 v54, v22, v54
	v_add_f32_e32 v54, v23, v54
	v_add_f32_e64 v54, v54, v48
	v_cvt_pk_bf16_f32 v58, v44, v45
	v_cvt_pk_bf16_f32 v59, v46, v47
	v_cvt_pk_bf16_f32 v60, v40, v41
	v_cvt_pk_bf16_f32 v61, v42, v43
	v_add_f32_e64 v54, v49, v54
	global_store_dwordx4 v[52:53], v[58:61], off
	v_add_f32_e32 v54, v50, v54
	v_add_f32_e32 v54, v51, v54
	v_cvt_pk_bf16_f32 v58, v36, v37
	v_cvt_pk_bf16_f32 v59, v38, v39
	v_cvt_pk_bf16_f32 v60, v32, v33
	v_cvt_pk_bf16_f32 v61, v34, v35
	global_store_dwordx4 v[52:53], v[58:61], off offset:16
	v_add_u32_e32 v56, 0xa200, v56
	s_nop 0
	v_cvt_pk_bf16_f32 v58, v28, v29
	v_cvt_pk_bf16_f32 v59, v30, v31
	v_cvt_pk_bf16_f32 v60, v24, v25
	v_cvt_pk_bf16_f32 v61, v26, v27
	global_store_dwordx4 v[52:53], v[58:61], off offset:32
	s_nop 1
	v_cvt_pk_bf16_f32 v58, v20, v21
	v_cvt_pk_bf16_f32 v59, v22, v23
	v_cvt_pk_bf16_f32 v60, v48, v49
	v_cvt_pk_bf16_f32 v61, v50, v51
	global_store_dwordx4 v[52:53], v[58:61], off offset:48
	v_add_f32_dpp v52, v54, v54 quad_perm:[1,0,3,2] row_mask:0xf bank_mask:0xf bound_ctrl:1
	s_nop 1
	v_add_f32_dpp v52, v52, v52 quad_perm:[2,3,0,1] row_mask:0xf bank_mask:0xf bound_ctrl:1
	s_nop 1
	v_add_f32_dpp v52, v52, v52 row_ror:4 row_mask:0xf bank_mask:0xf bound_ctrl:1
	s_nop 1
	v_add_f32_dpp v52, v52, v52 row_ror:8 row_mask:0xf bank_mask:0xf bound_ctrl:1
	s_nop 0
	v_readlane_b32 s6, v52, 16
	v_readlane_b32 s50, v52, 48
	v_readlane_b32 s8, v52, 0
	v_readlane_b32 s9, v52, 32
	v_mov_b32_e32 v52, s6
	v_mov_b32_e32 v53, s50
	v_pk_add_f32 v[52:53], s[8:9], v[52:53]
	s_nop 0
	v_add_f32_e32 v52, v52, v53
	v_fmac_f32_e32 v45, 0xba000000, v52
	v_fmamk_f32 v44, v52, 0xba000000, v44
	v_mul_f32_e32 v53, v45, v45
	v_fmac_f32_e32 v53, v44, v44
	v_fmamk_f32 v46, v52, 0xba000000, v46
	v_fmac_f32_e32 v53, v46, v46
	v_fmac_f32_e32 v47, 0xba000000, v52
	v_fmac_f32_e32 v53, v47, v47
	v_fmamk_f32 v57, v52, 0xba000000, v40
	v_fmac_f32_e32 v53, v57, v57
	v_fmac_f32_e32 v41, 0xba000000, v52
	v_fmac_f32_e32 v53, v41, v41
	v_fmamk_f32 v42, v52, 0xba000000, v42
	v_fmac_f32_e32 v53, v42, v42
	v_fmac_f32_e32 v43, 0xba000000, v52
	v_fmac_f32_e32 v53, v43, v43
	v_fmamk_f32 v36, v52, 0xba000000, v36
	v_fmac_f32_e32 v53, v36, v36
	v_fmac_f32_e32 v37, 0xba000000, v52
	v_fmac_f32_e32 v53, v37, v37
	v_fmamk_f32 v38, v52, 0xba000000, v38
	v_fmac_f32_e32 v53, v38, v38
	v_fmac_f32_e32 v39, 0xba000000, v52
	v_fmac_f32_e32 v53, v39, v39
	v_fmamk_f32 v32, v52, 0xba000000, v32
	v_fmac_f32_e32 v53, v32, v32
	v_fmac_f32_e32 v33, 0xba000000, v52
	v_fmac_f32_e32 v53, v33, v33
	v_fmamk_f32 v34, v52, 0xba000000, v34
	v_fmac_f32_e32 v53, v34, v34
	v_fmac_f32_e32 v35, 0xba000000, v52
	v_fmac_f32_e32 v53, v35, v35
	v_fmamk_f32 v66, v52, 0xba000000, v28
	v_fmac_f32_e32 v53, v66, v66
	v_fmac_f32_e32 v29, 0xba000000, v52
	v_fmac_f32_e32 v53, v29, v29
	v_fmamk_f32 v30, v52, 0xba000000, v30
	v_fmac_f32_e32 v53, v30, v30
	v_fmac_f32_e32 v31, 0xba000000, v52
	v_fmac_f32_e32 v53, v31, v31
	v_fmamk_f32 v28, v52, 0xba000000, v24
	v_fmac_f32_e32 v53, v28, v28
	v_fmac_f32_e32 v25, 0xba000000, v52
	v_fmac_f32_e32 v53, v25, v25
	v_fmamk_f32 v26, v52, 0xba000000, v26
	v_fmac_f32_e32 v53, v26, v26
	v_fmac_f32_e32 v27, 0xba000000, v52
	v_mul_f32_e32 v58, 0x3a000000, v52
	v_fmac_f32_e32 v53, v27, v27
	v_fmamk_f32 v24, v52, 0xba000000, v20
	v_fmac_f32_e32 v53, v24, v24
	v_fmac_f32_e32 v21, 0xba000000, v52
	v_pk_add_f32 v[54:55], v[22:23], v[58:59] op_sel_hi:[1,0] neg_lo:[0,1] neg_hi:[0,1]
	v_fmac_f32_e32 v53, v21, v21
	v_pk_mul_f32 v[22:23], v[54:55], v[54:55]
	s_nop 0
	v_add_f32_e32 v20, v22, v53
	v_pk_add_f32 v[52:53], v[48:49], v[58:59] op_sel_hi:[1,0] neg_lo:[0,1] neg_hi:[0,1]
	v_add_f32_e64 v20, v23, v20
	v_pk_mul_f32 v[22:23], v[52:53], v[52:53]
	v_pk_add_f32 v[48:49], v[50:51], v[58:59] op_sel_hi:[1,0] neg_lo:[0,1] neg_hi:[0,1]
	v_add_f32_e32 v20, v22, v20
	v_add_f32_e32 v20, v23, v20
	v_pk_mul_f32 v[22:23], v[48:49], v[48:49]
	ds_read_b128 v[58:61], v56 offset:24576
	ds_read_b128 v[62:65], v56 offset:49152
	v_add_f32_e64 v20, v22, v20
	v_add_f32_e32 v20, v23, v20
	s_nop 1
	v_add_f32_dpp v20, v20, v20 quad_perm:[1,0,3,2] row_mask:0xf bank_mask:0xf bound_ctrl:1
	s_nop 1
	v_add_f32_dpp v20, v20, v20 quad_perm:[2,3,0,1] row_mask:0xf bank_mask:0xf bound_ctrl:1
	s_nop 1
	v_add_f32_dpp v20, v20, v20 row_ror:4 row_mask:0xf bank_mask:0xf bound_ctrl:1
	s_nop 1
	v_add_f32_dpp v20, v20, v20 row_ror:8 row_mask:0xf bank_mask:0xf bound_ctrl:1
	s_nop 0
	v_readlane_b32 s6, v20, 16
	v_readlane_b32 s50, v20, 48
	v_readlane_b32 s8, v20, 0
	v_readlane_b32 s9, v20, 32
	v_mov_b32_e32 v22, s6
	v_mov_b32_e32 v23, s50
	v_pk_add_f32 v[22:23], s[8:9], v[22:23]
	s_nop 0
	v_add_f32_e32 v20, v22, v23
	v_fmamk_f32 v20, v20, 0x3a000000, v207
	v_cmp_gt_f32_e32 vcc, s10, v20
	v_mul_f32_e32 v22, 0x4f800000, v20
	s_nop 0
	v_cndmask_b32_e32 v20, v20, v22, vcc
	v_sqrt_f32_e32 v22, v20
	s_nop 0
	v_add_u32_e32 v23, -1, v22
	v_fma_f32 v40, -v23, v22, v20
	v_cmp_ge_f32_e64 s[50:51], 0, v40
	v_add_u32_e32 v40, 1, v22
	s_nop 0
	v_cndmask_b32_e64 v23, v22, v23, s[50:51]
	v_fma_f32 v22, -v40, v22, v20
	v_cmp_lt_f32_e64 s[50:51], 0, v22
	s_nop 1
	v_cndmask_b32_e64 v22, v23, v40, s[50:51]
	v_mul_f32_e32 v23, 0x37800000, v22
	v_cndmask_b32_e32 v22, v22, v23, vcc
	v_cmp_class_f32_e32 vcc, v20, v208
	s_nop 1
	v_cndmask_b32_e64 v20, v22, v20, vcc
	v_div_scale_f32 v22, s[8:9], v20, v20, 1.0
	v_rcp_f32_e32 v23, v22
	s_nop 0
	v_fma_f32 v40, -v22, v23, 1.0
	v_fmac_f32_e32 v23, v40, v23
	v_div_scale_f32 v40, vcc, 1.0, v20, 1.0
	v_mul_f32_e32 v50, v40, v23
	v_fma_f32 v51, -v22, v50, v40
	v_fmac_f32_e32 v50, v51, v23
	v_fma_f32 v22, -v22, v50, v40
	v_div_fmas_f32 v22, v22, v23, v50
	v_div_fixup_f32 v20, v22, v20, 1.0
	v_mul_f32_e32 v22, v44, v20
	s_waitcnt lgkmcnt(0)
	v_add_f32_e32 v23, 1.0, v62
	v_fma_f32 v22, v23, v22, v58
	v_mul_f32_e32 v23, v45, v20
	v_add_f32_e32 v40, 1.0, v63
	v_fma_f32 v23, v40, v23, v59
	v_mul_f32_e32 v40, v46, v20
	v_add_f32_e32 v44, 1.0, v64
	v_fma_f32 v44, v44, v40, v60
	v_mul_f32_e32 v40, v47, v20
	v_add_f32_e32 v45, 1.0, v65
	v_fmac_f32_e32 v61, v45, v40
	v_mov_b32_e32 v40, v3
	v_cvt_pk_fp8_f32 v40, v22, v23
	v_mul_f32_e32 v22, v57, v20
	v_mul_f32_e32 v24, v24, v20
	v_mul_f32_e64 v21, v21, v20
	v_cvt_pk_fp8_f32 v40, v44, v61 op_sel:[0,0,1]
	ds_read_b128 v[44:47], v56 offset:25600
	ds_read_b128 v[58:61], v56 offset:50176
	s_waitcnt lgkmcnt(0)
	v_add_f32_e32 v23, 1.0, v58
	v_fma_f32 v22, v22, v23, v44
	v_mul_f32_e32 v23, v41, v20
	v_add_f32_e32 v41, 1.0, v59
	v_fma_f32 v23, v41, v23, v45
	v_mul_f32_e32 v41, v42, v20
	v_add_f32_e32 v42, 1.0, v60
	v_fma_f32 v42, v42, v41, v46
	v_mul_f32_e32 v41, v43, v20
	v_add_f32_e32 v43, 1.0, v61
	v_fmac_f32_e32 v47, v43, v41
	v_mov_b32_e32 v41, v3
	v_cvt_pk_fp8_f32 v41, v22, v23
	v_mul_f32_e64 v22, v36, v20
	v_cvt_pk_fp8_f32 v41, v42, v47 op_sel:[0,0,1]
	ds_read_b128 v[42:45], v56 offset:26624
	ds_read_b128 v[58:61], v56 offset:51200
	s_waitcnt lgkmcnt(0)
	v_add_f32_e32 v23, 1.0, v58
	v_fma_f32 v22, v22, v23, v42
	v_mul_f32_e32 v23, v37, v20
	v_add_f32_e32 v36, 1.0, v59
	v_fma_f32 v23, v23, v36, v43
	v_mov_b32_e64 v42, v3
	v_cvt_pk_fp8_f32 v42, v22, v23
	v_mul_f32_e32 v36, v38, v20
	v_add_f32_e32 v37, 1.0, v60
	v_fma_f32 v36, v36, v37, v44
	v_mul_f32_e64 v37, v39, v20
	v_add_f32_e32 v38, 1.0, v61
	v_fmac_f32_e32 v45, v37, v38
	v_cvt_pk_fp8_f32 v42, v36, v45 op_sel:[0,0,1]
	ds_read_b128 v[36:39], v56 offset:27648
	ds_read_b128 v[44:47], v56 offset:52224
	v_mul_f32_e32 v22, v32, v20
	v_mov_b32_e32 v43, v3
	s_waitcnt lgkmcnt(0)
	v_add_f32_e32 v23, 1.0, v44
	v_fma_f32 v22, v22, v23, v36
	v_mul_f32_e32 v23, v33, v20
	v_add_f32_e32 v32, 1.0, v45
	v_fma_f32 v23, v23, v32, v37
	v_cvt_pk_fp8_f32 v43, v22, v23
	v_mul_f32_e32 v32, v34, v20
	v_add_f32_e32 v33, 1.0, v46
	v_fma_f32 v32, v32, v33, v38
	v_mul_f32_e64 v33, v35, v20
	v_add_f32_e32 v34, 1.0, v47
	v_fmac_f32_e32 v39, v33, v34
	v_cvt_pk_fp8_f32 v43, v32, v39 op_sel:[0,0,1]
	v_lshl_add_u64 v[22:23], v[136:137], 0, s[74:75]
	global_store_dwordx4 v[22:23], v[40:43], off
	ds_read_b128 v[32:35], v56 offset:28672
	ds_read_b128 v[36:39], v56 offset:53248
	v_mul_f32_e32 v22, v66, v20
	s_waitcnt lgkmcnt(0)
	v_add_f32_e64 v23, 1.0, v36
	v_fma_f32 v23, v22, v23, v32
	v_mul_f32_e32 v22, v29, v20
	v_add_f32_e32 v29, 1.0, v37
	v_fma_f32 v29, v22, v29, v33
	v_mul_f32_e32 v22, v30, v20
	v_add_f32_e32 v30, 1.0, v38
	v_fma_f32 v30, v22, v30, v34
	v_mul_f32_e32 v22, v31, v20
	v_add_f32_e32 v31, 1.0, v39
	v_fmac_f32_e32 v35, v22, v31
	v_mov_b32_e32 v22, v3
	v_cvt_pk_fp8_f32 v22, v23, v29
	v_mul_f32_e64 v23, v28, v20
	v_cvt_pk_fp8_f32 v22, v30, v35 op_sel:[0,0,1]
	ds_read_b128 v[30:33], v56 offset:29696
	ds_read_b128 v[34:37], v56 offset:54272
	s_waitcnt lgkmcnt(0)
	v_add_f32_e32 v28, 1.0, v34
	v_fma_f32 v28, v23, v28, v30
	v_mul_f32_e32 v23, v25, v20
	v_add_f32_e32 v25, 1.0, v35
	v_fma_f32 v25, v23, v25, v31
	v_mul_f32_e32 v23, v26, v20
	v_add_f32_e32 v26, 1.0, v36
	v_fma_f32 v26, v23, v26, v32
	v_mul_f32_e32 v23, v27, v20
	v_add_f32_e32 v27, 1.0, v37
	v_fmac_f32_e32 v33, v23, v27
	v_mov_b32_e32 v23, v3
	v_cvt_pk_fp8_f32 v23, v28, v25
	v_cvt_pk_fp8_f32 v23, v26, v33 op_sel:[0,0,1]
	ds_read_b128 v[26:29], v56 offset:30720
	ds_read_b128 v[30:33], v56 offset:55296
	s_waitcnt lgkmcnt(0)
	v_add_f32_e32 v25, 1.0, v30
	v_fma_f32 v25, v24, v25, v26
	v_add_f32_e64 v24, 1.0, v31
	v_fma_f32 v21, v21, v24, v27
	v_mul_f32_e32 v24, v54, v20
	v_add_f32_e32 v26, 1.0, v32
	v_fma_f32 v26, v24, v26, v28
	v_mul_f32_e32 v24, v55, v20
	v_add_f32_e32 v27, 1.0, v33
	v_fmac_f32_e32 v29, v24, v27
	v_mov_b32_e32 v24, v3
	v_cvt_pk_fp8_f32 v24, v25, v21
	v_mul_f32_e64 v21, v52, v20
	v_cvt_pk_fp8_f32 v24, v26, v29 op_sel:[0,0,1]
	ds_read_b128 v[26:29], v56 offset:31744
	ds_read_b128 v[30:33], v56 offset:56320
	s_waitcnt lgkmcnt(0)
	v_add_f32_e32 v25, 1.0, v30
	v_fma_f32 v21, v21, v25, v26
	v_mul_f32_e32 v25, v53, v20
	v_add_f32_e32 v26, 1.0, v31
	v_fma_f32 v26, v25, v26, v27
	v_mul_f32_e32 v25, v48, v20
	v_add_f32_e32 v27, 1.0, v32
	v_fma_f32 v27, v25, v27, v28
	v_mul_f32_e32 v20, v49, v20
	v_add_f32_e32 v25, 1.0, v33
	v_fmac_f32_e32 v29, v20, v25
	v_mov_b32_e32 v25, v3
	v_cvt_pk_fp8_f32 v25, v21, v26
	v_lshl_add_u64 v[20:21], v[130:131], 0, s[74:75]
	v_add_co_u32_e32 v20, vcc, 0x3d300000, v20
	v_cvt_pk_fp8_f32 v25, v27, v29 op_sel:[0,0,1]
	s_nop 0
	v_addc_co_u32_e32 v21, vcc, 0, v21, vcc
	global_store_dwordx4 v[20:21], v[22:25], off offset:16
	s_branch .LBB0_718
